# baseline (speedup 1.0000x reference)
.LBB3_7:
	v_add_u32_e32 v182, s33, v161
	v_add_u32_e32 v181, -1, v182
	v_or_b32_e32 v2, v181, v164
	v_add_u32_e32 v180, 0x18400, v171
	v_cmp_gt_u32_e64 s[0:1], 64, v2
	s_mov_b64 s[4:5], -1
	s_and_b64 vcc, exec, s[24:25]
	s_cbranch_vccz .LBB3_45
	s_load_dwordx2 s[4:5], s[22:23], 0x20
	s_waitcnt lgkmcnt(0)
	s_load_dwordx2 s[26:27], s[4:5], 0x0
	s_load_dword s34, s[4:5], 0x8
	v_cmp_lt_u32_e64 s[64:65], 0, v182
	v_cmp_gt_u32_e64 s[66:67], 63, v182
	v_cmp_lt_u32_e64 s[68:69], 0, v162
	v_cmp_gt_u32_e64 s[70:71], 60, v162
	buffer_load_dwordx4 v[186:189], v180, s[16:19], 0 offen sc1
	s_and_b64 s[72:73], s[68:69], s[64:65]
	s_and_b64 s[74:75], s[68:69], s[66:67]
	s_and_b64 s[76:77], s[70:71], s[64:65]
	s_and_b64 s[78:79], s[70:71], s[66:67]
	v_add_u32_e32 v249, 0xfffe7c00, v180
	v_add_u32_e32 v250, 0xfffe8000, v180
	s_mov_b64 exec, s[72:73]
	buffer_load_dwordx4 v[110:113], v249, s[16:19], 0 offen
	buffer_load_dwordx4 v[70:73], v249, s[16:19], 0 offen offset:512
	s_mov_b64 exec, -1
	s_mov_b64 exec, s[68:69]
	buffer_load_dwordx4 v[126:129], v250, s[16:19], 0 offen offset:512
	buffer_load_dwordx4 v[98:101], v250, s[16:19], 0 offen offset:1024
	s_mov_b64 exec, -1
	s_mov_b64 exec, s[74:75]
	buffer_load_dwordx4 v[134:137], v250, s[16:19], 0 offen offset:2048
	buffer_load_dwordx4 v[114:117], v250, s[16:19], 0 offen offset:2560
	s_mov_b64 exec, -1
	v_add_u32_e32 v249, 0xfffffc00, v180
	s_mov_b64 exec, s[64:65]
	buffer_load_dwordx4 v[82:85], v249, s[16:19], 0 offen
	buffer_load_dwordx4 v[42:45], v249, s[16:19], 0 offen offset:512
	s_mov_b64 exec, -1
	buffer_load_dwordx4 v[106:109], v180, s[16:19], 0 offen offset:512
	buffer_load_dwordx4 v[62:65], v180, s[16:19], 0 offen offset:1024
	s_mov_b64 exec, s[66:67]
	buffer_load_dwordx4 v[122:125], v180, s[16:19], 0 offen offset:2048
	buffer_load_dwordx4 v[86:89], v180, s[16:19], 0 offen offset:2560
	s_mov_b64 exec, -1
	v_add_u32_e32 v249, 0x17c00, v180
	v_add_u32_e32 v250, 0x18000, v180
	s_mov_b64 exec, s[64:65]
	buffer_load_dwordx4 v[50:53], v249, s[16:19], 0 offen
	buffer_load_dwordx4 v[22:25], v249, s[16:19], 0 offen offset:512
	s_mov_b64 exec, -1
	buffer_load_dwordx4 v[66:69], v250, s[16:19], 0 offen offset:512
	buffer_load_dwordx4 v[30:33], v250, s[16:19], 0 offen offset:1024
	s_mov_b64 exec, s[66:67]
	buffer_load_dwordx4 v[94:97], v250, s[16:19], 0 offen offset:2048
	buffer_load_dwordx4 v[46:49], v250, s[16:19], 0 offen offset:2560
	s_mov_b64 exec, -1
	v_add_u32_e32 v249, 0x18000, v180
	buffer_load_dwordx4 v[154:157], v249, s[16:19], 0 offen sc1
	v_add_u32_e32 v250, 0x30000, v180
	buffer_load_dwordx4 v[150:153], v250, s[16:19], 0 offen sc1
	v_add_u32_e32 v249, 0x48000, v180
	buffer_load_dwordx4 v[146:149], v249, s[16:19], 0 offen sc1
	v_add_u32_e32 v249, 0x2fc00, v180
	v_add_u32_e32 v250, 0x30000, v180
	v_add_u32_e32 v251, 0x47c00, v180
	v_add_u32_e32 v252, 0x48000, v180
	v_add_u32_e32 v253, 0x5fc00, v180
	v_add_u32_e32 v254, 0x60000, v180
	s_cmp_lg_u32 s93, 0
	s_cbranch_scc1 .Lmybg_B1
	s_waitcnt vmcnt(22)
	v_cvt_pk_f16_f32 v172, v230, v231
	v_cvt_pk_f16_f32 v173, v234, v235
	v_cvt_pk_f16_f32 v174, v232, v233
	v_cvt_pk_f16_f32 v175, v236, v237
	v_cvt_pk_f16_f32 v176, v238, v239
	v_cvt_pk_f16_f32 v177, v242, v243
	v_cvt_pk_f16_f32 v178, v240, v241
	v_cvt_pk_f16_f32 v179, v244, v245
	s_mov_b32 s93, 1

.LBB3_45:
	s_and_b64 vcc, exec, s[4:5]
	s_cbranch_vccz .LBB3_6
	s_load_dwordx2 s[0:1], s[22:23], 0x18
	s_waitcnt lgkmcnt(0)
	s_load_dwordx2 s[6:7], s[0:1], 0x0
	s_load_dword s28, s[0:1], 0x8
	v_cmp_lt_u32_e64 s[64:65], 0, v182
	v_cmp_gt_u32_e64 s[66:67], 63, v182
	v_cmp_lt_u32_e64 s[68:69], 0, v162
	v_cmp_gt_u32_e64 s[70:71], 60, v162
	buffer_load_dwordx4 v[184:187], v180, s[16:19], 0 offen sc1
	s_and_b64 s[72:73], s[68:69], s[64:65]
	s_and_b64 s[74:75], s[68:69], s[66:67]
	s_and_b64 s[76:77], s[70:71], s[64:65]
	s_and_b64 s[78:79], s[70:71], s[66:67]
	v_add_u32_e32 v249, 0xfffe7c00, v180
	v_add_u32_e32 v250, 0xfffe8000, v180
	s_mov_b64 exec, s[72:73]
	buffer_load_dwordx4 v[110:113], v249, s[16:19], 0 offen
	buffer_load_dwordx4 v[78:81], v249, s[16:19], 0 offen offset:512
	s_mov_b64 exec, -1
	s_mov_b64 exec, s[68:69]
	buffer_load_dwordx4 v[126:129], v250, s[16:19], 0 offen offset:512
	buffer_load_dwordx4 v[102:105], v250, s[16:19], 0 offen offset:1024
	s_mov_b64 exec, -1
	s_mov_b64 exec, s[74:75]
	buffer_load_dwordx4 v[138:141], v250, s[16:19], 0 offen offset:2048
	buffer_load_dwordx4 v[118:121], v250, s[16:19], 0 offen offset:2560
	s_mov_b64 exec, -1
	v_add_u32_e32 v249, 0xfffffc00, v180
	s_mov_b64 exec, s[64:65]
	buffer_load_dwordx4 v[86:89], v249, s[16:19], 0 offen
	buffer_load_dwordx4 v[46:49], v249, s[16:19], 0 offen offset:512
	s_mov_b64 exec, -1
	buffer_load_dwordx4 v[106:109], v180, s[16:19], 0 offen offset:512
	buffer_load_dwordx4 v[62:65], v180, s[16:19], 0 offen offset:1024
	s_mov_b64 exec, s[66:67]
	buffer_load_dwordx4 v[122:125], v180, s[16:19], 0 offen offset:2048
	buffer_load_dwordx4 v[82:85], v180, s[16:19], 0 offen offset:2560
	s_mov_b64 exec, -1
	v_add_u32_e32 v249, 0x17c00, v180
	v_add_u32_e32 v250, 0x18000, v180
	s_mov_b64 exec, s[64:65]
	buffer_load_dwordx4 v[50:53], v249, s[16:19], 0 offen
	buffer_load_dwordx4 v[22:25], v249, s[16:19], 0 offen offset:512
	s_mov_b64 exec, -1
	buffer_load_dwordx4 v[66:69], v250, s[16:19], 0 offen offset:512
	buffer_load_dwordx4 v[34:37], v250, s[16:19], 0 offen offset:1024
	s_mov_b64 exec, s[66:67]
	buffer_load_dwordx4 v[94:97], v250, s[16:19], 0 offen offset:2048
	buffer_load_dwordx4 v[42:45], v250, s[16:19], 0 offen offset:2560
	s_mov_b64 exec, -1
	v_add_u32_e32 v249, 0x18000, v180
	buffer_load_dwordx4 v[154:157], v249, s[16:19], 0 offen sc1
	v_add_u32_e32 v250, 0x30000, v180
	buffer_load_dwordx4 v[150:153], v250, s[16:19], 0 offen sc1
	v_add_u32_e32 v249, 0x48000, v180
	buffer_load_dwordx4 v[146:149], v249, s[16:19], 0 offen sc1
	v_add_u32_e32 v249, 0x2fc00, v180
	v_add_u32_e32 v250, 0x30000, v180
	v_add_u32_e32 v251, 0x47c00, v180
	v_add_u32_e32 v252, 0x48000, v180
	v_add_u32_e32 v253, 0x5fc00, v180
	v_add_u32_e32 v254, 0x60000, v180
	s_cmp_lg_u32 s93, 0
	s_cbranch_scc1 .Lmybg_B2
	s_waitcnt vmcnt(22)
	v_cvt_pk_f16_f32 v172, v230, v231
	v_cvt_pk_f16_f32 v173, v234, v235
	v_cvt_pk_f16_f32 v174, v232, v233
	v_cvt_pk_f16_f32 v175, v236, v237
	v_cvt_pk_f16_f32 v176, v238, v239
	v_cvt_pk_f16_f32 v177, v242, v243
	v_cvt_pk_f16_f32 v178, v240, v241
	v_cvt_pk_f16_f32 v179, v244, v245
	s_mov_b32 s93, 1

.LBB4_4:
	global_load_dwordx4 v[2:5], v[170:171], off
	global_load_dwordx4 v[8:11], v[172:173], off
	global_load_dwordx4 v[210:213], v[170:171], off offset:16
	global_load_dwordx4 v[214:217], v[172:173], off offset:16
	s_lshl_b32 s48, s46, 3
	s_add_i32 s48, s48, s44
	v_or_b32_e32 v199, s48, v178
	v_add_u32_e32 v168, v199, v181
	v_add_u32_e32 v201, -1, v199
	v_mul_lo_u32 v6, v168, s47
	v_or_b32_e32 v7, v201, v182
	v_or_b32_e32 v6, v6, v166
	s_mov_b64 s[4:5], -1
	s_and_b64 vcc, exec, s[26:27]
	v_cmp_gt_u32_e64 s[2:3], 64, v7
	v_lshlrev_b32_e32 v200, 1, v6
	s_cbranch_vccz .LBB4_42
	global_load_dwordx3 v[154:156], v169, s[10:11]
	v_cmp_lt_u32_e64 s[64:65], 0, v199
	v_cmp_gt_u32_e64 s[66:67], 63, v199
	v_cmp_lt_u32_e64 s[68:69], 0, v180
	v_cmp_gt_u32_e64 s[70:71], 60, v180
	buffer_load_dwordx4 v[206:209], v200, s[36:39], 0 offen sc1
	s_and_b64 s[72:73], s[68:69], s[64:65]
	s_and_b64 s[74:75], s[68:69], s[66:67]
	s_and_b64 s[76:77], s[70:71], s[64:65]
	s_and_b64 s[78:79], s[70:71], s[66:67]
	v_add_u32_e32 v245, 0xfffe7c00, v200
	v_add_u32_e32 v246, 0xfffe8000, v200
	s_mov_b64 exec, s[72:73]
	buffer_load_dwordx4 v[122:125], v245, s[36:39], 0 offen
	buffer_load_dwordx4 v[82:85], v245, s[36:39], 0 offen offset:512
	s_mov_b64 exec, -1
	s_mov_b64 exec, s[68:69]
	buffer_load_dwordx4 v[138:141], v246, s[36:39], 0 offen offset:512
	buffer_load_dwordx4 v[106:109], v246, s[36:39], 0 offen offset:1024
	s_mov_b64 exec, -1
	s_mov_b64 exec, s[74:75]
	buffer_load_dwordx4 v[146:149], v246, s[36:39], 0 offen offset:2048
	buffer_load_dwordx4 v[126:129], v246, s[36:39], 0 offen offset:2560
	s_mov_b64 exec, -1
	v_add_u32_e32 v245, 0xfffffc00, v200
	s_mov_b64 exec, s[64:65]
	buffer_load_dwordx4 v[94:97], v245, s[36:39], 0 offen
	buffer_load_dwordx4 v[54:57], v245, s[36:39], 0 offen offset:512
	s_mov_b64 exec, -1
	buffer_load_dwordx4 v[118:121], v200, s[36:39], 0 offen offset:512
	buffer_load_dwordx4 v[74:77], v200, s[36:39], 0 offen offset:1024
	s_mov_b64 exec, s[66:67]
	buffer_load_dwordx4 v[134:137], v200, s[36:39], 0 offen offset:2048
	buffer_load_dwordx4 v[98:101], v200, s[36:39], 0 offen offset:2560
	s_mov_b64 exec, -1
	v_add_u32_e32 v245, 0x17c00, v200
	v_add_u32_e32 v246, 0x18000, v200
	s_mov_b64 exec, s[64:65]
	buffer_load_dwordx4 v[62:65], v245, s[36:39], 0 offen
	buffer_load_dwordx4 v[30:33], v245, s[36:39], 0 offen offset:512
	s_mov_b64 exec, -1
	buffer_load_dwordx4 v[78:81], v246, s[36:39], 0 offen offset:512
	buffer_load_dwordx4 v[42:45], v246, s[36:39], 0 offen offset:1024
	s_mov_b64 exec, s[66:67]
	buffer_load_dwordx4 v[102:105], v246, s[36:39], 0 offen offset:2048
	buffer_load_dwordx4 v[58:61], v246, s[36:39], 0 offen offset:2560
	s_mov_b64 exec, -1
	v_add_u32_e32 v245, 0x18000, v200
	buffer_load_dwordx4 v[162:165], v245, s[36:39], 0 offen sc1
	v_add_u32_e32 v246, 0x30000, v200
	buffer_load_dwordx4 v[158:161], v246, s[36:39], 0 offen sc1
	v_add_u32_e32 v245, 0x2fc00, v200
	v_add_u32_e32 v246, 0x30000, v200
	v_add_u32_e32 v247, 0x47c00, v200
	v_add_u32_e32 v248, 0x48000, v200
	v_add_u32_e32 v249, 0x5fc00, v200
	v_add_u32_e32 v250, 0x60000, v200
	s_waitcnt vmcnt(22)
	v_cvt_pk_f16_f32 v6, v2, v3
	v_cvt_pk_f16_f32 v2, v8, v9
	v_cvt_pk_f16_f32 v7, v4, v5
	v_cvt_pk_f16_f32 v3, v10, v11
	v_cvt_pk_f16_f32 v8, v210, v211
	v_cvt_pk_f16_f32 v4, v214, v215
	v_cvt_pk_f16_f32 v9, v212, v213
	v_cvt_pk_f16_f32 v5, v216, v217
	s_not_b64 exec, s[72:73]
	s_cbranch_execz .Lmyf_C1_0
	v_mov_b32_e32 v122, v6
	v_mov_b32_e32 v123, v7
	v_mov_b32_e32 v124, v8
	v_mov_b32_e32 v125, v9
	v_mov_b32_e32 v82, v2
	v_mov_b32_e32 v83, v3
	v_mov_b32_e32 v84, v4
	v_mov_b32_e32 v85, v5

.Lmyf_C1_7:
	s_mov_b64 exec, -1
	s_waitcnt vmcnt(21)
	v_cvt_f16_f32_e32 v202, v155
	v_cvt_f16_f32_e32 v204, v154
	v_cvt_f16_f32_e32 v203, v156
	v_add_u32_e32 v251, 0x48000, v200
	buffer_load_dwordx4 v[154:157], v251, s[36:39], 0 offen sc1
	s_mov_b64 s[4:5], 0
	s_waitcnt vmcnt(3)
	v_pk_mul_f16 v212, v204, v209 op_sel_hi:[0,1]
	v_pk_mul_f16 v216, v202, v209 op_sel_hi:[0,1]
	v_pk_mul_f16 v220, v203, v209 op_sel_hi:[0,1]
	v_pk_mul_f16 v205, v204, v206 op_sel_hi:[0,1]
	v_pk_mul_f16 v210, v204, v207 op_sel_hi:[0,1]
	v_pk_mul_f16 v211, v204, v208 op_sel_hi:[0,1]
	v_pk_mul_f16 v213, v202, v206 op_sel_hi:[0,1]
	s_mov_b64 exec, s[64:65]
	buffer_load_dwordx4 v[34:37], v245, s[36:39], 0 offen
	buffer_load_dwordx4 v[18:21], v245, s[36:39], 0 offen offset:512
	s_mov_b64 exec, -1
	v_pk_mul_f16 v214, v202, v207 op_sel_hi:[0,1]
	v_pk_mul_f16 v215, v202, v208 op_sel_hi:[0,1]
	v_pk_mul_f16 v217, v203, v206 op_sel_hi:[0,1]
	v_pk_mul_f16 v218, v203, v207 op_sel_hi:[0,1]
	v_pk_mul_f16 v219, v203, v208 op_sel_hi:[0,1]
	v_pk_fma_f16 v125, v125, v209, v212
	v_pk_fma_f16 v141, v141, v209, v216
	v_pk_fma_f16 v149, v149, v209, v220
	v_pk_fma_f16 v221, v97, v209, v212
	v_pk_fma_f16 v225, v121, v209, v216
	v_pk_fma_f16 v229, v137, v209, v220
	v_pk_fma_f16 v212, v65, v209, v212
	v_pk_fma_f16 v216, v81, v209, v216
	buffer_load_dwordx4 v[46:49], v246, s[36:39], 0 offen offset:512
	buffer_load_dwordx4 v[22:25], v246, s[36:39], 0 offen offset:1024
	v_pk_fma_f16 v209, v105, v209, v220
	v_pk_maximum3_f16 v220, v125, v141, v149
	v_pk_fma_f16 v124, v124, v208, v211
	v_pk_fma_f16 v123, v123, v207, v210
	v_pk_fma_f16 v122, v122, v206, v205
	v_pk_fma_f16 v140, v140, v208, v215
	v_pk_fma_f16 v139, v139, v207, v214
	v_pk_fma_f16 v138, v138, v206, v213
	v_pk_fma_f16 v148, v148, v208, v219
	v_pk_fma_f16 v147, v147, v207, v218
	v_pk_fma_f16 v146, v146, v206, v217
	v_pk_fma_f16 v222, v96, v208, v211
	v_pk_fma_f16 v223, v95, v207, v210
	v_pk_fma_f16 v224, v94, v206, v205
	v_pk_fma_f16 v226, v120, v208, v215
	v_pk_fma_f16 v227, v119, v207, v214
	s_mov_b64 exec, s[66:67]
	buffer_load_dwordx4 v[66:69], v246, s[36:39], 0 offen offset:2048
	buffer_load_dwordx4 v[26:29], v246, s[36:39], 0 offen offset:2560
	s_mov_b64 exec, -1
	v_pk_fma_f16 v228, v118, v206, v213
	v_pk_fma_f16 v230, v136, v208, v219
	v_pk_fma_f16 v231, v135, v207, v218
	v_pk_fma_f16 v232, v134, v206, v217
	v_pk_fma_f16 v211, v64, v208, v211
	v_pk_fma_f16 v210, v63, v207, v210
	v_pk_fma_f16 v205, v62, v206, v205
	v_pk_fma_f16 v215, v80, v208, v215
	v_pk_fma_f16 v214, v79, v207, v214
	v_pk_fma_f16 v213, v78, v206, v213
	v_pk_fma_f16 v208, v104, v208, v219
	v_pk_fma_f16 v207, v103, v207, v218
	v_pk_fma_f16 v206, v102, v206, v217
	v_pk_maximum3_f16 v217, v122, v138, v146
	v_pk_maximum3_f16 v218, v123, v139, v147
	v_pk_maximum3_f16 v219, v124, v140, v148
	v_pk_maximum3_f16 v236, v221, v225, v229
	v_pk_maximum3_f16 v240, v212, v216, v209
	v_pk_maximum3_f16 v233, v224, v228, v232
	v_pk_maximum3_f16 v234, v223, v227, v231
	v_pk_maximum3_f16 v235, v222, v226, v230
	v_pk_maximum3_f16 v237, v205, v213, v206
	v_pk_maximum3_f16 v238, v210, v214, v207
	v_pk_maximum3_f16 v220, v220, v236, v240
	v_pk_maximum3_f16 v239, v211, v215, v208
	v_pk_maximum3_f16 v217, v217, v233, v237
	v_pk_maximum3_f16 v218, v218, v234, v238
	v_pk_maximum3_f16 v219, v219, v235, v239
	v_pk_add_f16 v125, v125, v220 neg_lo:[0,1] neg_hi:[0,1]
	s_mov_b64 exec, s[64:65]
	buffer_load_dwordx4 v[86:89], v247, s[36:39], 0 offen
	buffer_load_dwordx4 v[38:41], v247, s[36:39], 0 offen offset:512
	s_mov_b64 exec, -1
	v_pk_add_f16 v122, v122, v217 neg_lo:[0,1] neg_hi:[0,1]
	v_pk_add_f16 v123, v123, v218 neg_lo:[0,1] neg_hi:[0,1]
	v_pk_add_f16 v124, v124, v219 neg_lo:[0,1] neg_hi:[0,1]
	v_pk_add_f16 v138, v138, v217 neg_lo:[0,1] neg_hi:[0,1]
	v_exp_f16_sdwa v233, v122 dst_sel:WORD_0 dst_unused:UNUSED_PAD src0_sel:WORD_0
	v_exp_f16_sdwa v234, v123 dst_sel:WORD_0 dst_unused:UNUSED_PAD src0_sel:WORD_0
	v_exp_f16_sdwa v235, v124 dst_sel:WORD_0 dst_unused:UNUSED_PAD src0_sel:WORD_0
	v_exp_f16_sdwa v236, v125 dst_sel:WORD_0 dst_unused:UNUSED_PAD src0_sel:WORD_0
	v_exp_f16_sdwa v233, v122 dst_sel:WORD_1 dst_unused:UNUSED_PRESERVE src0_sel:WORD_1
	v_exp_f16_sdwa v234, v123 dst_sel:WORD_1 dst_unused:UNUSED_PRESERVE src0_sel:WORD_1
	v_exp_f16_sdwa v235, v124 dst_sel:WORD_1 dst_unused:UNUSED_PRESERVE src0_sel:WORD_1
	v_exp_f16_sdwa v236, v125 dst_sel:WORD_1 dst_unused:UNUSED_PRESERVE src0_sel:WORD_1
	v_pk_add_f16 v139, v139, v218 neg_lo:[0,1] neg_hi:[0,1]
	v_pk_add_f16 v125, v233, 0
	v_pk_fma_f16 v85, v85, v236, 0
	v_pk_add_f16 v122, v236, 0
	v_pk_add_f16 v123, v235, 0
	v_pk_add_f16 v124, v234, 0
	v_pk_fma_f16 v84, v84, v235, 0
	v_pk_fma_f16 v83, v83, v234, 0
	v_pk_fma_f16 v82, v82, v233, 0
	v_pk_add_f16 v140, v140, v219 neg_lo:[0,1] neg_hi:[0,1]
	buffer_load_dwordx4 v[114:117], v248, s[36:39], 0 offen offset:512
	buffer_load_dwordx4 v[50:53], v248, s[36:39], 0 offen offset:1024
	v_pk_add_f16 v141, v141, v220 neg_lo:[0,1] neg_hi:[0,1]
	v_exp_f16_sdwa v233, v138 dst_sel:WORD_0 dst_unused:UNUSED_PAD src0_sel:WORD_0
	v_exp_f16_sdwa v234, v139 dst_sel:WORD_0 dst_unused:UNUSED_PAD src0_sel:WORD_0
	v_exp_f16_sdwa v235, v140 dst_sel:WORD_0 dst_unused:UNUSED_PAD src0_sel:WORD_0
	v_exp_f16_sdwa v236, v141 dst_sel:WORD_0 dst_unused:UNUSED_PAD src0_sel:WORD_0
	v_exp_f16_sdwa v233, v138 dst_sel:WORD_1 dst_unused:UNUSED_PRESERVE src0_sel:WORD_1
	v_exp_f16_sdwa v234, v139 dst_sel:WORD_1 dst_unused:UNUSED_PRESERVE src0_sel:WORD_1
	v_exp_f16_sdwa v235, v140 dst_sel:WORD_1 dst_unused:UNUSED_PRESERVE src0_sel:WORD_1
	v_exp_f16_sdwa v236, v141 dst_sel:WORD_1 dst_unused:UNUSED_PRESERVE src0_sel:WORD_1
	v_pk_add_f16 v125, v125, v233
	v_pk_fma_f16 v85, v109, v236, v85
	v_pk_add_f16 v109, v149, v220 neg_lo:[0,1] neg_hi:[0,1]
	v_pk_add_f16 v124, v124, v234
	v_pk_add_f16 v123, v123, v235
	v_pk_add_f16 v122, v122, v236
	v_pk_fma_f16 v82, v106, v233, v82
	v_pk_fma_f16 v83, v107, v234, v83
	v_pk_fma_f16 v84, v108, v235, v84
	v_pk_add_f16 v106, v146, v217 neg_lo:[0,1] neg_hi:[0,1]
	v_pk_add_f16 v107, v147, v218 neg_lo:[0,1] neg_hi:[0,1]
	v_pk_add_f16 v108, v148, v219 neg_lo:[0,1] neg_hi:[0,1]
	v_exp_f16_sdwa v138, v106 dst_sel:WORD_0 dst_unused:UNUSED_PAD src0_sel:WORD_0
	v_exp_f16_sdwa v139, v107 dst_sel:WORD_0 dst_unused:UNUSED_PAD src0_sel:WORD_0
	v_exp_f16_sdwa v140, v108 dst_sel:WORD_0 dst_unused:UNUSED_PAD src0_sel:WORD_0
	v_exp_f16_sdwa v141, v109 dst_sel:WORD_0 dst_unused:UNUSED_PAD src0_sel:WORD_0
	v_exp_f16_sdwa v138, v106 dst_sel:WORD_1 dst_unused:UNUSED_PRESERVE src0_sel:WORD_1
	v_exp_f16_sdwa v139, v107 dst_sel:WORD_1 dst_unused:UNUSED_PRESERVE src0_sel:WORD_1
	v_exp_f16_sdwa v140, v108 dst_sel:WORD_1 dst_unused:UNUSED_PRESERVE src0_sel:WORD_1
	v_exp_f16_sdwa v141, v109 dst_sel:WORD_1 dst_unused:UNUSED_PRESERVE src0_sel:WORD_1
	v_pk_add_f16 v109, v125, v138
	v_pk_add_f16 v106, v122, v141
	s_mov_b64 exec, s[66:67]
	buffer_load_dwordx4 v[130:133], v248, s[36:39], 0 offen offset:2048
	buffer_load_dwordx4 v[70:73], v248, s[36:39], 0 offen offset:2560
	s_mov_b64 exec, -1
	v_pk_add_f16 v107, v123, v140
	v_pk_add_f16 v108, v124, v139
	v_pk_fma_f16 v85, v129, v141, v85
	v_pk_fma_f16 v84, v128, v140, v84
	v_pk_fma_f16 v83, v127, v139, v83
	v_pk_fma_f16 v82, v126, v138, v82
	v_pk_add_f16 v122, v224, v217 neg_lo:[0,1] neg_hi:[0,1]
	v_pk_add_f16 v123, v223, v218 neg_lo:[0,1] neg_hi:[0,1]
	v_pk_add_f16 v124, v222, v219 neg_lo:[0,1] neg_hi:[0,1]
	v_pk_add_f16 v125, v221, v220 neg_lo:[0,1] neg_hi:[0,1]
	v_exp_f16_sdwa v126, v122 dst_sel:WORD_0 dst_unused:UNUSED_PAD src0_sel:WORD_0
	v_exp_f16_sdwa v127, v123 dst_sel:WORD_0 dst_unused:UNUSED_PAD src0_sel:WORD_0
	v_exp_f16_sdwa v128, v124 dst_sel:WORD_0 dst_unused:UNUSED_PAD src0_sel:WORD_0
	v_exp_f16_sdwa v129, v125 dst_sel:WORD_0 dst_unused:UNUSED_PAD src0_sel:WORD_0
	v_exp_f16_sdwa v126, v122 dst_sel:WORD_1 dst_unused:UNUSED_PRESERVE src0_sel:WORD_1
	v_exp_f16_sdwa v127, v123 dst_sel:WORD_1 dst_unused:UNUSED_PRESERVE src0_sel:WORD_1
	v_exp_f16_sdwa v128, v124 dst_sel:WORD_1 dst_unused:UNUSED_PRESERVE src0_sel:WORD_1
	v_exp_f16_sdwa v129, v125 dst_sel:WORD_1 dst_unused:UNUSED_PRESERVE src0_sel:WORD_1
	v_pk_add_f16 v122, v228, v217 neg_lo:[0,1] neg_hi:[0,1]
	v_pk_add_f16 v109, v109, v126
	v_pk_add_f16 v108, v108, v127
	v_pk_add_f16 v107, v107, v128
	s_mov_b64 exec, s[76:77]
	buffer_load_dwordx4 v[142:145], v249, s[36:39], 0 offen
	buffer_load_dwordx4 v[90:93], v249, s[36:39], 0 offen offset:512
	s_mov_b64 exec, -1
	v_pk_add_f16 v106, v106, v129
	v_pk_fma_f16 v82, v54, v126, v82
	v_pk_fma_f16 v83, v55, v127, v83
	v_pk_fma_f16 v84, v56, v128, v84
	v_pk_fma_f16 v85, v57, v129, v85
	v_pk_add_f16 v123, v227, v218 neg_lo:[0,1] neg_hi:[0,1]
	v_pk_add_f16 v124, v226, v219 neg_lo:[0,1] neg_hi:[0,1]
	v_pk_add_f16 v125, v225, v220 neg_lo:[0,1] neg_hi:[0,1]
	v_exp_f16_sdwa v126, v122 dst_sel:WORD_0 dst_unused:UNUSED_PAD src0_sel:WORD_0
	v_exp_f16_sdwa v127, v123 dst_sel:WORD_0 dst_unused:UNUSED_PAD src0_sel:WORD_0
	v_exp_f16_sdwa v128, v124 dst_sel:WORD_0 dst_unused:UNUSED_PAD src0_sel:WORD_0
	v_exp_f16_sdwa v129, v125 dst_sel:WORD_0 dst_unused:UNUSED_PAD src0_sel:WORD_0
	v_exp_f16_sdwa v126, v122 dst_sel:WORD_1 dst_unused:UNUSED_PRESERVE src0_sel:WORD_1
	v_exp_f16_sdwa v127, v123 dst_sel:WORD_1 dst_unused:UNUSED_PRESERVE src0_sel:WORD_1
	v_exp_f16_sdwa v128, v124 dst_sel:WORD_1 dst_unused:UNUSED_PRESERVE src0_sel:WORD_1
	v_exp_f16_sdwa v129, v125 dst_sel:WORD_1 dst_unused:UNUSED_PRESERVE src0_sel:WORD_1
	v_pk_add_f16 v122, v232, v217 neg_lo:[0,1] neg_hi:[0,1]
	v_pk_add_f16 v109, v109, v126
	v_pk_add_f16 v106, v106, v129
	v_pk_add_f16 v107, v107, v128
	v_pk_add_f16 v108, v108, v127
	v_pk_fma_f16 v85, v77, v129, v85
	v_pk_fma_f16 v84, v76, v128, v84
	s_mov_b64 exec, s[70:71]
	buffer_load_dwordx4 v[150:153], v250, s[36:39], 0 offen offset:512
	buffer_load_dwordx4 v[110:113], v250, s[36:39], 0 offen offset:1024
	s_mov_b64 exec, -1
	v_pk_fma_f16 v83, v75, v127, v83
	v_pk_fma_f16 v82, v74, v126, v82
	v_pk_add_f16 v123, v231, v218 neg_lo:[0,1] neg_hi:[0,1]
	v_pk_add_f16 v124, v230, v219 neg_lo:[0,1] neg_hi:[0,1]
	v_pk_add_f16 v125, v229, v220 neg_lo:[0,1] neg_hi:[0,1]
	v_exp_f16_sdwa v126, v122 dst_sel:WORD_0 dst_unused:UNUSED_PAD src0_sel:WORD_0
	v_exp_f16_sdwa v127, v123 dst_sel:WORD_0 dst_unused:UNUSED_PAD src0_sel:WORD_0
	v_exp_f16_sdwa v128, v124 dst_sel:WORD_0 dst_unused:UNUSED_PAD src0_sel:WORD_0
	v_exp_f16_sdwa v129, v125 dst_sel:WORD_0 dst_unused:UNUSED_PAD src0_sel:WORD_0
	v_exp_f16_sdwa v126, v122 dst_sel:WORD_1 dst_unused:UNUSED_PRESERVE src0_sel:WORD_1
	v_exp_f16_sdwa v127, v123 dst_sel:WORD_1 dst_unused:UNUSED_PRESERVE src0_sel:WORD_1
	v_exp_f16_sdwa v128, v124 dst_sel:WORD_1 dst_unused:UNUSED_PRESERVE src0_sel:WORD_1
	v_exp_f16_sdwa v129, v125 dst_sel:WORD_1 dst_unused:UNUSED_PRESERVE src0_sel:WORD_1
	v_pk_add_f16 v122, v205, v217 neg_lo:[0,1] neg_hi:[0,1]
	v_pk_add_f16 v109, v109, v126
	v_pk_add_f16 v108, v108, v127
	v_pk_add_f16 v107, v107, v128
	v_pk_add_f16 v106, v106, v129
	v_pk_fma_f16 v82, v98, v126, v82
	v_pk_fma_f16 v83, v99, v127, v83
	v_pk_fma_f16 v84, v100, v128, v84
	v_pk_fma_f16 v85, v101, v129, v85
	s_mov_b64 exec, s[78:79]
	buffer_load_dwordx4 v[14:17], v250, s[36:39], 0 offen offset:2048
	buffer_load_dwordx4 v[10:13], v250, s[36:39], 0 offen offset:2560
	s_mov_b64 exec, -1
	v_pk_add_f16 v123, v210, v218 neg_lo:[0,1] neg_hi:[0,1]
	v_pk_add_f16 v124, v211, v219 neg_lo:[0,1] neg_hi:[0,1]
	v_pk_add_f16 v125, v212, v220 neg_lo:[0,1] neg_hi:[0,1]
	v_exp_f16_sdwa v126, v122 dst_sel:WORD_0 dst_unused:UNUSED_PAD src0_sel:WORD_0
	v_exp_f16_sdwa v127, v123 dst_sel:WORD_0 dst_unused:UNUSED_PAD src0_sel:WORD_0
	v_exp_f16_sdwa v128, v124 dst_sel:WORD_0 dst_unused:UNUSED_PAD src0_sel:WORD_0
	v_exp_f16_sdwa v129, v125 dst_sel:WORD_0 dst_unused:UNUSED_PAD src0_sel:WORD_0
	v_exp_f16_sdwa v126, v122 dst_sel:WORD_1 dst_unused:UNUSED_PRESERVE src0_sel:WORD_1
	v_exp_f16_sdwa v127, v123 dst_sel:WORD_1 dst_unused:UNUSED_PRESERVE src0_sel:WORD_1
	v_exp_f16_sdwa v128, v124 dst_sel:WORD_1 dst_unused:UNUSED_PRESERVE src0_sel:WORD_1
	v_exp_f16_sdwa v129, v125 dst_sel:WORD_1 dst_unused:UNUSED_PRESERVE src0_sel:WORD_1
	v_pk_add_f16 v122, v213, v217 neg_lo:[0,1] neg_hi:[0,1]
	v_pk_add_f16 v109, v109, v126
	v_pk_add_f16 v106, v106, v129
	v_pk_add_f16 v107, v107, v128
	v_pk_add_f16 v108, v108, v127
	v_pk_fma_f16 v85, v33, v129, v85
	v_pk_fma_f16 v84, v32, v128, v84
	v_pk_fma_f16 v83, v31, v127, v83
	v_pk_fma_f16 v82, v30, v126, v82
	v_pk_add_f16 v123, v214, v218 neg_lo:[0,1] neg_hi:[0,1]
	v_pk_add_f16 v124, v215, v219 neg_lo:[0,1] neg_hi:[0,1]
	v_pk_add_f16 v125, v216, v220 neg_lo:[0,1] neg_hi:[0,1]
	v_exp_f16_sdwa v126, v122 dst_sel:WORD_0 dst_unused:UNUSED_PAD src0_sel:WORD_0
	v_exp_f16_sdwa v127, v123 dst_sel:WORD_0 dst_unused:UNUSED_PAD src0_sel:WORD_0
	v_exp_f16_sdwa v128, v124 dst_sel:WORD_0 dst_unused:UNUSED_PAD src0_sel:WORD_0
	v_exp_f16_sdwa v129, v125 dst_sel:WORD_0 dst_unused:UNUSED_PAD src0_sel:WORD_0
	v_exp_f16_sdwa v126, v122 dst_sel:WORD_1 dst_unused:UNUSED_PRESERVE src0_sel:WORD_1
	v_exp_f16_sdwa v127, v123 dst_sel:WORD_1 dst_unused:UNUSED_PRESERVE src0_sel:WORD_1
	v_exp_f16_sdwa v128, v124 dst_sel:WORD_1 dst_unused:UNUSED_PRESERVE src0_sel:WORD_1
	v_exp_f16_sdwa v129, v125 dst_sel:WORD_1 dst_unused:UNUSED_PRESERVE src0_sel:WORD_1
	v_pk_add_f16 v122, v206, v217 neg_lo:[0,1] neg_hi:[0,1]
	v_pk_add_f16 v109, v109, v126
	v_pk_add_f16 v108, v108, v127
	v_pk_add_f16 v107, v107, v128
	v_pk_add_f16 v106, v106, v129
	v_pk_fma_f16 v82, v42, v126, v82
	v_pk_fma_f16 v83, v43, v127, v83
	v_pk_fma_f16 v84, v44, v128, v84
	v_pk_fma_f16 v85, v45, v129, v85
	v_pk_add_f16 v123, v207, v218 neg_lo:[0,1] neg_hi:[0,1]
	v_pk_add_f16 v124, v208, v219 neg_lo:[0,1] neg_hi:[0,1]
	v_pk_add_f16 v125, v209, v220 neg_lo:[0,1] neg_hi:[0,1]
	v_exp_f16_sdwa v126, v122 dst_sel:WORD_0 dst_unused:UNUSED_PAD src0_sel:WORD_0
	v_exp_f16_sdwa v127, v123 dst_sel:WORD_0 dst_unused:UNUSED_PAD src0_sel:WORD_0
	v_exp_f16_sdwa v128, v124 dst_sel:WORD_0 dst_unused:UNUSED_PAD src0_sel:WORD_0
	v_exp_f16_sdwa v129, v125 dst_sel:WORD_0 dst_unused:UNUSED_PAD src0_sel:WORD_0
	v_exp_f16_sdwa v126, v122 dst_sel:WORD_1 dst_unused:UNUSED_PRESERVE src0_sel:WORD_1
	v_exp_f16_sdwa v127, v123 dst_sel:WORD_1 dst_unused:UNUSED_PRESERVE src0_sel:WORD_1
	v_exp_f16_sdwa v128, v124 dst_sel:WORD_1 dst_unused:UNUSED_PRESERVE src0_sel:WORD_1
	v_exp_f16_sdwa v129, v125 dst_sel:WORD_1 dst_unused:UNUSED_PRESERVE src0_sel:WORD_1
	v_pk_add_f16 v109, v109, v126
	v_pk_add_f16 v108, v108, v127
	v_rcp_f16_e32 v122, v109
	v_rcp_f16_sdwa v109, v109 dst_sel:DWORD dst_unused:UNUSED_PAD src0_sel:WORD_1
	v_pk_add_f16 v107, v107, v128
	v_rcp_f16_e32 v123, v108
	v_rcp_f16_sdwa v108, v108 dst_sel:DWORD dst_unused:UNUSED_PAD src0_sel:WORD_1
	v_pk_add_f16 v106, v106, v129
	v_rcp_f16_e32 v124, v107
	v_rcp_f16_sdwa v107, v107 dst_sel:DWORD dst_unused:UNUSED_PAD src0_sel:WORD_1
	v_rcp_f16_e32 v125, v106
	v_rcp_f16_sdwa v106, v106 dst_sel:DWORD dst_unused:UNUSED_PAD src0_sel:WORD_1
	v_pk_fma_f16 v82, v58, v126, v82
	v_pack_b32_f16 v109, v122, v109
	v_pk_fma_f16 v83, v59, v127, v83
	v_pk_mul_f16 v138, v82, v109
	v_pack_b32_f16 v82, v123, v108
	v_pk_fma_f16 v84, v60, v128, v84
	v_pk_mul_f16 v139, v83, v82
	v_pack_b32_f16 v82, v124, v107
	v_pk_fma_f16 v85, v61, v129, v85
	v_pk_mul_f16 v140, v84, v82
	v_pack_b32_f16 v82, v125, v106
	v_pk_mul_f16 v141, v85, v82
	s_waitcnt vmcnt(12)
	v_pk_mul_f16 v85, v204, v165 op_sel_hi:[0,1]
	v_pk_mul_f16 v109, v202, v165 op_sel_hi:[0,1]
	v_pk_mul_f16 v122, v203, v162 op_sel_hi:[0,1]
	v_pk_mul_f16 v125, v203, v165 op_sel_hi:[0,1]
	v_pk_mul_f16 v82, v204, v162 op_sel_hi:[0,1]
	v_pk_mul_f16 v83, v204, v163 op_sel_hi:[0,1]
	v_pk_mul_f16 v84, v204, v164 op_sel_hi:[0,1]
	v_pk_mul_f16 v106, v202, v162 op_sel_hi:[0,1]
	v_pk_mul_f16 v107, v202, v163 op_sel_hi:[0,1]
	v_pk_mul_f16 v108, v202, v164 op_sel_hi:[0,1]
	v_pk_mul_f16 v123, v203, v163 op_sel_hi:[0,1]
	v_pk_mul_f16 v124, v203, v164 op_sel_hi:[0,1]
	v_pk_fma_f16 v97, v97, v165, v85
	v_pk_fma_f16 v121, v121, v165, v109
	v_pk_fma_f16 v126, v137, v165, v125
	v_pk_fma_f16 v129, v134, v162, v122
	v_pk_fma_f16 v134, v65, v165, v85
	v_pk_fma_f16 v146, v81, v165, v109
	v_pk_fma_f16 v205, v105, v165, v125
	v_pk_fma_f16 v85, v37, v165, v85
	v_pk_fma_f16 v109, v49, v165, v109
	v_pk_fma_f16 v125, v69, v165, v125
	v_pk_maximum3_f16 v165, v97, v121, v126
	v_pk_fma_f16 v96, v96, v164, v84
	v_pk_fma_f16 v95, v95, v163, v83
	v_pk_fma_f16 v94, v94, v162, v82
	v_pk_fma_f16 v120, v120, v164, v108
	v_pk_fma_f16 v119, v119, v163, v107
	v_pk_fma_f16 v118, v118, v162, v106
	v_pk_fma_f16 v127, v136, v164, v124
	v_pk_fma_f16 v128, v135, v163, v123
	v_pk_fma_f16 v135, v64, v164, v84
	v_pk_fma_f16 v136, v63, v163, v83
	v_pk_fma_f16 v137, v62, v162, v82
	v_pk_fma_f16 v147, v80, v164, v108
	v_pk_fma_f16 v148, v79, v163, v107
	v_pk_fma_f16 v149, v78, v162, v106
	v_pk_fma_f16 v206, v104, v164, v124
	v_pk_fma_f16 v207, v103, v163, v123
	v_pk_fma_f16 v208, v102, v162, v122
	v_pk_fma_f16 v84, v36, v164, v84
	v_pk_fma_f16 v83, v35, v163, v83
	v_pk_fma_f16 v82, v34, v162, v82
	v_pk_fma_f16 v108, v48, v164, v108
	v_pk_fma_f16 v107, v47, v163, v107
	v_pk_fma_f16 v106, v46, v162, v106
	v_pk_fma_f16 v124, v68, v164, v124
	v_pk_fma_f16 v123, v67, v163, v123
	v_pk_fma_f16 v122, v66, v162, v122
	v_pk_maximum3_f16 v162, v94, v118, v129
	v_pk_maximum3_f16 v163, v95, v119, v128
	v_pk_maximum3_f16 v164, v96, v120, v127
	v_pk_maximum3_f16 v212, v134, v146, v205
	v_pk_maximum3_f16 v216, v85, v109, v125
	v_pk_maximum3_f16 v209, v137, v149, v208
	v_pk_maximum3_f16 v210, v136, v148, v207
	v_pk_maximum3_f16 v211, v135, v147, v206
	v_pk_maximum3_f16 v213, v82, v106, v122
	v_pk_maximum3_f16 v214, v83, v107, v123
	v_pk_maximum3_f16 v165, v165, v212, v216
	v_pk_maximum3_f16 v215, v84, v108, v124
	v_pk_maximum3_f16 v162, v162, v209, v213
	v_pk_maximum3_f16 v163, v163, v210, v214
	v_pk_maximum3_f16 v164, v164, v211, v215
	v_pk_add_f16 v97, v97, v165 neg_lo:[0,1] neg_hi:[0,1]
	v_pk_add_f16 v94, v94, v162 neg_lo:[0,1] neg_hi:[0,1]
	v_pk_add_f16 v95, v95, v163 neg_lo:[0,1] neg_hi:[0,1]
	v_pk_add_f16 v96, v96, v164 neg_lo:[0,1] neg_hi:[0,1]
	v_pk_add_f16 v118, v118, v162 neg_lo:[0,1] neg_hi:[0,1]
	v_exp_f16_sdwa v209, v94 dst_sel:WORD_0 dst_unused:UNUSED_PAD src0_sel:WORD_0
	v_exp_f16_sdwa v210, v95 dst_sel:WORD_0 dst_unused:UNUSED_PAD src0_sel:WORD_0
	v_exp_f16_sdwa v211, v96 dst_sel:WORD_0 dst_unused:UNUSED_PAD src0_sel:WORD_0
	v_exp_f16_sdwa v212, v97 dst_sel:WORD_0 dst_unused:UNUSED_PAD src0_sel:WORD_0
	v_exp_f16_sdwa v209, v94 dst_sel:WORD_1 dst_unused:UNUSED_PRESERVE src0_sel:WORD_1
	v_exp_f16_sdwa v210, v95 dst_sel:WORD_1 dst_unused:UNUSED_PRESERVE src0_sel:WORD_1
	v_exp_f16_sdwa v211, v96 dst_sel:WORD_1 dst_unused:UNUSED_PRESERVE src0_sel:WORD_1
	v_exp_f16_sdwa v212, v97 dst_sel:WORD_1 dst_unused:UNUSED_PRESERVE src0_sel:WORD_1
	v_pk_add_f16 v119, v119, v163 neg_lo:[0,1] neg_hi:[0,1]
	v_pk_add_f16 v97, v209, 0
	v_pk_fma_f16 v57, v57, v212, 0
	v_pk_add_f16 v94, v212, 0
	v_pk_add_f16 v95, v211, 0
	v_pk_add_f16 v96, v210, 0
	v_pk_fma_f16 v56, v56, v211, 0
	v_pk_fma_f16 v55, v55, v210, 0
	v_pk_fma_f16 v54, v54, v209, 0
	v_pk_add_f16 v120, v120, v164 neg_lo:[0,1] neg_hi:[0,1]
	v_pk_add_f16 v121, v121, v165 neg_lo:[0,1] neg_hi:[0,1]
	v_pk_add_f16 v82, v82, v162 neg_lo:[0,1] neg_hi:[0,1]
	v_exp_f16_sdwa v209, v118 dst_sel:WORD_0 dst_unused:UNUSED_PAD src0_sel:WORD_0
	v_exp_f16_sdwa v210, v119 dst_sel:WORD_0 dst_unused:UNUSED_PAD src0_sel:WORD_0
	v_exp_f16_sdwa v211, v120 dst_sel:WORD_0 dst_unused:UNUSED_PAD src0_sel:WORD_0
	v_exp_f16_sdwa v212, v121 dst_sel:WORD_0 dst_unused:UNUSED_PAD src0_sel:WORD_0
	v_exp_f16_sdwa v209, v118 dst_sel:WORD_1 dst_unused:UNUSED_PRESERVE src0_sel:WORD_1
	v_exp_f16_sdwa v210, v119 dst_sel:WORD_1 dst_unused:UNUSED_PRESERVE src0_sel:WORD_1
	v_exp_f16_sdwa v211, v120 dst_sel:WORD_1 dst_unused:UNUSED_PRESERVE src0_sel:WORD_1
	v_exp_f16_sdwa v212, v121 dst_sel:WORD_1 dst_unused:UNUSED_PRESERVE src0_sel:WORD_1
	v_pk_add_f16 v83, v83, v163 neg_lo:[0,1] neg_hi:[0,1]
	v_pk_add_f16 v97, v97, v209
	v_pk_fma_f16 v57, v77, v212, v57
	v_pk_add_f16 v77, v126, v165 neg_lo:[0,1] neg_hi:[0,1]
	v_pk_add_f16 v96, v96, v210
	v_pk_add_f16 v95, v95, v211
	v_pk_add_f16 v94, v94, v212
	v_pk_fma_f16 v54, v74, v209, v54
	v_pk_fma_f16 v55, v75, v210, v55
	v_pk_fma_f16 v56, v76, v211, v56
	v_pk_add_f16 v74, v129, v162 neg_lo:[0,1] neg_hi:[0,1]
	v_pk_add_f16 v75, v128, v163 neg_lo:[0,1] neg_hi:[0,1]
	v_pk_add_f16 v76, v127, v164 neg_lo:[0,1] neg_hi:[0,1]
	v_pk_add_f16 v84, v84, v164 neg_lo:[0,1] neg_hi:[0,1]
	v_exp_f16_sdwa v118, v74 dst_sel:WORD_0 dst_unused:UNUSED_PAD src0_sel:WORD_0
	v_exp_f16_sdwa v119, v75 dst_sel:WORD_0 dst_unused:UNUSED_PAD src0_sel:WORD_0
	v_exp_f16_sdwa v120, v76 dst_sel:WORD_0 dst_unused:UNUSED_PAD src0_sel:WORD_0
	v_exp_f16_sdwa v121, v77 dst_sel:WORD_0 dst_unused:UNUSED_PAD src0_sel:WORD_0
	v_exp_f16_sdwa v118, v74 dst_sel:WORD_1 dst_unused:UNUSED_PRESERVE src0_sel:WORD_1
	v_exp_f16_sdwa v119, v75 dst_sel:WORD_1 dst_unused:UNUSED_PRESERVE src0_sel:WORD_1
	v_exp_f16_sdwa v120, v76 dst_sel:WORD_1 dst_unused:UNUSED_PRESERVE src0_sel:WORD_1
	v_exp_f16_sdwa v121, v77 dst_sel:WORD_1 dst_unused:UNUSED_PRESERVE src0_sel:WORD_1
	v_pk_add_f16 v85, v85, v165 neg_lo:[0,1] neg_hi:[0,1]
	v_pk_add_f16 v77, v97, v118
	v_pk_add_f16 v74, v94, v121
	v_pk_add_f16 v75, v95, v120
	v_pk_add_f16 v76, v96, v119
	v_pk_fma_f16 v57, v101, v121, v57
	v_pk_fma_f16 v56, v100, v120, v56
	v_pk_fma_f16 v55, v99, v119, v55
	v_pk_fma_f16 v54, v98, v118, v54
	v_pk_add_f16 v94, v137, v162 neg_lo:[0,1] neg_hi:[0,1]
	v_pk_add_f16 v95, v136, v163 neg_lo:[0,1] neg_hi:[0,1]
	v_pk_add_f16 v96, v135, v164 neg_lo:[0,1] neg_hi:[0,1]
	v_pk_add_f16 v97, v134, v165 neg_lo:[0,1] neg_hi:[0,1]
	v_exp_f16_sdwa v98, v94 dst_sel:WORD_0 dst_unused:UNUSED_PAD src0_sel:WORD_0
	v_exp_f16_sdwa v99, v95 dst_sel:WORD_0 dst_unused:UNUSED_PAD src0_sel:WORD_0
	v_exp_f16_sdwa v100, v96 dst_sel:WORD_0 dst_unused:UNUSED_PAD src0_sel:WORD_0
	v_exp_f16_sdwa v101, v97 dst_sel:WORD_0 dst_unused:UNUSED_PAD src0_sel:WORD_0
	v_exp_f16_sdwa v98, v94 dst_sel:WORD_1 dst_unused:UNUSED_PRESERVE src0_sel:WORD_1
	v_exp_f16_sdwa v99, v95 dst_sel:WORD_1 dst_unused:UNUSED_PRESERVE src0_sel:WORD_1
	v_exp_f16_sdwa v100, v96 dst_sel:WORD_1 dst_unused:UNUSED_PRESERVE src0_sel:WORD_1
	v_exp_f16_sdwa v101, v97 dst_sel:WORD_1 dst_unused:UNUSED_PRESERVE src0_sel:WORD_1
	v_pk_add_f16 v94, v149, v162 neg_lo:[0,1] neg_hi:[0,1]
	v_pk_add_f16 v77, v77, v98
	v_pk_add_f16 v76, v76, v99
	v_pk_add_f16 v75, v75, v100
	v_pk_add_f16 v74, v74, v101
	v_pk_fma_f16 v54, v30, v98, v54
	v_pk_fma_f16 v55, v31, v99, v55
	v_pk_fma_f16 v56, v32, v100, v56
	v_pk_fma_f16 v57, v33, v101, v57
	v_pk_add_f16 v95, v148, v163 neg_lo:[0,1] neg_hi:[0,1]
	v_pk_add_f16 v96, v147, v164 neg_lo:[0,1] neg_hi:[0,1]
	v_pk_add_f16 v97, v146, v165 neg_lo:[0,1] neg_hi:[0,1]
	v_exp_f16_sdwa v98, v94 dst_sel:WORD_0 dst_unused:UNUSED_PAD src0_sel:WORD_0
	v_exp_f16_sdwa v99, v95 dst_sel:WORD_0 dst_unused:UNUSED_PAD src0_sel:WORD_0
	v_exp_f16_sdwa v100, v96 dst_sel:WORD_0 dst_unused:UNUSED_PAD src0_sel:WORD_0
	v_exp_f16_sdwa v101, v97 dst_sel:WORD_0 dst_unused:UNUSED_PAD src0_sel:WORD_0
	v_exp_f16_sdwa v98, v94 dst_sel:WORD_1 dst_unused:UNUSED_PRESERVE src0_sel:WORD_1
	v_exp_f16_sdwa v99, v95 dst_sel:WORD_1 dst_unused:UNUSED_PRESERVE src0_sel:WORD_1
	v_exp_f16_sdwa v100, v96 dst_sel:WORD_1 dst_unused:UNUSED_PRESERVE src0_sel:WORD_1
	v_exp_f16_sdwa v101, v97 dst_sel:WORD_1 dst_unused:UNUSED_PRESERVE src0_sel:WORD_1
	v_pk_add_f16 v94, v208, v162 neg_lo:[0,1] neg_hi:[0,1]
	v_pk_add_f16 v77, v77, v98
	v_pk_add_f16 v74, v74, v101
	v_pk_add_f16 v75, v75, v100
	v_pk_add_f16 v76, v76, v99
	v_pk_fma_f16 v57, v45, v101, v57
	v_pk_fma_f16 v56, v44, v100, v56
	v_pk_fma_f16 v55, v43, v99, v55
	v_pk_fma_f16 v54, v42, v98, v54
	v_pk_add_f16 v95, v207, v163 neg_lo:[0,1] neg_hi:[0,1]
	v_pk_add_f16 v96, v206, v164 neg_lo:[0,1] neg_hi:[0,1]
	v_pk_add_f16 v97, v205, v165 neg_lo:[0,1] neg_hi:[0,1]
	v_exp_f16_sdwa v98, v94 dst_sel:WORD_0 dst_unused:UNUSED_PAD src0_sel:WORD_0
	v_exp_f16_sdwa v99, v95 dst_sel:WORD_0 dst_unused:UNUSED_PAD src0_sel:WORD_0
	v_exp_f16_sdwa v100, v96 dst_sel:WORD_0 dst_unused:UNUSED_PAD src0_sel:WORD_0
	v_exp_f16_sdwa v101, v97 dst_sel:WORD_0 dst_unused:UNUSED_PAD src0_sel:WORD_0
	v_exp_f16_sdwa v98, v94 dst_sel:WORD_1 dst_unused:UNUSED_PRESERVE src0_sel:WORD_1
	v_exp_f16_sdwa v99, v95 dst_sel:WORD_1 dst_unused:UNUSED_PRESERVE src0_sel:WORD_1
	v_exp_f16_sdwa v100, v96 dst_sel:WORD_1 dst_unused:UNUSED_PRESERVE src0_sel:WORD_1
	v_exp_f16_sdwa v101, v97 dst_sel:WORD_1 dst_unused:UNUSED_PRESERVE src0_sel:WORD_1
	v_exp_f16_sdwa v94, v82 dst_sel:WORD_0 dst_unused:UNUSED_PAD src0_sel:WORD_0
	v_exp_f16_sdwa v95, v83 dst_sel:WORD_0 dst_unused:UNUSED_PAD src0_sel:WORD_0
	v_exp_f16_sdwa v96, v84 dst_sel:WORD_0 dst_unused:UNUSED_PAD src0_sel:WORD_0
	v_exp_f16_sdwa v97, v85 dst_sel:WORD_0 dst_unused:UNUSED_PAD src0_sel:WORD_0
	v_exp_f16_sdwa v94, v82 dst_sel:WORD_1 dst_unused:UNUSED_PRESERVE src0_sel:WORD_1
	v_exp_f16_sdwa v95, v83 dst_sel:WORD_1 dst_unused:UNUSED_PRESERVE src0_sel:WORD_1
	v_exp_f16_sdwa v96, v84 dst_sel:WORD_1 dst_unused:UNUSED_PRESERVE src0_sel:WORD_1
	v_exp_f16_sdwa v97, v85 dst_sel:WORD_1 dst_unused:UNUSED_PRESERVE src0_sel:WORD_1
	v_pk_add_f16 v82, v106, v162 neg_lo:[0,1] neg_hi:[0,1]
	v_pk_add_f16 v77, v77, v98
	v_pk_add_f16 v76, v76, v99
	v_pk_add_f16 v75, v75, v100
	v_pk_add_f16 v74, v74, v101
	v_pk_fma_f16 v54, v58, v98, v54
	v_pk_fma_f16 v55, v59, v99, v55
	v_pk_fma_f16 v56, v60, v100, v56
	v_pk_fma_f16 v57, v61, v101, v57
	v_pk_add_f16 v77, v77, v94
	v_pk_add_f16 v74, v74, v97
	v_pk_add_f16 v75, v75, v96
	v_pk_add_f16 v76, v76, v95
	v_pk_fma_f16 v57, v21, v97, v57
	v_pk_fma_f16 v56, v20, v96, v56
	v_pk_fma_f16 v55, v19, v95, v55
	v_pk_fma_f16 v54, v18, v94, v54
	v_pk_add_f16 v83, v107, v163 neg_lo:[0,1] neg_hi:[0,1]
	v_pk_add_f16 v84, v108, v164 neg_lo:[0,1] neg_hi:[0,1]
	v_pk_add_f16 v85, v109, v165 neg_lo:[0,1] neg_hi:[0,1]
	v_exp_f16_sdwa v94, v82 dst_sel:WORD_0 dst_unused:UNUSED_PAD src0_sel:WORD_0
	v_exp_f16_sdwa v95, v83 dst_sel:WORD_0 dst_unused:UNUSED_PAD src0_sel:WORD_0
	v_exp_f16_sdwa v96, v84 dst_sel:WORD_0 dst_unused:UNUSED_PAD src0_sel:WORD_0
	v_exp_f16_sdwa v97, v85 dst_sel:WORD_0 dst_unused:UNUSED_PAD src0_sel:WORD_0
	v_exp_f16_sdwa v94, v82 dst_sel:WORD_1 dst_unused:UNUSED_PRESERVE src0_sel:WORD_1
	v_exp_f16_sdwa v95, v83 dst_sel:WORD_1 dst_unused:UNUSED_PRESERVE src0_sel:WORD_1
	v_exp_f16_sdwa v96, v84 dst_sel:WORD_1 dst_unused:UNUSED_PRESERVE src0_sel:WORD_1
	v_exp_f16_sdwa v97, v85 dst_sel:WORD_1 dst_unused:UNUSED_PRESERVE src0_sel:WORD_1
	v_pk_add_f16 v82, v122, v162 neg_lo:[0,1] neg_hi:[0,1]
	v_pk_add_f16 v77, v77, v94
	v_pk_add_f16 v76, v76, v95
	v_pk_add_f16 v75, v75, v96
	v_pk_add_f16 v74, v74, v97
	v_pk_fma_f16 v54, v22, v94, v54
	v_pk_fma_f16 v55, v23, v95, v55
	v_pk_fma_f16 v56, v24, v96, v56
	v_pk_fma_f16 v57, v25, v97, v57
	v_pk_add_f16 v83, v123, v163 neg_lo:[0,1] neg_hi:[0,1]
	v_pk_add_f16 v84, v124, v164 neg_lo:[0,1] neg_hi:[0,1]
	v_pk_add_f16 v85, v125, v165 neg_lo:[0,1] neg_hi:[0,1]
	v_exp_f16_sdwa v94, v82 dst_sel:WORD_0 dst_unused:UNUSED_PAD src0_sel:WORD_0
	v_exp_f16_sdwa v95, v83 dst_sel:WORD_0 dst_unused:UNUSED_PAD src0_sel:WORD_0
	v_exp_f16_sdwa v96, v84 dst_sel:WORD_0 dst_unused:UNUSED_PAD src0_sel:WORD_0
	v_exp_f16_sdwa v97, v85 dst_sel:WORD_0 dst_unused:UNUSED_PAD src0_sel:WORD_0
	v_exp_f16_sdwa v94, v82 dst_sel:WORD_1 dst_unused:UNUSED_PRESERVE src0_sel:WORD_1
	v_exp_f16_sdwa v95, v83 dst_sel:WORD_1 dst_unused:UNUSED_PRESERVE src0_sel:WORD_1
	v_exp_f16_sdwa v96, v84 dst_sel:WORD_1 dst_unused:UNUSED_PRESERVE src0_sel:WORD_1
	v_exp_f16_sdwa v97, v85 dst_sel:WORD_1 dst_unused:UNUSED_PRESERVE src0_sel:WORD_1
	v_pk_add_f16 v77, v77, v94
	v_pk_add_f16 v76, v76, v95
	v_rcp_f16_e32 v82, v77
	v_rcp_f16_sdwa v77, v77 dst_sel:DWORD dst_unused:UNUSED_PAD src0_sel:WORD_1
	v_pk_add_f16 v75, v75, v96
	v_rcp_f16_e32 v83, v76
	v_rcp_f16_sdwa v76, v76 dst_sel:DWORD dst_unused:UNUSED_PAD src0_sel:WORD_1
	v_pk_add_f16 v74, v74, v97
	v_rcp_f16_e32 v84, v75
	v_rcp_f16_sdwa v75, v75 dst_sel:DWORD dst_unused:UNUSED_PAD src0_sel:WORD_1
	v_rcp_f16_e32 v85, v74
	v_rcp_f16_sdwa v74, v74 dst_sel:DWORD dst_unused:UNUSED_PAD src0_sel:WORD_1
	v_pk_fma_f16 v54, v26, v94, v54
	v_pack_b32_f16 v77, v82, v77
	v_pk_fma_f16 v55, v27, v95, v55
	v_pk_mul_f16 v77, v54, v77
	v_pack_b32_f16 v54, v83, v76
	v_pk_fma_f16 v56, v28, v96, v56
	v_pk_mul_f16 v76, v55, v54
	v_pack_b32_f16 v54, v84, v75
	v_pk_fma_f16 v57, v29, v97, v57
	v_pk_mul_f16 v75, v56, v54
	v_pack_b32_f16 v54, v85, v74
	v_pk_mul_f16 v74, v57, v54
	s_waitcnt vmcnt(6)
	v_pk_mul_f16 v57, v204, v161 op_sel_hi:[0,1]
	v_pk_mul_f16 v85, v202, v161 op_sel_hi:[0,1]
	v_pk_mul_f16 v97, v203, v161 op_sel_hi:[0,1]
	v_pk_mul_f16 v54, v204, v158 op_sel_hi:[0,1]
	v_pk_mul_f16 v55, v204, v159 op_sel_hi:[0,1]
	v_pk_mul_f16 v56, v204, v160 op_sel_hi:[0,1]
	v_pk_mul_f16 v82, v202, v158 op_sel_hi:[0,1]
	v_pk_mul_f16 v83, v202, v159 op_sel_hi:[0,1]
	v_pk_mul_f16 v84, v202, v160 op_sel_hi:[0,1]
	v_pk_mul_f16 v94, v203, v158 op_sel_hi:[0,1]
	v_pk_mul_f16 v95, v203, v159 op_sel_hi:[0,1]
	v_pk_mul_f16 v96, v203, v160 op_sel_hi:[0,1]
	v_pk_fma_f16 v65, v65, v161, v57
	v_pk_fma_f16 v81, v81, v161, v85
	v_pk_fma_f16 v98, v105, v161, v97
	v_pk_fma_f16 v64, v64, v160, v56
	v_pk_maximum3_f16 v125, v65, v81, v98
	v_pk_fma_f16 v63, v63, v159, v55
	v_pk_fma_f16 v62, v62, v158, v54
	v_pk_fma_f16 v80, v80, v160, v84
	v_pk_fma_f16 v79, v79, v159, v83
	v_pk_fma_f16 v78, v78, v158, v82
	v_pk_fma_f16 v99, v104, v160, v96
	v_pk_fma_f16 v100, v103, v159, v95
	v_pk_fma_f16 v101, v102, v158, v94
	v_pk_fma_f16 v102, v37, v161, v57
	v_pk_fma_f16 v106, v49, v161, v85
	v_pk_fma_f16 v118, v69, v161, v97
	v_pk_fma_f16 v57, v89, v161, v57
	v_pk_fma_f16 v85, v117, v161, v85
	v_pk_fma_f16 v97, v133, v161, v97
	v_pk_maximum3_f16 v122, v62, v78, v101
	v_pk_maximum3_f16 v123, v63, v79, v100
	v_pk_maximum3_f16 v124, v64, v80, v99
	v_pk_maximum3_f16 v129, v102, v106, v118
	v_pk_fma_f16 v103, v36, v160, v56
	v_pk_maximum3_f16 v137, v57, v85, v97
	v_pk_fma_f16 v104, v35, v159, v55
	v_pk_maximum3_f16 v125, v125, v129, v137
	v_pk_fma_f16 v105, v34, v158, v54
	v_pk_fma_f16 v107, v48, v160, v84
	v_pk_fma_f16 v108, v47, v159, v83
	v_pk_fma_f16 v109, v46, v158, v82
	v_pk_fma_f16 v119, v68, v160, v96
	v_pk_fma_f16 v120, v67, v159, v95
	v_pk_fma_f16 v121, v66, v158, v94
	v_pk_fma_f16 v56, v88, v160, v56
	v_pk_fma_f16 v55, v87, v159, v55
	v_pk_fma_f16 v54, v86, v158, v54
	v_pk_fma_f16 v84, v116, v160, v84
	v_pk_fma_f16 v83, v115, v159, v83
	v_pk_fma_f16 v82, v114, v158, v82
	v_pk_fma_f16 v96, v132, v160, v96
	v_pk_fma_f16 v95, v131, v159, v95
	v_pk_fma_f16 v94, v130, v158, v94
	v_pk_maximum3_f16 v126, v105, v109, v121
	v_pk_maximum3_f16 v127, v104, v108, v120
	v_pk_maximum3_f16 v128, v103, v107, v119
	v_pk_maximum3_f16 v135, v55, v83, v95
	v_pk_maximum3_f16 v136, v56, v84, v96
	v_pk_maximum3_f16 v134, v54, v82, v94
	v_pk_maximum3_f16 v122, v122, v126, v134
	v_pk_maximum3_f16 v123, v123, v127, v135
	v_pk_maximum3_f16 v124, v124, v128, v136
	v_pk_add_f16 v65, v65, v125 neg_lo:[0,1] neg_hi:[0,1]
	v_pk_add_f16 v62, v62, v122 neg_lo:[0,1] neg_hi:[0,1]
	v_pk_add_f16 v63, v63, v123 neg_lo:[0,1] neg_hi:[0,1]
	v_pk_add_f16 v64, v64, v124 neg_lo:[0,1] neg_hi:[0,1]
	v_pk_add_f16 v78, v78, v122 neg_lo:[0,1] neg_hi:[0,1]
	v_exp_f16_sdwa v126, v62 dst_sel:WORD_0 dst_unused:UNUSED_PAD src0_sel:WORD_0
	v_exp_f16_sdwa v127, v63 dst_sel:WORD_0 dst_unused:UNUSED_PAD src0_sel:WORD_0
	v_exp_f16_sdwa v128, v64 dst_sel:WORD_0 dst_unused:UNUSED_PAD src0_sel:WORD_0
	v_exp_f16_sdwa v129, v65 dst_sel:WORD_0 dst_unused:UNUSED_PAD src0_sel:WORD_0
	v_exp_f16_sdwa v126, v62 dst_sel:WORD_1 dst_unused:UNUSED_PRESERVE src0_sel:WORD_1
	v_exp_f16_sdwa v127, v63 dst_sel:WORD_1 dst_unused:UNUSED_PRESERVE src0_sel:WORD_1
	v_exp_f16_sdwa v128, v64 dst_sel:WORD_1 dst_unused:UNUSED_PRESERVE src0_sel:WORD_1
	v_exp_f16_sdwa v129, v65 dst_sel:WORD_1 dst_unused:UNUSED_PRESERVE src0_sel:WORD_1
	v_pk_add_f16 v79, v79, v123 neg_lo:[0,1] neg_hi:[0,1]
	v_pk_add_f16 v65, v126, 0
	v_pk_fma_f16 v33, v33, v129, 0
	v_pk_add_f16 v62, v129, 0
	v_pk_add_f16 v63, v128, 0
	v_pk_add_f16 v64, v127, 0
	v_pk_fma_f16 v32, v32, v128, 0
	v_pk_fma_f16 v31, v31, v127, 0
	v_pk_fma_f16 v30, v30, v126, 0
	v_pk_add_f16 v80, v80, v124 neg_lo:[0,1] neg_hi:[0,1]
	v_pk_add_f16 v81, v81, v125 neg_lo:[0,1] neg_hi:[0,1]
	v_pk_add_f16 v54, v54, v122 neg_lo:[0,1] neg_hi:[0,1]
	v_exp_f16_sdwa v126, v78 dst_sel:WORD_0 dst_unused:UNUSED_PAD src0_sel:WORD_0
	v_exp_f16_sdwa v127, v79 dst_sel:WORD_0 dst_unused:UNUSED_PAD src0_sel:WORD_0
	v_exp_f16_sdwa v128, v80 dst_sel:WORD_0 dst_unused:UNUSED_PAD src0_sel:WORD_0
	v_exp_f16_sdwa v129, v81 dst_sel:WORD_0 dst_unused:UNUSED_PAD src0_sel:WORD_0
	v_exp_f16_sdwa v126, v78 dst_sel:WORD_1 dst_unused:UNUSED_PRESERVE src0_sel:WORD_1
	v_exp_f16_sdwa v127, v79 dst_sel:WORD_1 dst_unused:UNUSED_PRESERVE src0_sel:WORD_1
	v_exp_f16_sdwa v128, v80 dst_sel:WORD_1 dst_unused:UNUSED_PRESERVE src0_sel:WORD_1
	v_exp_f16_sdwa v129, v81 dst_sel:WORD_1 dst_unused:UNUSED_PRESERVE src0_sel:WORD_1
	v_pk_add_f16 v55, v55, v123 neg_lo:[0,1] neg_hi:[0,1]
	v_pk_add_f16 v65, v65, v126
	v_pk_fma_f16 v33, v45, v129, v33
	v_pk_add_f16 v45, v98, v125 neg_lo:[0,1] neg_hi:[0,1]
	v_pk_add_f16 v64, v64, v127
	v_pk_add_f16 v63, v63, v128
	v_pk_add_f16 v62, v62, v129
	v_pk_fma_f16 v30, v42, v126, v30
	v_pk_fma_f16 v31, v43, v127, v31
	v_pk_fma_f16 v32, v44, v128, v32
	v_pk_add_f16 v42, v101, v122 neg_lo:[0,1] neg_hi:[0,1]
	v_pk_add_f16 v43, v100, v123 neg_lo:[0,1] neg_hi:[0,1]
	v_pk_add_f16 v44, v99, v124 neg_lo:[0,1] neg_hi:[0,1]
	v_pk_add_f16 v56, v56, v124 neg_lo:[0,1] neg_hi:[0,1]
	v_exp_f16_sdwa v78, v42 dst_sel:WORD_0 dst_unused:UNUSED_PAD src0_sel:WORD_0
	v_exp_f16_sdwa v79, v43 dst_sel:WORD_0 dst_unused:UNUSED_PAD src0_sel:WORD_0
	v_exp_f16_sdwa v80, v44 dst_sel:WORD_0 dst_unused:UNUSED_PAD src0_sel:WORD_0
	v_exp_f16_sdwa v81, v45 dst_sel:WORD_0 dst_unused:UNUSED_PAD src0_sel:WORD_0
	v_exp_f16_sdwa v78, v42 dst_sel:WORD_1 dst_unused:UNUSED_PRESERVE src0_sel:WORD_1
	v_exp_f16_sdwa v79, v43 dst_sel:WORD_1 dst_unused:UNUSED_PRESERVE src0_sel:WORD_1
	v_exp_f16_sdwa v80, v44 dst_sel:WORD_1 dst_unused:UNUSED_PRESERVE src0_sel:WORD_1
	v_exp_f16_sdwa v81, v45 dst_sel:WORD_1 dst_unused:UNUSED_PRESERVE src0_sel:WORD_1
	v_pk_add_f16 v57, v57, v125 neg_lo:[0,1] neg_hi:[0,1]
	v_pk_add_f16 v45, v65, v78
	v_pk_add_f16 v42, v62, v81
	v_pk_add_f16 v43, v63, v80
	v_pk_add_f16 v44, v64, v79
	v_pk_fma_f16 v33, v61, v81, v33
	v_pk_fma_f16 v32, v60, v80, v32
	v_pk_fma_f16 v31, v59, v79, v31
	v_pk_fma_f16 v30, v58, v78, v30
	v_pk_add_f16 v58, v105, v122 neg_lo:[0,1] neg_hi:[0,1]
	v_pk_add_f16 v59, v104, v123 neg_lo:[0,1] neg_hi:[0,1]
	v_pk_add_f16 v60, v103, v124 neg_lo:[0,1] neg_hi:[0,1]
	v_pk_add_f16 v61, v102, v125 neg_lo:[0,1] neg_hi:[0,1]
	v_exp_f16_sdwa v62, v58 dst_sel:WORD_0 dst_unused:UNUSED_PAD src0_sel:WORD_0
	v_exp_f16_sdwa v63, v59 dst_sel:WORD_0 dst_unused:UNUSED_PAD src0_sel:WORD_0
	v_exp_f16_sdwa v64, v60 dst_sel:WORD_0 dst_unused:UNUSED_PAD src0_sel:WORD_0
	v_exp_f16_sdwa v65, v61 dst_sel:WORD_0 dst_unused:UNUSED_PAD src0_sel:WORD_0
	v_exp_f16_sdwa v62, v58 dst_sel:WORD_1 dst_unused:UNUSED_PRESERVE src0_sel:WORD_1
	v_exp_f16_sdwa v63, v59 dst_sel:WORD_1 dst_unused:UNUSED_PRESERVE src0_sel:WORD_1
	v_exp_f16_sdwa v64, v60 dst_sel:WORD_1 dst_unused:UNUSED_PRESERVE src0_sel:WORD_1
	v_exp_f16_sdwa v65, v61 dst_sel:WORD_1 dst_unused:UNUSED_PRESERVE src0_sel:WORD_1
	v_pk_add_f16 v58, v109, v122 neg_lo:[0,1] neg_hi:[0,1]
	v_pk_add_f16 v45, v45, v62
	v_pk_add_f16 v44, v44, v63
	v_pk_add_f16 v43, v43, v64
	v_pk_add_f16 v42, v42, v65
	v_pk_fma_f16 v30, v18, v62, v30
	v_pk_fma_f16 v31, v19, v63, v31
	v_pk_fma_f16 v32, v20, v64, v32
	v_pk_fma_f16 v33, v21, v65, v33
	v_pk_add_f16 v59, v108, v123 neg_lo:[0,1] neg_hi:[0,1]
	v_pk_add_f16 v60, v107, v124 neg_lo:[0,1] neg_hi:[0,1]
	v_pk_add_f16 v61, v106, v125 neg_lo:[0,1] neg_hi:[0,1]
	v_exp_f16_sdwa v62, v58 dst_sel:WORD_0 dst_unused:UNUSED_PAD src0_sel:WORD_0
	v_exp_f16_sdwa v63, v59 dst_sel:WORD_0 dst_unused:UNUSED_PAD src0_sel:WORD_0
	v_exp_f16_sdwa v64, v60 dst_sel:WORD_0 dst_unused:UNUSED_PAD src0_sel:WORD_0
	v_exp_f16_sdwa v65, v61 dst_sel:WORD_0 dst_unused:UNUSED_PAD src0_sel:WORD_0
	v_exp_f16_sdwa v62, v58 dst_sel:WORD_1 dst_unused:UNUSED_PRESERVE src0_sel:WORD_1
	v_exp_f16_sdwa v63, v59 dst_sel:WORD_1 dst_unused:UNUSED_PRESERVE src0_sel:WORD_1
	v_exp_f16_sdwa v64, v60 dst_sel:WORD_1 dst_unused:UNUSED_PRESERVE src0_sel:WORD_1
	v_exp_f16_sdwa v65, v61 dst_sel:WORD_1 dst_unused:UNUSED_PRESERVE src0_sel:WORD_1
	v_pk_add_f16 v58, v121, v122 neg_lo:[0,1] neg_hi:[0,1]
	v_pk_add_f16 v45, v45, v62
	v_pk_add_f16 v42, v42, v65
	v_pk_add_f16 v43, v43, v64
	v_pk_add_f16 v44, v44, v63
	v_pk_fma_f16 v33, v25, v65, v33
	v_pk_fma_f16 v32, v24, v64, v32
	v_pk_fma_f16 v31, v23, v63, v31
	v_pk_fma_f16 v30, v22, v62, v30
	v_pk_add_f16 v59, v120, v123 neg_lo:[0,1] neg_hi:[0,1]
	v_pk_add_f16 v60, v119, v124 neg_lo:[0,1] neg_hi:[0,1]
	v_pk_add_f16 v61, v118, v125 neg_lo:[0,1] neg_hi:[0,1]
	v_exp_f16_sdwa v62, v58 dst_sel:WORD_0 dst_unused:UNUSED_PAD src0_sel:WORD_0
	v_exp_f16_sdwa v63, v59 dst_sel:WORD_0 dst_unused:UNUSED_PAD src0_sel:WORD_0
	v_exp_f16_sdwa v64, v60 dst_sel:WORD_0 dst_unused:UNUSED_PAD src0_sel:WORD_0
	v_exp_f16_sdwa v65, v61 dst_sel:WORD_0 dst_unused:UNUSED_PAD src0_sel:WORD_0
	v_exp_f16_sdwa v62, v58 dst_sel:WORD_1 dst_unused:UNUSED_PRESERVE src0_sel:WORD_1
	v_exp_f16_sdwa v63, v59 dst_sel:WORD_1 dst_unused:UNUSED_PRESERVE src0_sel:WORD_1
	v_exp_f16_sdwa v64, v60 dst_sel:WORD_1 dst_unused:UNUSED_PRESERVE src0_sel:WORD_1
	v_exp_f16_sdwa v65, v61 dst_sel:WORD_1 dst_unused:UNUSED_PRESERVE src0_sel:WORD_1
	v_exp_f16_sdwa v58, v54 dst_sel:WORD_0 dst_unused:UNUSED_PAD src0_sel:WORD_0
	v_exp_f16_sdwa v59, v55 dst_sel:WORD_0 dst_unused:UNUSED_PAD src0_sel:WORD_0
	v_exp_f16_sdwa v60, v56 dst_sel:WORD_0 dst_unused:UNUSED_PAD src0_sel:WORD_0
	v_exp_f16_sdwa v61, v57 dst_sel:WORD_0 dst_unused:UNUSED_PAD src0_sel:WORD_0
	v_exp_f16_sdwa v58, v54 dst_sel:WORD_1 dst_unused:UNUSED_PRESERVE src0_sel:WORD_1
	v_exp_f16_sdwa v59, v55 dst_sel:WORD_1 dst_unused:UNUSED_PRESERVE src0_sel:WORD_1
	v_exp_f16_sdwa v60, v56 dst_sel:WORD_1 dst_unused:UNUSED_PRESERVE src0_sel:WORD_1
	v_exp_f16_sdwa v61, v57 dst_sel:WORD_1 dst_unused:UNUSED_PRESERVE src0_sel:WORD_1
	v_pk_add_f16 v54, v82, v122 neg_lo:[0,1] neg_hi:[0,1]
	v_pk_add_f16 v45, v45, v62
	v_pk_add_f16 v44, v44, v63
	v_pk_add_f16 v43, v43, v64
	v_pk_add_f16 v42, v42, v65
	v_pk_fma_f16 v30, v26, v62, v30
	v_pk_fma_f16 v31, v27, v63, v31
	v_pk_fma_f16 v32, v28, v64, v32
	v_pk_fma_f16 v33, v29, v65, v33
	v_pk_add_f16 v45, v45, v58
	v_pk_add_f16 v42, v42, v61
	v_pk_add_f16 v43, v43, v60
	v_pk_add_f16 v44, v44, v59
	v_pk_fma_f16 v33, v41, v61, v33
	v_pk_fma_f16 v32, v40, v60, v32
	v_pk_fma_f16 v31, v39, v59, v31
	v_pk_fma_f16 v30, v38, v58, v30
	v_pk_add_f16 v55, v83, v123 neg_lo:[0,1] neg_hi:[0,1]
	v_pk_add_f16 v56, v84, v124 neg_lo:[0,1] neg_hi:[0,1]
	v_pk_add_f16 v57, v85, v125 neg_lo:[0,1] neg_hi:[0,1]
	v_exp_f16_sdwa v58, v54 dst_sel:WORD_0 dst_unused:UNUSED_PAD src0_sel:WORD_0
	v_exp_f16_sdwa v59, v55 dst_sel:WORD_0 dst_unused:UNUSED_PAD src0_sel:WORD_0
	v_exp_f16_sdwa v60, v56 dst_sel:WORD_0 dst_unused:UNUSED_PAD src0_sel:WORD_0
	v_exp_f16_sdwa v61, v57 dst_sel:WORD_0 dst_unused:UNUSED_PAD src0_sel:WORD_0
	v_exp_f16_sdwa v58, v54 dst_sel:WORD_1 dst_unused:UNUSED_PRESERVE src0_sel:WORD_1
	v_exp_f16_sdwa v59, v55 dst_sel:WORD_1 dst_unused:UNUSED_PRESERVE src0_sel:WORD_1
	v_exp_f16_sdwa v60, v56 dst_sel:WORD_1 dst_unused:UNUSED_PRESERVE src0_sel:WORD_1
	v_exp_f16_sdwa v61, v57 dst_sel:WORD_1 dst_unused:UNUSED_PRESERVE src0_sel:WORD_1
	v_pk_add_f16 v54, v94, v122 neg_lo:[0,1] neg_hi:[0,1]
	v_pk_add_f16 v45, v45, v58
	v_pk_add_f16 v44, v44, v59
	v_pk_add_f16 v43, v43, v60
	v_pk_add_f16 v42, v42, v61
	v_pk_fma_f16 v30, v50, v58, v30
	v_pk_fma_f16 v31, v51, v59, v31
	v_pk_fma_f16 v32, v52, v60, v32
	v_pk_fma_f16 v33, v53, v61, v33
	v_pk_add_f16 v55, v95, v123 neg_lo:[0,1] neg_hi:[0,1]
	v_pk_add_f16 v56, v96, v124 neg_lo:[0,1] neg_hi:[0,1]
	v_pk_add_f16 v57, v97, v125 neg_lo:[0,1] neg_hi:[0,1]
	v_exp_f16_sdwa v58, v54 dst_sel:WORD_0 dst_unused:UNUSED_PAD src0_sel:WORD_0
	v_exp_f16_sdwa v59, v55 dst_sel:WORD_0 dst_unused:UNUSED_PAD src0_sel:WORD_0
	v_exp_f16_sdwa v60, v56 dst_sel:WORD_0 dst_unused:UNUSED_PAD src0_sel:WORD_0
	v_exp_f16_sdwa v61, v57 dst_sel:WORD_0 dst_unused:UNUSED_PAD src0_sel:WORD_0
	v_exp_f16_sdwa v58, v54 dst_sel:WORD_1 dst_unused:UNUSED_PRESERVE src0_sel:WORD_1
	v_exp_f16_sdwa v59, v55 dst_sel:WORD_1 dst_unused:UNUSED_PRESERVE src0_sel:WORD_1
	v_exp_f16_sdwa v60, v56 dst_sel:WORD_1 dst_unused:UNUSED_PRESERVE src0_sel:WORD_1
	v_exp_f16_sdwa v61, v57 dst_sel:WORD_1 dst_unused:UNUSED_PRESERVE src0_sel:WORD_1
	v_pk_add_f16 v45, v45, v58
	v_pk_add_f16 v44, v44, v59
	v_rcp_f16_e32 v54, v45
	v_rcp_f16_sdwa v45, v45 dst_sel:DWORD dst_unused:UNUSED_PAD src0_sel:WORD_1
	v_pk_add_f16 v43, v43, v60
	v_rcp_f16_e32 v55, v44
	v_rcp_f16_sdwa v44, v44 dst_sel:DWORD dst_unused:UNUSED_PAD src0_sel:WORD_1
	v_pk_add_f16 v42, v42, v61
	v_pk_fma_f16 v30, v70, v58, v30
	v_rcp_f16_e32 v58, v43
	v_rcp_f16_sdwa v43, v43 dst_sel:DWORD dst_unused:UNUSED_PAD src0_sel:WORD_1
	v_pk_fma_f16 v31, v71, v59, v31
	v_rcp_f16_e32 v59, v42
	v_rcp_f16_sdwa v42, v42 dst_sel:DWORD dst_unused:UNUSED_PAD src0_sel:WORD_1
	v_pack_b32_f16 v45, v54, v45
	v_pk_mul_f16 v57, v30, v45
	v_pack_b32_f16 v30, v55, v44
	v_pk_fma_f16 v32, v72, v60, v32
	v_pk_mul_f16 v56, v31, v30
	v_pack_b32_f16 v30, v58, v43
	v_pk_fma_f16 v33, v73, v61, v33
	v_pk_mul_f16 v55, v32, v30
	v_pack_b32_f16 v30, v59, v42
	v_pk_mul_f16 v54, v33, v30
	s_waitcnt vmcnt(0)
	v_pk_mul_f16 v30, v204, v154 op_sel_hi:[0,1]
	v_pk_mul_f16 v31, v204, v155 op_sel_hi:[0,1]
	v_pk_mul_f16 v32, v204, v156 op_sel_hi:[0,1]
	v_pk_mul_f16 v33, v204, v157 op_sel_hi:[0,1]
	v_pk_mul_f16 v42, v202, v154 op_sel_hi:[0,1]
	v_pk_mul_f16 v43, v202, v155 op_sel_hi:[0,1]
	v_pk_mul_f16 v44, v202, v156 op_sel_hi:[0,1]
	v_pk_mul_f16 v45, v202, v157 op_sel_hi:[0,1]
	v_pk_mul_f16 v58, v203, v154 op_sel_hi:[0,1]
	v_pk_mul_f16 v59, v203, v155 op_sel_hi:[0,1]
	v_pk_mul_f16 v60, v203, v156 op_sel_hi:[0,1]
	v_pk_mul_f16 v61, v203, v157 op_sel_hi:[0,1]
	v_pk_fma_f16 v37, v37, v157, v33
	v_pk_fma_f16 v36, v36, v156, v32
	v_pk_fma_f16 v35, v35, v155, v31
	v_pk_fma_f16 v34, v34, v154, v30
	v_pk_fma_f16 v49, v49, v157, v45
	v_pk_fma_f16 v48, v48, v156, v44
	v_pk_fma_f16 v47, v47, v155, v43
	v_pk_fma_f16 v46, v46, v154, v42
	v_pk_fma_f16 v62, v69, v157, v61
	v_pk_fma_f16 v63, v68, v156, v60
	v_pk_fma_f16 v64, v67, v155, v59
	v_pk_fma_f16 v65, v66, v154, v58
	v_pk_fma_f16 v66, v89, v157, v33
	v_pk_fma_f16 v67, v88, v156, v32
	v_pk_fma_f16 v68, v87, v155, v31
	v_pk_fma_f16 v69, v86, v154, v30
	v_pk_fma_f16 v78, v117, v157, v45
	v_pk_fma_f16 v79, v116, v156, v44
	v_pk_fma_f16 v80, v115, v155, v43
	v_pk_fma_f16 v81, v114, v154, v42
	v_pk_fma_f16 v82, v133, v157, v61
	v_pk_fma_f16 v83, v132, v156, v60
	v_pk_fma_f16 v84, v131, v155, v59
	v_pk_fma_f16 v85, v130, v154, v58
	v_pk_fma_f16 v61, v17, v157, v61
	v_pk_fma_f16 v60, v16, v156, v60
	v_pk_fma_f16 v59, v15, v155, v59
	v_pk_fma_f16 v58, v14, v154, v58
	v_pk_maximum3_f16 v14, v34, v46, v65
	v_pk_maximum3_f16 v15, v35, v47, v64
	v_pk_maximum3_f16 v16, v36, v48, v63
	v_pk_maximum3_f16 v17, v37, v49, v62
	v_pk_maximum3_f16 v86, v69, v81, v85
	v_pk_maximum3_f16 v87, v68, v80, v84
	v_pk_maximum3_f16 v88, v67, v79, v83
	v_pk_maximum3_f16 v89, v66, v78, v82
	v_pk_fma_f16 v33, v145, v157, v33
	v_pk_fma_f16 v32, v144, v156, v32
	v_pk_fma_f16 v31, v143, v155, v31
	v_pk_fma_f16 v30, v142, v154, v30
	v_pk_fma_f16 v45, v153, v157, v45
	v_pk_fma_f16 v44, v152, v156, v44
	v_pk_fma_f16 v43, v151, v155, v43
	v_pk_fma_f16 v42, v150, v154, v42
	v_pk_maximum3_f16 v95, v31, v43, v59
	v_pk_maximum3_f16 v96, v32, v44, v60
	v_pk_maximum3_f16 v97, v33, v45, v61
	v_pk_maximum3_f16 v94, v30, v42, v58
	v_pk_maximum3_f16 v15, v15, v87, v95
	v_pk_maximum3_f16 v16, v16, v88, v96
	v_pk_maximum3_f16 v17, v17, v89, v97
	v_pk_maximum3_f16 v14, v14, v86, v94
	v_xor_b32_e32 v86, 0x80008000, v17
	v_xor_b32_e32 v87, 0x80008000, v16
	v_xor_b32_e32 v88, 0x80008000, v15
	v_xor_b32_e32 v89, 0x80008000, v14
	v_pk_add_f16 v14, v34, v89
	v_pk_add_f16 v15, v35, v88
	v_pk_add_f16 v16, v36, v87
	v_pk_add_f16 v17, v37, v86
	v_exp_f16_sdwa v34, v14 dst_sel:WORD_0 dst_unused:UNUSED_PAD src0_sel:WORD_0
	v_exp_f16_sdwa v35, v15 dst_sel:WORD_0 dst_unused:UNUSED_PAD src0_sel:WORD_0
	v_exp_f16_sdwa v36, v16 dst_sel:WORD_0 dst_unused:UNUSED_PAD src0_sel:WORD_0
	v_exp_f16_sdwa v37, v17 dst_sel:WORD_0 dst_unused:UNUSED_PAD src0_sel:WORD_0
	v_exp_f16_sdwa v34, v14 dst_sel:WORD_1 dst_unused:UNUSED_PRESERVE src0_sel:WORD_1
	v_exp_f16_sdwa v35, v15 dst_sel:WORD_1 dst_unused:UNUSED_PRESERVE src0_sel:WORD_1
	v_exp_f16_sdwa v36, v16 dst_sel:WORD_1 dst_unused:UNUSED_PRESERVE src0_sel:WORD_1
	v_exp_f16_sdwa v37, v17 dst_sel:WORD_1 dst_unused:UNUSED_PRESERVE src0_sel:WORD_1
	v_pk_add_f16 v14, v34, 0
	v_pk_add_f16 v15, v35, 0
	v_pk_add_f16 v16, v36, 0
	v_pk_add_f16 v17, v37, 0
	v_pk_fma_f16 v18, v18, v34, 0
	v_pk_fma_f16 v19, v19, v35, 0
	v_pk_fma_f16 v20, v20, v36, 0
	v_pk_fma_f16 v21, v21, v37, 0
	v_pk_add_f16 v34, v46, v89
	v_pk_add_f16 v35, v47, v88
	v_pk_add_f16 v36, v48, v87
	v_pk_add_f16 v37, v49, v86
	v_exp_f16_sdwa v46, v34 dst_sel:WORD_0 dst_unused:UNUSED_PAD src0_sel:WORD_0
	v_exp_f16_sdwa v47, v35 dst_sel:WORD_0 dst_unused:UNUSED_PAD src0_sel:WORD_0
	v_exp_f16_sdwa v48, v36 dst_sel:WORD_0 dst_unused:UNUSED_PAD src0_sel:WORD_0
	v_exp_f16_sdwa v49, v37 dst_sel:WORD_0 dst_unused:UNUSED_PAD src0_sel:WORD_0
	v_exp_f16_sdwa v46, v34 dst_sel:WORD_1 dst_unused:UNUSED_PRESERVE src0_sel:WORD_1
	v_exp_f16_sdwa v47, v35 dst_sel:WORD_1 dst_unused:UNUSED_PRESERVE src0_sel:WORD_1
	v_exp_f16_sdwa v48, v36 dst_sel:WORD_1 dst_unused:UNUSED_PRESERVE src0_sel:WORD_1
	v_exp_f16_sdwa v49, v37 dst_sel:WORD_1 dst_unused:UNUSED_PRESERVE src0_sel:WORD_1
	s_nop 0
	v_pk_add_f16 v17, v17, v49
	v_pk_add_f16 v16, v16, v48
	v_pk_add_f16 v15, v15, v47
	v_pk_add_f16 v14, v14, v46
	v_pk_fma_f16 v21, v25, v49, v21
	v_pk_fma_f16 v20, v24, v48, v20
	v_pk_fma_f16 v19, v23, v47, v19
	v_pk_fma_f16 v18, v22, v46, v18
	v_pk_add_f16 v22, v65, v89
	v_pk_add_f16 v23, v64, v88
	v_pk_add_f16 v24, v63, v87
	v_pk_add_f16 v25, v62, v86
	v_exp_f16_sdwa v34, v22 dst_sel:WORD_0 dst_unused:UNUSED_PAD src0_sel:WORD_0
	v_exp_f16_sdwa v35, v23 dst_sel:WORD_0 dst_unused:UNUSED_PAD src0_sel:WORD_0
	v_exp_f16_sdwa v36, v24 dst_sel:WORD_0 dst_unused:UNUSED_PAD src0_sel:WORD_0
	v_exp_f16_sdwa v37, v25 dst_sel:WORD_0 dst_unused:UNUSED_PAD src0_sel:WORD_0
	v_exp_f16_sdwa v34, v22 dst_sel:WORD_1 dst_unused:UNUSED_PRESERVE src0_sel:WORD_1
	v_exp_f16_sdwa v35, v23 dst_sel:WORD_1 dst_unused:UNUSED_PRESERVE src0_sel:WORD_1
	v_exp_f16_sdwa v36, v24 dst_sel:WORD_1 dst_unused:UNUSED_PRESERVE src0_sel:WORD_1
	v_exp_f16_sdwa v37, v25 dst_sel:WORD_1 dst_unused:UNUSED_PRESERVE src0_sel:WORD_1
	v_pk_add_f16 v22, v69, v89
	v_pk_add_f16 v14, v14, v34
	v_pk_add_f16 v15, v15, v35
	v_pk_add_f16 v16, v16, v36
	v_pk_add_f16 v17, v17, v37
	v_pk_fma_f16 v18, v26, v34, v18
	v_pk_fma_f16 v19, v27, v35, v19
	v_pk_fma_f16 v20, v28, v36, v20
	v_pk_fma_f16 v21, v29, v37, v21
	v_pk_add_f16 v23, v68, v88
	v_pk_add_f16 v24, v67, v87
	v_pk_add_f16 v25, v66, v86
	v_exp_f16_sdwa v26, v22 dst_sel:WORD_0 dst_unused:UNUSED_PAD src0_sel:WORD_0
	v_exp_f16_sdwa v27, v23 dst_sel:WORD_0 dst_unused:UNUSED_PAD src0_sel:WORD_0
	v_exp_f16_sdwa v28, v24 dst_sel:WORD_0 dst_unused:UNUSED_PAD src0_sel:WORD_0
	v_exp_f16_sdwa v29, v25 dst_sel:WORD_0 dst_unused:UNUSED_PAD src0_sel:WORD_0
	v_exp_f16_sdwa v26, v22 dst_sel:WORD_1 dst_unused:UNUSED_PRESERVE src0_sel:WORD_1
	v_exp_f16_sdwa v27, v23 dst_sel:WORD_1 dst_unused:UNUSED_PRESERVE src0_sel:WORD_1
	v_exp_f16_sdwa v28, v24 dst_sel:WORD_1 dst_unused:UNUSED_PRESERVE src0_sel:WORD_1
	v_exp_f16_sdwa v29, v25 dst_sel:WORD_1 dst_unused:UNUSED_PRESERVE src0_sel:WORD_1
	v_pk_add_f16 v22, v81, v89
	v_pk_add_f16 v17, v17, v29
	v_pk_add_f16 v16, v16, v28
	v_pk_add_f16 v15, v15, v27
	v_pk_add_f16 v14, v14, v26
	v_pk_fma_f16 v21, v41, v29, v21
	v_pk_fma_f16 v20, v40, v28, v20
	v_pk_fma_f16 v19, v39, v27, v19
	v_pk_fma_f16 v18, v38, v26, v18
	v_pk_add_f16 v23, v80, v88
	v_pk_add_f16 v24, v79, v87
	v_pk_add_f16 v25, v78, v86
	v_exp_f16_sdwa v26, v22 dst_sel:WORD_0 dst_unused:UNUSED_PAD src0_sel:WORD_0
	v_exp_f16_sdwa v27, v23 dst_sel:WORD_0 dst_unused:UNUSED_PAD src0_sel:WORD_0
	v_exp_f16_sdwa v28, v24 dst_sel:WORD_0 dst_unused:UNUSED_PAD src0_sel:WORD_0
	v_exp_f16_sdwa v29, v25 dst_sel:WORD_0 dst_unused:UNUSED_PAD src0_sel:WORD_0
	v_exp_f16_sdwa v26, v22 dst_sel:WORD_1 dst_unused:UNUSED_PRESERVE src0_sel:WORD_1
	v_exp_f16_sdwa v27, v23 dst_sel:WORD_1 dst_unused:UNUSED_PRESERVE src0_sel:WORD_1
	v_exp_f16_sdwa v28, v24 dst_sel:WORD_1 dst_unused:UNUSED_PRESERVE src0_sel:WORD_1
	v_exp_f16_sdwa v29, v25 dst_sel:WORD_1 dst_unused:UNUSED_PRESERVE src0_sel:WORD_1
	v_pk_add_f16 v22, v85, v89
	v_pk_add_f16 v14, v14, v26
	v_pk_add_f16 v15, v15, v27
	v_pk_add_f16 v16, v16, v28
	v_pk_add_f16 v17, v17, v29
	v_pk_fma_f16 v18, v50, v26, v18
	v_pk_fma_f16 v19, v51, v27, v19
	v_pk_fma_f16 v20, v52, v28, v20
	v_pk_fma_f16 v21, v53, v29, v21
	v_pk_add_f16 v23, v84, v88
	v_pk_add_f16 v24, v83, v87
	v_pk_add_f16 v25, v82, v86
	v_exp_f16_sdwa v26, v22 dst_sel:WORD_0 dst_unused:UNUSED_PAD src0_sel:WORD_0
	v_exp_f16_sdwa v27, v23 dst_sel:WORD_0 dst_unused:UNUSED_PAD src0_sel:WORD_0
	v_exp_f16_sdwa v28, v24 dst_sel:WORD_0 dst_unused:UNUSED_PAD src0_sel:WORD_0
	v_exp_f16_sdwa v29, v25 dst_sel:WORD_0 dst_unused:UNUSED_PAD src0_sel:WORD_0
	v_exp_f16_sdwa v26, v22 dst_sel:WORD_1 dst_unused:UNUSED_PRESERVE src0_sel:WORD_1
	v_exp_f16_sdwa v27, v23 dst_sel:WORD_1 dst_unused:UNUSED_PRESERVE src0_sel:WORD_1
	v_exp_f16_sdwa v28, v24 dst_sel:WORD_1 dst_unused:UNUSED_PRESERVE src0_sel:WORD_1
	v_exp_f16_sdwa v29, v25 dst_sel:WORD_1 dst_unused:UNUSED_PRESERVE src0_sel:WORD_1
	v_pk_add_f16 v22, v30, v89
	v_pk_add_f16 v17, v17, v29
	v_pk_add_f16 v16, v16, v28
	v_pk_add_f16 v15, v15, v27
	v_pk_add_f16 v14, v14, v26
	v_pk_fma_f16 v21, v73, v29, v21
	v_pk_fma_f16 v20, v72, v28, v20
	v_pk_fma_f16 v19, v71, v27, v19
	v_pk_fma_f16 v18, v70, v26, v18
	v_pk_add_f16 v23, v31, v88
	v_pk_add_f16 v24, v32, v87
	v_pk_add_f16 v25, v33, v86
	v_exp_f16_sdwa v26, v22 dst_sel:WORD_0 dst_unused:UNUSED_PAD src0_sel:WORD_0
	v_exp_f16_sdwa v27, v23 dst_sel:WORD_0 dst_unused:UNUSED_PAD src0_sel:WORD_0
	v_exp_f16_sdwa v28, v24 dst_sel:WORD_0 dst_unused:UNUSED_PAD src0_sel:WORD_0
	v_exp_f16_sdwa v29, v25 dst_sel:WORD_0 dst_unused:UNUSED_PAD src0_sel:WORD_0
	v_exp_f16_sdwa v26, v22 dst_sel:WORD_1 dst_unused:UNUSED_PRESERVE src0_sel:WORD_1
	v_exp_f16_sdwa v27, v23 dst_sel:WORD_1 dst_unused:UNUSED_PRESERVE src0_sel:WORD_1
	v_exp_f16_sdwa v28, v24 dst_sel:WORD_1 dst_unused:UNUSED_PRESERVE src0_sel:WORD_1
	v_exp_f16_sdwa v29, v25 dst_sel:WORD_1 dst_unused:UNUSED_PRESERVE src0_sel:WORD_1
	v_pk_add_f16 v22, v42, v89
	v_pk_add_f16 v14, v14, v26
	v_pk_add_f16 v15, v15, v27
	v_pk_add_f16 v16, v16, v28
	v_pk_add_f16 v17, v17, v29
	v_pk_fma_f16 v18, v90, v26, v18
	v_pk_fma_f16 v19, v91, v27, v19
	v_pk_fma_f16 v20, v92, v28, v20
	v_pk_fma_f16 v21, v93, v29, v21
	v_pk_add_f16 v23, v43, v88
	v_pk_add_f16 v24, v44, v87
	v_pk_add_f16 v25, v45, v86
	v_exp_f16_sdwa v26, v22 dst_sel:WORD_0 dst_unused:UNUSED_PAD src0_sel:WORD_0
	v_exp_f16_sdwa v27, v23 dst_sel:WORD_0 dst_unused:UNUSED_PAD src0_sel:WORD_0
	v_exp_f16_sdwa v28, v24 dst_sel:WORD_0 dst_unused:UNUSED_PAD src0_sel:WORD_0
	v_exp_f16_sdwa v29, v25 dst_sel:WORD_0 dst_unused:UNUSED_PAD src0_sel:WORD_0
	v_exp_f16_sdwa v26, v22 dst_sel:WORD_1 dst_unused:UNUSED_PRESERVE src0_sel:WORD_1
	v_exp_f16_sdwa v27, v23 dst_sel:WORD_1 dst_unused:UNUSED_PRESERVE src0_sel:WORD_1
	v_exp_f16_sdwa v28, v24 dst_sel:WORD_1 dst_unused:UNUSED_PRESERVE src0_sel:WORD_1
	v_exp_f16_sdwa v29, v25 dst_sel:WORD_1 dst_unused:UNUSED_PRESERVE src0_sel:WORD_1
	v_pk_add_f16 v22, v58, v89
	v_pk_add_f16 v17, v17, v29
	v_pk_add_f16 v16, v16, v28
	v_pk_add_f16 v15, v15, v27
	v_pk_add_f16 v14, v14, v26
	v_pk_fma_f16 v21, v113, v29, v21
	v_pk_fma_f16 v20, v112, v28, v20
	v_pk_fma_f16 v19, v111, v27, v19
	v_pk_fma_f16 v18, v110, v26, v18
	v_pk_add_f16 v23, v59, v88
	v_pk_add_f16 v24, v60, v87
	v_pk_add_f16 v25, v61, v86
	v_exp_f16_sdwa v30, v22 dst_sel:WORD_0 dst_unused:UNUSED_PAD src0_sel:WORD_0
	v_exp_f16_sdwa v31, v23 dst_sel:WORD_0 dst_unused:UNUSED_PAD src0_sel:WORD_0
	v_exp_f16_sdwa v32, v24 dst_sel:WORD_0 dst_unused:UNUSED_PAD src0_sel:WORD_0
	v_exp_f16_sdwa v33, v25 dst_sel:WORD_0 dst_unused:UNUSED_PAD src0_sel:WORD_0
	v_exp_f16_sdwa v30, v22 dst_sel:WORD_1 dst_unused:UNUSED_PRESERVE src0_sel:WORD_1
	v_exp_f16_sdwa v31, v23 dst_sel:WORD_1 dst_unused:UNUSED_PRESERVE src0_sel:WORD_1
	v_exp_f16_sdwa v32, v24 dst_sel:WORD_1 dst_unused:UNUSED_PRESERVE src0_sel:WORD_1
	v_exp_f16_sdwa v33, v25 dst_sel:WORD_1 dst_unused:UNUSED_PRESERVE src0_sel:WORD_1
	s_nop 0
.LBB4_42:
	s_and_b64 vcc, exec, s[4:5]
	s_cbranch_vccz .LBB4_80
	global_load_dwordx3 v[146:148], v169, s[8:9]
	v_cmp_lt_u32_e64 s[64:65], 0, v199
	v_cmp_gt_u32_e64 s[66:67], 63, v199
	v_cmp_lt_u32_e64 s[68:69], 0, v180
	v_cmp_gt_u32_e64 s[70:71], 60, v180
	buffer_load_dwordx4 v[162:165], v200, s[36:39], 0 offen sc1
	s_and_b64 s[72:73], s[68:69], s[64:65]
	s_and_b64 s[74:75], s[68:69], s[66:67]
	s_and_b64 s[76:77], s[70:71], s[64:65]
	s_and_b64 s[78:79], s[70:71], s[66:67]
	v_add_u32_e32 v245, 0xfffe7c00, v200
	v_add_u32_e32 v246, 0xfffe8000, v200
	s_mov_b64 exec, s[72:73]
	buffer_load_dwordx4 v[114:117], v245, s[36:39], 0 offen
	buffer_load_dwordx4 v[74:77], v245, s[36:39], 0 offen offset:512
	s_mov_b64 exec, -1
	s_mov_b64 exec, s[68:69]
	buffer_load_dwordx4 v[130:133], v246, s[36:39], 0 offen offset:512
	buffer_load_dwordx4 v[98:101], v246, s[36:39], 0 offen offset:1024
	s_mov_b64 exec, -1
	s_mov_b64 exec, s[74:75]
	buffer_load_dwordx4 v[138:141], v246, s[36:39], 0 offen offset:2048
	buffer_load_dwordx4 v[118:121], v246, s[36:39], 0 offen offset:2560
	s_mov_b64 exec, -1
	v_add_u32_e32 v245, 0xfffffc00, v200
	s_mov_b64 exec, s[64:65]
	buffer_load_dwordx4 v[86:89], v245, s[36:39], 0 offen
	buffer_load_dwordx4 v[46:49], v245, s[36:39], 0 offen offset:512
	s_mov_b64 exec, -1
	buffer_load_dwordx4 v[110:113], v200, s[36:39], 0 offen offset:512
	buffer_load_dwordx4 v[66:69], v200, s[36:39], 0 offen offset:1024
	s_mov_b64 exec, s[66:67]
	buffer_load_dwordx4 v[126:129], v200, s[36:39], 0 offen offset:2048
	buffer_load_dwordx4 v[90:93], v200, s[36:39], 0 offen offset:2560
	s_mov_b64 exec, -1
	v_add_u32_e32 v245, 0x17c00, v200
	v_add_u32_e32 v246, 0x18000, v200
	s_mov_b64 exec, s[64:65]
	buffer_load_dwordx4 v[54:57], v245, s[36:39], 0 offen
	buffer_load_dwordx4 v[22:25], v245, s[36:39], 0 offen offset:512
	s_mov_b64 exec, -1
	buffer_load_dwordx4 v[70:73], v246, s[36:39], 0 offen offset:512
	buffer_load_dwordx4 v[34:37], v246, s[36:39], 0 offen offset:1024
	s_mov_b64 exec, s[66:67]
	buffer_load_dwordx4 v[94:97], v246, s[36:39], 0 offen offset:2048
	buffer_load_dwordx4 v[50:53], v246, s[36:39], 0 offen offset:2560
	s_mov_b64 exec, -1
	v_add_u32_e32 v245, 0x18000, v200
	buffer_load_dwordx4 v[154:157], v245, s[36:39], 0 offen sc1
	v_add_u32_e32 v246, 0x30000, v200
	buffer_load_dwordx4 v[150:153], v246, s[36:39], 0 offen sc1
	v_add_u32_e32 v245, 0x2fc00, v200
	v_add_u32_e32 v246, 0x30000, v200
	v_add_u32_e32 v247, 0x47c00, v200
	v_add_u32_e32 v248, 0x48000, v200
	v_add_u32_e32 v249, 0x5fc00, v200
	v_add_u32_e32 v250, 0x60000, v200
	s_waitcnt vmcnt(22)
	v_cvt_pk_f16_f32 v6, v2, v3
	v_cvt_pk_f16_f32 v2, v8, v9
	v_cvt_pk_f16_f32 v7, v4, v5
	v_cvt_pk_f16_f32 v3, v10, v11
	v_cvt_pk_f16_f32 v8, v210, v211
	v_cvt_pk_f16_f32 v4, v214, v215
	v_cvt_pk_f16_f32 v9, v212, v213
	v_cvt_pk_f16_f32 v5, v216, v217
	s_not_b64 exec, s[72:73]
	s_cbranch_execz .Lmyf_C2_0
	v_mov_b32_e32 v114, v6
	v_mov_b32_e32 v115, v7
	v_mov_b32_e32 v116, v8
	v_mov_b32_e32 v117, v9
	v_mov_b32_e32 v74, v2
	v_mov_b32_e32 v75, v3
	v_mov_b32_e32 v76, v4
	v_mov_b32_e32 v77, v5

.Lmyf_C2_7:
	s_mov_b64 exec, -1
	s_waitcnt vmcnt(21)
	v_cvt_f16_f32_e32 v158, v147
	v_cvt_f16_f32_e32 v160, v146
	v_cvt_f16_f32_e32 v159, v148
	v_add_u32_e32 v251, 0x48000, v200
	buffer_load_dwordx4 v[146:149], v251, s[36:39], 0 offen sc1
	s_waitcnt vmcnt(3)
	v_pk_mul_f16 v161, v160, v162 op_sel_hi:[0,1]
	v_pk_mul_f16 v204, v160, v165 op_sel_hi:[0,1]
	v_pk_mul_f16 v208, v158, v165 op_sel_hi:[0,1]
	v_pk_mul_f16 v212, v159, v165 op_sel_hi:[0,1]
	v_pk_mul_f16 v202, v160, v163 op_sel_hi:[0,1]
	v_pk_mul_f16 v203, v160, v164 op_sel_hi:[0,1]
	v_pk_mul_f16 v205, v158, v162 op_sel_hi:[0,1]
	s_mov_b64 exec, s[64:65]
	buffer_load_dwordx4 v[26:29], v245, s[36:39], 0 offen
	buffer_load_dwordx4 v[10:13], v245, s[36:39], 0 offen offset:512
	s_mov_b64 exec, -1
	v_pk_mul_f16 v206, v158, v163 op_sel_hi:[0,1]
	v_pk_mul_f16 v207, v158, v164 op_sel_hi:[0,1]
	v_pk_mul_f16 v209, v159, v162 op_sel_hi:[0,1]
	v_pk_mul_f16 v210, v159, v163 op_sel_hi:[0,1]
	v_pk_mul_f16 v211, v159, v164 op_sel_hi:[0,1]
	v_pk_fma_f16 v117, v117, v165, v204
	v_pk_fma_f16 v114, v114, v162, v161
	v_pk_fma_f16 v133, v133, v165, v204
	v_pk_fma_f16 v130, v130, v162, v161
	v_pk_fma_f16 v141, v141, v165, v204
	v_pk_fma_f16 v138, v138, v162, v161
	v_pk_fma_f16 v161, v89, v165, v208
	v_pk_fma_f16 v213, v113, v165, v208
	buffer_load_dwordx4 v[38:41], v246, s[36:39], 0 offen offset:512
	buffer_load_dwordx4 v[14:17], v246, s[36:39], 0 offen offset:1024
	v_pk_fma_f16 v208, v129, v165, v208
	v_pk_fma_f16 v217, v57, v165, v212
	v_pk_fma_f16 v221, v73, v165, v212
	v_pk_fma_f16 v165, v97, v165, v212
	v_pk_maximum3_f16 v212, v117, v133, v141
	v_pk_fma_f16 v116, v116, v164, v203
	v_pk_fma_f16 v115, v115, v163, v202
	v_pk_fma_f16 v132, v132, v164, v203
	v_pk_fma_f16 v131, v131, v163, v202
	v_pk_fma_f16 v140, v140, v164, v203
	v_pk_fma_f16 v139, v139, v163, v202
	v_pk_fma_f16 v202, v88, v164, v207
	v_pk_fma_f16 v203, v87, v163, v206
	v_pk_fma_f16 v204, v86, v162, v205
	v_pk_fma_f16 v214, v112, v164, v207
	v_pk_fma_f16 v215, v111, v163, v206
	s_mov_b64 exec, s[66:67]
	buffer_load_dwordx4 v[58:61], v246, s[36:39], 0 offen offset:2048
	buffer_load_dwordx4 v[18:21], v246, s[36:39], 0 offen offset:2560
	s_mov_b64 exec, -1
	v_pk_fma_f16 v216, v110, v162, v205
	v_pk_fma_f16 v207, v128, v164, v207
	v_pk_fma_f16 v206, v127, v163, v206
	v_pk_fma_f16 v205, v126, v162, v205
	v_pk_fma_f16 v218, v56, v164, v211
	v_pk_fma_f16 v219, v55, v163, v210
	v_pk_fma_f16 v220, v54, v162, v209
	v_pk_fma_f16 v222, v72, v164, v211
	v_pk_fma_f16 v223, v71, v163, v210
	v_pk_fma_f16 v224, v70, v162, v209
	v_pk_fma_f16 v164, v96, v164, v211
	v_pk_fma_f16 v163, v95, v163, v210
	v_pk_fma_f16 v162, v94, v162, v209
	v_pk_maximum3_f16 v209, v114, v130, v138
	v_pk_maximum3_f16 v210, v115, v131, v139
	v_pk_maximum3_f16 v211, v116, v132, v140
	v_pk_maximum3_f16 v228, v161, v213, v208
	v_pk_maximum3_f16 v232, v217, v221, v165
	v_pk_maximum3_f16 v225, v204, v216, v205
	v_pk_maximum3_f16 v226, v203, v215, v206
	v_pk_maximum3_f16 v227, v202, v214, v207
	v_pk_maximum3_f16 v229, v220, v224, v162
	v_pk_maximum3_f16 v230, v219, v223, v163
	v_pk_maximum3_f16 v212, v212, v228, v232
	v_pk_maximum3_f16 v231, v218, v222, v164
	v_pk_maximum3_f16 v209, v209, v225, v229
	v_pk_maximum3_f16 v210, v210, v226, v230
	v_pk_maximum3_f16 v211, v211, v227, v231
	v_pk_add_f16 v117, v117, v212 neg_lo:[0,1] neg_hi:[0,1]
	s_mov_b64 exec, s[64:65]
	buffer_load_dwordx4 v[78:81], v247, s[36:39], 0 offen
	buffer_load_dwordx4 v[30:33], v247, s[36:39], 0 offen offset:512
	s_mov_b64 exec, -1
	v_pk_add_f16 v114, v114, v209 neg_lo:[0,1] neg_hi:[0,1]
	v_pk_add_f16 v115, v115, v210 neg_lo:[0,1] neg_hi:[0,1]
	v_pk_add_f16 v116, v116, v211 neg_lo:[0,1] neg_hi:[0,1]
	v_pk_add_f16 v130, v130, v209 neg_lo:[0,1] neg_hi:[0,1]
	v_exp_f16_sdwa v225, v114 dst_sel:WORD_0 dst_unused:UNUSED_PAD src0_sel:WORD_0
	v_exp_f16_sdwa v226, v115 dst_sel:WORD_0 dst_unused:UNUSED_PAD src0_sel:WORD_0
	v_exp_f16_sdwa v227, v116 dst_sel:WORD_0 dst_unused:UNUSED_PAD src0_sel:WORD_0
	v_exp_f16_sdwa v228, v117 dst_sel:WORD_0 dst_unused:UNUSED_PAD src0_sel:WORD_0
	v_exp_f16_sdwa v225, v114 dst_sel:WORD_1 dst_unused:UNUSED_PRESERVE src0_sel:WORD_1
	v_exp_f16_sdwa v226, v115 dst_sel:WORD_1 dst_unused:UNUSED_PRESERVE src0_sel:WORD_1
	v_exp_f16_sdwa v227, v116 dst_sel:WORD_1 dst_unused:UNUSED_PRESERVE src0_sel:WORD_1
	v_exp_f16_sdwa v228, v117 dst_sel:WORD_1 dst_unused:UNUSED_PRESERVE src0_sel:WORD_1
	v_pk_add_f16 v131, v131, v210 neg_lo:[0,1] neg_hi:[0,1]
	v_pk_add_f16 v117, v225, 0
	v_pk_fma_f16 v77, v77, v228, 0
	v_pk_add_f16 v114, v228, 0
	v_pk_add_f16 v115, v227, 0
	v_pk_add_f16 v116, v226, 0
	v_pk_fma_f16 v76, v76, v227, 0
	v_pk_fma_f16 v75, v75, v226, 0
	v_pk_fma_f16 v74, v74, v225, 0
	v_pk_add_f16 v132, v132, v211 neg_lo:[0,1] neg_hi:[0,1]
	buffer_load_dwordx4 v[106:109], v248, s[36:39], 0 offen offset:512
	buffer_load_dwordx4 v[42:45], v248, s[36:39], 0 offen offset:1024
	v_pk_add_f16 v133, v133, v212 neg_lo:[0,1] neg_hi:[0,1]
	v_exp_f16_sdwa v225, v130 dst_sel:WORD_0 dst_unused:UNUSED_PAD src0_sel:WORD_0
	v_exp_f16_sdwa v226, v131 dst_sel:WORD_0 dst_unused:UNUSED_PAD src0_sel:WORD_0
	v_exp_f16_sdwa v227, v132 dst_sel:WORD_0 dst_unused:UNUSED_PAD src0_sel:WORD_0
	v_exp_f16_sdwa v228, v133 dst_sel:WORD_0 dst_unused:UNUSED_PAD src0_sel:WORD_0
	v_exp_f16_sdwa v225, v130 dst_sel:WORD_1 dst_unused:UNUSED_PRESERVE src0_sel:WORD_1
	v_exp_f16_sdwa v226, v131 dst_sel:WORD_1 dst_unused:UNUSED_PRESERVE src0_sel:WORD_1
	v_exp_f16_sdwa v227, v132 dst_sel:WORD_1 dst_unused:UNUSED_PRESERVE src0_sel:WORD_1
	v_exp_f16_sdwa v228, v133 dst_sel:WORD_1 dst_unused:UNUSED_PRESERVE src0_sel:WORD_1
	v_pk_add_f16 v117, v117, v225
	v_pk_fma_f16 v77, v101, v228, v77
	v_pk_add_f16 v101, v141, v212 neg_lo:[0,1] neg_hi:[0,1]
	v_pk_add_f16 v116, v116, v226
	v_pk_add_f16 v115, v115, v227
	v_pk_add_f16 v114, v114, v228
	v_pk_fma_f16 v74, v98, v225, v74
	v_pk_fma_f16 v75, v99, v226, v75
	v_pk_fma_f16 v76, v100, v227, v76
	v_pk_add_f16 v98, v138, v209 neg_lo:[0,1] neg_hi:[0,1]
	v_pk_add_f16 v99, v139, v210 neg_lo:[0,1] neg_hi:[0,1]
	v_pk_add_f16 v100, v140, v211 neg_lo:[0,1] neg_hi:[0,1]
	v_exp_f16_sdwa v130, v98 dst_sel:WORD_0 dst_unused:UNUSED_PAD src0_sel:WORD_0
	v_exp_f16_sdwa v131, v99 dst_sel:WORD_0 dst_unused:UNUSED_PAD src0_sel:WORD_0
	v_exp_f16_sdwa v132, v100 dst_sel:WORD_0 dst_unused:UNUSED_PAD src0_sel:WORD_0
	v_exp_f16_sdwa v133, v101 dst_sel:WORD_0 dst_unused:UNUSED_PAD src0_sel:WORD_0
	v_exp_f16_sdwa v130, v98 dst_sel:WORD_1 dst_unused:UNUSED_PRESERVE src0_sel:WORD_1
	v_exp_f16_sdwa v131, v99 dst_sel:WORD_1 dst_unused:UNUSED_PRESERVE src0_sel:WORD_1
	v_exp_f16_sdwa v132, v100 dst_sel:WORD_1 dst_unused:UNUSED_PRESERVE src0_sel:WORD_1
	v_exp_f16_sdwa v133, v101 dst_sel:WORD_1 dst_unused:UNUSED_PRESERVE src0_sel:WORD_1
	v_pk_add_f16 v101, v117, v130
	v_pk_add_f16 v98, v114, v133
	s_mov_b64 exec, s[66:67]
	buffer_load_dwordx4 v[122:125], v248, s[36:39], 0 offen offset:2048
	buffer_load_dwordx4 v[62:65], v248, s[36:39], 0 offen offset:2560
	s_mov_b64 exec, -1
	v_pk_add_f16 v99, v115, v132
	v_pk_add_f16 v100, v116, v131
	v_pk_fma_f16 v77, v121, v133, v77
	v_pk_fma_f16 v76, v120, v132, v76
	v_pk_fma_f16 v75, v119, v131, v75
	v_pk_fma_f16 v74, v118, v130, v74
	v_pk_add_f16 v114, v204, v209 neg_lo:[0,1] neg_hi:[0,1]
	v_pk_add_f16 v115, v203, v210 neg_lo:[0,1] neg_hi:[0,1]
	v_pk_add_f16 v116, v202, v211 neg_lo:[0,1] neg_hi:[0,1]
	v_pk_add_f16 v117, v161, v212 neg_lo:[0,1] neg_hi:[0,1]
	v_exp_f16_sdwa v118, v114 dst_sel:WORD_0 dst_unused:UNUSED_PAD src0_sel:WORD_0
	v_exp_f16_sdwa v119, v115 dst_sel:WORD_0 dst_unused:UNUSED_PAD src0_sel:WORD_0
	v_exp_f16_sdwa v120, v116 dst_sel:WORD_0 dst_unused:UNUSED_PAD src0_sel:WORD_0
	v_exp_f16_sdwa v121, v117 dst_sel:WORD_0 dst_unused:UNUSED_PAD src0_sel:WORD_0
	v_exp_f16_sdwa v118, v114 dst_sel:WORD_1 dst_unused:UNUSED_PRESERVE src0_sel:WORD_1
	v_exp_f16_sdwa v119, v115 dst_sel:WORD_1 dst_unused:UNUSED_PRESERVE src0_sel:WORD_1
	v_exp_f16_sdwa v120, v116 dst_sel:WORD_1 dst_unused:UNUSED_PRESERVE src0_sel:WORD_1
	v_exp_f16_sdwa v121, v117 dst_sel:WORD_1 dst_unused:UNUSED_PRESERVE src0_sel:WORD_1
	v_pk_add_f16 v114, v216, v209 neg_lo:[0,1] neg_hi:[0,1]
	v_pk_add_f16 v101, v101, v118
	v_pk_add_f16 v100, v100, v119
	v_pk_add_f16 v99, v99, v120
	s_mov_b64 exec, s[76:77]
	buffer_load_dwordx4 v[134:137], v249, s[36:39], 0 offen
	buffer_load_dwordx4 v[82:85], v249, s[36:39], 0 offen offset:512
	s_mov_b64 exec, -1
	v_pk_add_f16 v98, v98, v121
	v_pk_fma_f16 v74, v46, v118, v74
	v_pk_fma_f16 v75, v47, v119, v75
	v_pk_fma_f16 v76, v48, v120, v76
	v_pk_fma_f16 v77, v49, v121, v77
	v_pk_add_f16 v115, v215, v210 neg_lo:[0,1] neg_hi:[0,1]
	v_pk_add_f16 v116, v214, v211 neg_lo:[0,1] neg_hi:[0,1]
	v_pk_add_f16 v117, v213, v212 neg_lo:[0,1] neg_hi:[0,1]
	v_exp_f16_sdwa v118, v114 dst_sel:WORD_0 dst_unused:UNUSED_PAD src0_sel:WORD_0
	v_exp_f16_sdwa v119, v115 dst_sel:WORD_0 dst_unused:UNUSED_PAD src0_sel:WORD_0
	v_exp_f16_sdwa v120, v116 dst_sel:WORD_0 dst_unused:UNUSED_PAD src0_sel:WORD_0
	v_exp_f16_sdwa v121, v117 dst_sel:WORD_0 dst_unused:UNUSED_PAD src0_sel:WORD_0
	v_exp_f16_sdwa v118, v114 dst_sel:WORD_1 dst_unused:UNUSED_PRESERVE src0_sel:WORD_1
	v_exp_f16_sdwa v119, v115 dst_sel:WORD_1 dst_unused:UNUSED_PRESERVE src0_sel:WORD_1
	v_exp_f16_sdwa v120, v116 dst_sel:WORD_1 dst_unused:UNUSED_PRESERVE src0_sel:WORD_1
	v_exp_f16_sdwa v121, v117 dst_sel:WORD_1 dst_unused:UNUSED_PRESERVE src0_sel:WORD_1
	v_pk_add_f16 v114, v205, v209 neg_lo:[0,1] neg_hi:[0,1]
	v_pk_add_f16 v101, v101, v118
	v_pk_add_f16 v98, v98, v121
	v_pk_add_f16 v99, v99, v120
	v_pk_add_f16 v100, v100, v119
	v_pk_fma_f16 v77, v69, v121, v77
	v_pk_fma_f16 v76, v68, v120, v76
	s_mov_b64 exec, s[70:71]
	buffer_load_dwordx4 v[142:145], v250, s[36:39], 0 offen offset:512
	buffer_load_dwordx4 v[102:105], v250, s[36:39], 0 offen offset:1024
	s_mov_b64 exec, -1
	v_pk_fma_f16 v75, v67, v119, v75
	v_pk_fma_f16 v74, v66, v118, v74
	v_pk_add_f16 v115, v206, v210 neg_lo:[0,1] neg_hi:[0,1]
	v_pk_add_f16 v116, v207, v211 neg_lo:[0,1] neg_hi:[0,1]
	v_pk_add_f16 v117, v208, v212 neg_lo:[0,1] neg_hi:[0,1]
	v_exp_f16_sdwa v118, v114 dst_sel:WORD_0 dst_unused:UNUSED_PAD src0_sel:WORD_0
	v_exp_f16_sdwa v119, v115 dst_sel:WORD_0 dst_unused:UNUSED_PAD src0_sel:WORD_0
	v_exp_f16_sdwa v120, v116 dst_sel:WORD_0 dst_unused:UNUSED_PAD src0_sel:WORD_0
	v_exp_f16_sdwa v121, v117 dst_sel:WORD_0 dst_unused:UNUSED_PAD src0_sel:WORD_0
	v_exp_f16_sdwa v118, v114 dst_sel:WORD_1 dst_unused:UNUSED_PRESERVE src0_sel:WORD_1
	v_exp_f16_sdwa v119, v115 dst_sel:WORD_1 dst_unused:UNUSED_PRESERVE src0_sel:WORD_1
	v_exp_f16_sdwa v120, v116 dst_sel:WORD_1 dst_unused:UNUSED_PRESERVE src0_sel:WORD_1
	v_exp_f16_sdwa v121, v117 dst_sel:WORD_1 dst_unused:UNUSED_PRESERVE src0_sel:WORD_1
	v_pk_add_f16 v114, v220, v209 neg_lo:[0,1] neg_hi:[0,1]
	v_pk_add_f16 v101, v101, v118
	v_pk_add_f16 v100, v100, v119
	v_pk_add_f16 v99, v99, v120
	v_pk_add_f16 v98, v98, v121
	v_pk_fma_f16 v74, v90, v118, v74
	v_pk_fma_f16 v75, v91, v119, v75
	v_pk_fma_f16 v76, v92, v120, v76
	v_pk_fma_f16 v77, v93, v121, v77
	s_mov_b64 exec, s[78:79]
	buffer_load_dwordx4 v[6:9], v250, s[36:39], 0 offen offset:2048
	buffer_load_dwordx4 v[2:5], v250, s[36:39], 0 offen offset:2560
	s_mov_b64 exec, -1
	v_pk_add_f16 v115, v219, v210 neg_lo:[0,1] neg_hi:[0,1]
	v_pk_add_f16 v116, v218, v211 neg_lo:[0,1] neg_hi:[0,1]
	v_pk_add_f16 v117, v217, v212 neg_lo:[0,1] neg_hi:[0,1]
	v_exp_f16_sdwa v118, v114 dst_sel:WORD_0 dst_unused:UNUSED_PAD src0_sel:WORD_0
	v_exp_f16_sdwa v119, v115 dst_sel:WORD_0 dst_unused:UNUSED_PAD src0_sel:WORD_0
	v_exp_f16_sdwa v120, v116 dst_sel:WORD_0 dst_unused:UNUSED_PAD src0_sel:WORD_0
	v_exp_f16_sdwa v121, v117 dst_sel:WORD_0 dst_unused:UNUSED_PAD src0_sel:WORD_0
	v_exp_f16_sdwa v118, v114 dst_sel:WORD_1 dst_unused:UNUSED_PRESERVE src0_sel:WORD_1
	v_exp_f16_sdwa v119, v115 dst_sel:WORD_1 dst_unused:UNUSED_PRESERVE src0_sel:WORD_1
	v_exp_f16_sdwa v120, v116 dst_sel:WORD_1 dst_unused:UNUSED_PRESERVE src0_sel:WORD_1
	v_exp_f16_sdwa v121, v117 dst_sel:WORD_1 dst_unused:UNUSED_PRESERVE src0_sel:WORD_1
	v_pk_add_f16 v114, v224, v209 neg_lo:[0,1] neg_hi:[0,1]
	v_pk_add_f16 v101, v101, v118
	v_pk_add_f16 v98, v98, v121
	v_pk_add_f16 v99, v99, v120
	v_pk_add_f16 v100, v100, v119
	v_pk_fma_f16 v77, v25, v121, v77
	v_pk_fma_f16 v76, v24, v120, v76
	v_pk_fma_f16 v75, v23, v119, v75
	v_pk_fma_f16 v74, v22, v118, v74
	v_pk_add_f16 v115, v223, v210 neg_lo:[0,1] neg_hi:[0,1]
	v_pk_add_f16 v116, v222, v211 neg_lo:[0,1] neg_hi:[0,1]
	v_pk_add_f16 v117, v221, v212 neg_lo:[0,1] neg_hi:[0,1]
	v_exp_f16_sdwa v118, v114 dst_sel:WORD_0 dst_unused:UNUSED_PAD src0_sel:WORD_0
	v_exp_f16_sdwa v119, v115 dst_sel:WORD_0 dst_unused:UNUSED_PAD src0_sel:WORD_0
	v_exp_f16_sdwa v120, v116 dst_sel:WORD_0 dst_unused:UNUSED_PAD src0_sel:WORD_0
	v_exp_f16_sdwa v121, v117 dst_sel:WORD_0 dst_unused:UNUSED_PAD src0_sel:WORD_0
	v_exp_f16_sdwa v118, v114 dst_sel:WORD_1 dst_unused:UNUSED_PRESERVE src0_sel:WORD_1
	v_exp_f16_sdwa v119, v115 dst_sel:WORD_1 dst_unused:UNUSED_PRESERVE src0_sel:WORD_1
	v_exp_f16_sdwa v120, v116 dst_sel:WORD_1 dst_unused:UNUSED_PRESERVE src0_sel:WORD_1
	v_exp_f16_sdwa v121, v117 dst_sel:WORD_1 dst_unused:UNUSED_PRESERVE src0_sel:WORD_1
	v_pk_add_f16 v114, v162, v209 neg_lo:[0,1] neg_hi:[0,1]
	v_pk_add_f16 v101, v101, v118
	v_pk_add_f16 v100, v100, v119
	v_pk_add_f16 v99, v99, v120
	v_pk_add_f16 v98, v98, v121
	v_pk_fma_f16 v74, v34, v118, v74
	v_pk_fma_f16 v75, v35, v119, v75
	v_pk_fma_f16 v76, v36, v120, v76
	v_pk_fma_f16 v77, v37, v121, v77
	v_pk_add_f16 v115, v163, v210 neg_lo:[0,1] neg_hi:[0,1]
	v_pk_add_f16 v116, v164, v211 neg_lo:[0,1] neg_hi:[0,1]
	v_pk_add_f16 v117, v165, v212 neg_lo:[0,1] neg_hi:[0,1]
	v_exp_f16_sdwa v118, v114 dst_sel:WORD_0 dst_unused:UNUSED_PAD src0_sel:WORD_0
	v_exp_f16_sdwa v119, v115 dst_sel:WORD_0 dst_unused:UNUSED_PAD src0_sel:WORD_0
	v_exp_f16_sdwa v120, v116 dst_sel:WORD_0 dst_unused:UNUSED_PAD src0_sel:WORD_0
	v_exp_f16_sdwa v121, v117 dst_sel:WORD_0 dst_unused:UNUSED_PAD src0_sel:WORD_0
	v_exp_f16_sdwa v118, v114 dst_sel:WORD_1 dst_unused:UNUSED_PRESERVE src0_sel:WORD_1
	v_exp_f16_sdwa v119, v115 dst_sel:WORD_1 dst_unused:UNUSED_PRESERVE src0_sel:WORD_1
	v_exp_f16_sdwa v120, v116 dst_sel:WORD_1 dst_unused:UNUSED_PRESERVE src0_sel:WORD_1
	v_exp_f16_sdwa v121, v117 dst_sel:WORD_1 dst_unused:UNUSED_PRESERVE src0_sel:WORD_1
	v_pk_add_f16 v101, v101, v118
	v_pk_add_f16 v100, v100, v119
	v_rcp_f16_e32 v114, v101
	v_rcp_f16_sdwa v101, v101 dst_sel:DWORD dst_unused:UNUSED_PAD src0_sel:WORD_1
	v_pk_add_f16 v99, v99, v120
	v_rcp_f16_e32 v115, v100
	v_rcp_f16_sdwa v100, v100 dst_sel:DWORD dst_unused:UNUSED_PAD src0_sel:WORD_1
	v_pk_add_f16 v98, v98, v121
	v_rcp_f16_e32 v116, v99
	v_rcp_f16_sdwa v99, v99 dst_sel:DWORD dst_unused:UNUSED_PAD src0_sel:WORD_1
	v_rcp_f16_e32 v117, v98
	v_rcp_f16_sdwa v98, v98 dst_sel:DWORD dst_unused:UNUSED_PAD src0_sel:WORD_1
	v_pk_fma_f16 v74, v50, v118, v74
	v_pack_b32_f16 v101, v114, v101
	v_pk_fma_f16 v75, v51, v119, v75
	v_pk_mul_f16 v138, v74, v101
	v_pack_b32_f16 v74, v115, v100
	v_pk_fma_f16 v76, v52, v120, v76
	v_pk_mul_f16 v139, v75, v74
	v_pack_b32_f16 v74, v116, v99
	v_pk_fma_f16 v77, v53, v121, v77
	v_pk_mul_f16 v140, v76, v74
	v_pack_b32_f16 v74, v117, v98
	v_pk_mul_f16 v141, v77, v74
	s_waitcnt vmcnt(12)
	v_pk_mul_f16 v74, v160, v154 op_sel_hi:[0,1]
	v_pk_mul_f16 v77, v160, v157 op_sel_hi:[0,1]
	v_pk_mul_f16 v101, v158, v157 op_sel_hi:[0,1]
	v_pk_mul_f16 v117, v159, v157 op_sel_hi:[0,1]
	v_pk_mul_f16 v75, v160, v155 op_sel_hi:[0,1]
	v_pk_mul_f16 v76, v160, v156 op_sel_hi:[0,1]
	v_pk_mul_f16 v98, v158, v154 op_sel_hi:[0,1]
	v_pk_mul_f16 v99, v158, v155 op_sel_hi:[0,1]
	v_pk_mul_f16 v100, v158, v156 op_sel_hi:[0,1]
	v_pk_mul_f16 v114, v159, v154 op_sel_hi:[0,1]
	v_pk_mul_f16 v115, v159, v155 op_sel_hi:[0,1]
	v_pk_mul_f16 v116, v159, v156 op_sel_hi:[0,1]
	v_pk_fma_f16 v89, v89, v157, v77
	v_pk_fma_f16 v86, v86, v154, v74
	v_pk_fma_f16 v113, v113, v157, v77
	v_pk_fma_f16 v110, v110, v154, v74
	v_pk_fma_f16 v77, v129, v157, v77
	v_pk_fma_f16 v74, v126, v154, v74
	v_pk_fma_f16 v118, v57, v157, v101
	v_pk_fma_f16 v126, v73, v157, v101
	v_pk_fma_f16 v101, v97, v157, v101
	v_pk_fma_f16 v130, v29, v157, v117
	v_pk_fma_f16 v161, v41, v157, v117
	v_pk_fma_f16 v117, v61, v157, v117
	v_pk_maximum3_f16 v157, v89, v113, v77
	v_pk_fma_f16 v88, v88, v156, v76
	v_pk_fma_f16 v87, v87, v155, v75
	v_pk_fma_f16 v112, v112, v156, v76
	v_pk_fma_f16 v111, v111, v155, v75
	v_pk_fma_f16 v76, v128, v156, v76
	v_pk_fma_f16 v75, v127, v155, v75
	v_pk_fma_f16 v119, v56, v156, v100
	v_pk_fma_f16 v120, v55, v155, v99
	v_pk_fma_f16 v121, v54, v154, v98
	v_pk_fma_f16 v127, v72, v156, v100
	v_pk_fma_f16 v128, v71, v155, v99
	v_pk_fma_f16 v129, v70, v154, v98
	v_pk_fma_f16 v100, v96, v156, v100
	v_pk_fma_f16 v99, v95, v155, v99
	v_pk_fma_f16 v98, v94, v154, v98
	v_pk_fma_f16 v131, v28, v156, v116
	v_pk_fma_f16 v132, v27, v155, v115
	v_pk_fma_f16 v133, v26, v154, v114
	v_pk_fma_f16 v162, v40, v156, v116
	v_pk_fma_f16 v163, v39, v155, v115
	v_pk_fma_f16 v164, v38, v154, v114
	v_pk_fma_f16 v116, v60, v156, v116
	v_pk_fma_f16 v115, v59, v155, v115
	v_pk_fma_f16 v114, v58, v154, v114
	v_pk_maximum3_f16 v154, v86, v110, v74
	v_pk_maximum3_f16 v155, v87, v111, v75
	v_pk_maximum3_f16 v156, v88, v112, v76
	v_pk_maximum3_f16 v204, v118, v126, v101
	v_pk_maximum3_f16 v208, v130, v161, v117
	v_pk_maximum3_f16 v165, v121, v129, v98
	v_pk_maximum3_f16 v202, v120, v128, v99
	v_pk_maximum3_f16 v203, v119, v127, v100
	v_pk_maximum3_f16 v205, v133, v164, v114
	v_pk_maximum3_f16 v206, v132, v163, v115
	v_pk_maximum3_f16 v157, v157, v204, v208
	v_pk_maximum3_f16 v207, v131, v162, v116
	v_pk_maximum3_f16 v154, v154, v165, v205
	v_pk_maximum3_f16 v155, v155, v202, v206
	v_pk_maximum3_f16 v156, v156, v203, v207
	v_pk_add_f16 v89, v89, v157 neg_lo:[0,1] neg_hi:[0,1]
	v_pk_add_f16 v86, v86, v154 neg_lo:[0,1] neg_hi:[0,1]
	v_pk_add_f16 v87, v87, v155 neg_lo:[0,1] neg_hi:[0,1]
	v_pk_add_f16 v88, v88, v156 neg_lo:[0,1] neg_hi:[0,1]
	v_pk_add_f16 v110, v110, v154 neg_lo:[0,1] neg_hi:[0,1]
	v_exp_f16_sdwa v165, v86 dst_sel:WORD_0 dst_unused:UNUSED_PAD src0_sel:WORD_0
	v_exp_f16_sdwa v202, v87 dst_sel:WORD_0 dst_unused:UNUSED_PAD src0_sel:WORD_0
	v_exp_f16_sdwa v203, v88 dst_sel:WORD_0 dst_unused:UNUSED_PAD src0_sel:WORD_0
	v_exp_f16_sdwa v204, v89 dst_sel:WORD_0 dst_unused:UNUSED_PAD src0_sel:WORD_0
	v_exp_f16_sdwa v165, v86 dst_sel:WORD_1 dst_unused:UNUSED_PRESERVE src0_sel:WORD_1
	v_exp_f16_sdwa v202, v87 dst_sel:WORD_1 dst_unused:UNUSED_PRESERVE src0_sel:WORD_1
	v_exp_f16_sdwa v203, v88 dst_sel:WORD_1 dst_unused:UNUSED_PRESERVE src0_sel:WORD_1
	v_exp_f16_sdwa v204, v89 dst_sel:WORD_1 dst_unused:UNUSED_PRESERVE src0_sel:WORD_1
	v_pk_add_f16 v111, v111, v155 neg_lo:[0,1] neg_hi:[0,1]
	v_pk_add_f16 v89, v165, 0
	v_pk_fma_f16 v49, v49, v204, 0
	v_pk_add_f16 v86, v204, 0
	v_pk_add_f16 v87, v203, 0
	v_pk_add_f16 v88, v202, 0
	v_pk_fma_f16 v48, v48, v203, 0
	v_pk_fma_f16 v47, v47, v202, 0
	v_pk_fma_f16 v46, v46, v165, 0
	v_pk_add_f16 v112, v112, v156 neg_lo:[0,1] neg_hi:[0,1]
	v_pk_add_f16 v113, v113, v157 neg_lo:[0,1] neg_hi:[0,1]
	v_exp_f16_sdwa v165, v110 dst_sel:WORD_0 dst_unused:UNUSED_PAD src0_sel:WORD_0
	v_exp_f16_sdwa v202, v111 dst_sel:WORD_0 dst_unused:UNUSED_PAD src0_sel:WORD_0
	v_exp_f16_sdwa v203, v112 dst_sel:WORD_0 dst_unused:UNUSED_PAD src0_sel:WORD_0
	v_exp_f16_sdwa v204, v113 dst_sel:WORD_0 dst_unused:UNUSED_PAD src0_sel:WORD_0
	v_exp_f16_sdwa v165, v110 dst_sel:WORD_1 dst_unused:UNUSED_PRESERVE src0_sel:WORD_1
	v_exp_f16_sdwa v202, v111 dst_sel:WORD_1 dst_unused:UNUSED_PRESERVE src0_sel:WORD_1
	v_exp_f16_sdwa v203, v112 dst_sel:WORD_1 dst_unused:UNUSED_PRESERVE src0_sel:WORD_1
	v_exp_f16_sdwa v204, v113 dst_sel:WORD_1 dst_unused:UNUSED_PRESERVE src0_sel:WORD_1
	v_pk_add_f16 v89, v89, v165
	v_pk_fma_f16 v49, v69, v204, v49
	v_pk_add_f16 v69, v77, v157 neg_lo:[0,1] neg_hi:[0,1]
	v_pk_add_f16 v88, v88, v202
	v_pk_add_f16 v87, v87, v203
	v_pk_add_f16 v86, v86, v204
	v_pk_fma_f16 v46, v66, v165, v46
	v_pk_fma_f16 v47, v67, v202, v47
	v_pk_fma_f16 v48, v68, v203, v48
	v_pk_add_f16 v66, v74, v154 neg_lo:[0,1] neg_hi:[0,1]
	v_pk_add_f16 v67, v75, v155 neg_lo:[0,1] neg_hi:[0,1]
	v_pk_add_f16 v68, v76, v156 neg_lo:[0,1] neg_hi:[0,1]
	v_exp_f16_sdwa v74, v66 dst_sel:WORD_0 dst_unused:UNUSED_PAD src0_sel:WORD_0
	v_exp_f16_sdwa v75, v67 dst_sel:WORD_0 dst_unused:UNUSED_PAD src0_sel:WORD_0
	v_exp_f16_sdwa v76, v68 dst_sel:WORD_0 dst_unused:UNUSED_PAD src0_sel:WORD_0
	v_exp_f16_sdwa v77, v69 dst_sel:WORD_0 dst_unused:UNUSED_PAD src0_sel:WORD_0
	v_exp_f16_sdwa v74, v66 dst_sel:WORD_1 dst_unused:UNUSED_PRESERVE src0_sel:WORD_1
	v_exp_f16_sdwa v75, v67 dst_sel:WORD_1 dst_unused:UNUSED_PRESERVE src0_sel:WORD_1
	v_exp_f16_sdwa v76, v68 dst_sel:WORD_1 dst_unused:UNUSED_PRESERVE src0_sel:WORD_1
	v_exp_f16_sdwa v77, v69 dst_sel:WORD_1 dst_unused:UNUSED_PRESERVE src0_sel:WORD_1
	v_pk_add_f16 v69, v89, v74
	v_pk_add_f16 v66, v86, v77
	v_pk_add_f16 v67, v87, v76
	v_pk_add_f16 v68, v88, v75
	v_pk_fma_f16 v49, v93, v77, v49
	v_pk_fma_f16 v48, v92, v76, v48
	v_pk_fma_f16 v47, v91, v75, v47
	v_pk_fma_f16 v46, v90, v74, v46
	v_pk_add_f16 v74, v121, v154 neg_lo:[0,1] neg_hi:[0,1]
	v_pk_add_f16 v75, v120, v155 neg_lo:[0,1] neg_hi:[0,1]
	v_pk_add_f16 v76, v119, v156 neg_lo:[0,1] neg_hi:[0,1]
	v_pk_add_f16 v77, v118, v157 neg_lo:[0,1] neg_hi:[0,1]
	v_exp_f16_sdwa v86, v74 dst_sel:WORD_0 dst_unused:UNUSED_PAD src0_sel:WORD_0
	v_exp_f16_sdwa v87, v75 dst_sel:WORD_0 dst_unused:UNUSED_PAD src0_sel:WORD_0
	v_exp_f16_sdwa v88, v76 dst_sel:WORD_0 dst_unused:UNUSED_PAD src0_sel:WORD_0
	v_exp_f16_sdwa v89, v77 dst_sel:WORD_0 dst_unused:UNUSED_PAD src0_sel:WORD_0
	v_exp_f16_sdwa v86, v74 dst_sel:WORD_1 dst_unused:UNUSED_PRESERVE src0_sel:WORD_1
	v_exp_f16_sdwa v87, v75 dst_sel:WORD_1 dst_unused:UNUSED_PRESERVE src0_sel:WORD_1
	v_exp_f16_sdwa v88, v76 dst_sel:WORD_1 dst_unused:UNUSED_PRESERVE src0_sel:WORD_1
	v_exp_f16_sdwa v89, v77 dst_sel:WORD_1 dst_unused:UNUSED_PRESERVE src0_sel:WORD_1
	v_pk_add_f16 v74, v129, v154 neg_lo:[0,1] neg_hi:[0,1]
	v_pk_add_f16 v69, v69, v86
	v_pk_add_f16 v68, v68, v87
	v_pk_add_f16 v67, v67, v88
	v_pk_add_f16 v66, v66, v89
	v_pk_fma_f16 v46, v22, v86, v46
	v_pk_fma_f16 v47, v23, v87, v47
	v_pk_fma_f16 v48, v24, v88, v48
	v_pk_fma_f16 v49, v25, v89, v49
	v_pk_add_f16 v75, v128, v155 neg_lo:[0,1] neg_hi:[0,1]
	v_pk_add_f16 v76, v127, v156 neg_lo:[0,1] neg_hi:[0,1]
	v_pk_add_f16 v77, v126, v157 neg_lo:[0,1] neg_hi:[0,1]
	v_exp_f16_sdwa v86, v74 dst_sel:WORD_0 dst_unused:UNUSED_PAD src0_sel:WORD_0
	v_exp_f16_sdwa v87, v75 dst_sel:WORD_0 dst_unused:UNUSED_PAD src0_sel:WORD_0
	v_exp_f16_sdwa v88, v76 dst_sel:WORD_0 dst_unused:UNUSED_PAD src0_sel:WORD_0
	v_exp_f16_sdwa v89, v77 dst_sel:WORD_0 dst_unused:UNUSED_PAD src0_sel:WORD_0
	v_exp_f16_sdwa v86, v74 dst_sel:WORD_1 dst_unused:UNUSED_PRESERVE src0_sel:WORD_1
	v_exp_f16_sdwa v87, v75 dst_sel:WORD_1 dst_unused:UNUSED_PRESERVE src0_sel:WORD_1
	v_exp_f16_sdwa v88, v76 dst_sel:WORD_1 dst_unused:UNUSED_PRESERVE src0_sel:WORD_1
	v_exp_f16_sdwa v89, v77 dst_sel:WORD_1 dst_unused:UNUSED_PRESERVE src0_sel:WORD_1
	v_pk_add_f16 v74, v98, v154 neg_lo:[0,1] neg_hi:[0,1]
	v_pk_add_f16 v69, v69, v86
	v_pk_add_f16 v66, v66, v89
	v_pk_add_f16 v67, v67, v88
	v_pk_add_f16 v68, v68, v87
	v_pk_fma_f16 v49, v37, v89, v49
	v_pk_fma_f16 v48, v36, v88, v48
	v_pk_fma_f16 v47, v35, v87, v47
	v_pk_fma_f16 v46, v34, v86, v46
	v_pk_add_f16 v75, v99, v155 neg_lo:[0,1] neg_hi:[0,1]
	v_pk_add_f16 v76, v100, v156 neg_lo:[0,1] neg_hi:[0,1]
	v_pk_add_f16 v77, v101, v157 neg_lo:[0,1] neg_hi:[0,1]
	v_exp_f16_sdwa v86, v74 dst_sel:WORD_0 dst_unused:UNUSED_PAD src0_sel:WORD_0
	v_exp_f16_sdwa v87, v75 dst_sel:WORD_0 dst_unused:UNUSED_PAD src0_sel:WORD_0
	v_exp_f16_sdwa v88, v76 dst_sel:WORD_0 dst_unused:UNUSED_PAD src0_sel:WORD_0
	v_exp_f16_sdwa v89, v77 dst_sel:WORD_0 dst_unused:UNUSED_PAD src0_sel:WORD_0
	v_exp_f16_sdwa v86, v74 dst_sel:WORD_1 dst_unused:UNUSED_PRESERVE src0_sel:WORD_1
	v_exp_f16_sdwa v87, v75 dst_sel:WORD_1 dst_unused:UNUSED_PRESERVE src0_sel:WORD_1
	v_exp_f16_sdwa v88, v76 dst_sel:WORD_1 dst_unused:UNUSED_PRESERVE src0_sel:WORD_1
	v_exp_f16_sdwa v89, v77 dst_sel:WORD_1 dst_unused:UNUSED_PRESERVE src0_sel:WORD_1
	v_pk_add_f16 v74, v133, v154 neg_lo:[0,1] neg_hi:[0,1]
	v_pk_add_f16 v69, v69, v86
	v_pk_add_f16 v68, v68, v87
	v_pk_add_f16 v67, v67, v88
	v_pk_add_f16 v66, v66, v89
	v_pk_fma_f16 v46, v50, v86, v46
	v_pk_fma_f16 v47, v51, v87, v47
	v_pk_fma_f16 v48, v52, v88, v48
	v_pk_fma_f16 v49, v53, v89, v49
	v_pk_add_f16 v75, v132, v155 neg_lo:[0,1] neg_hi:[0,1]
	v_pk_add_f16 v76, v131, v156 neg_lo:[0,1] neg_hi:[0,1]
	v_pk_add_f16 v77, v130, v157 neg_lo:[0,1] neg_hi:[0,1]
	v_exp_f16_sdwa v86, v74 dst_sel:WORD_0 dst_unused:UNUSED_PAD src0_sel:WORD_0
	v_exp_f16_sdwa v87, v75 dst_sel:WORD_0 dst_unused:UNUSED_PAD src0_sel:WORD_0
	v_exp_f16_sdwa v88, v76 dst_sel:WORD_0 dst_unused:UNUSED_PAD src0_sel:WORD_0
	v_exp_f16_sdwa v89, v77 dst_sel:WORD_0 dst_unused:UNUSED_PAD src0_sel:WORD_0
	v_exp_f16_sdwa v86, v74 dst_sel:WORD_1 dst_unused:UNUSED_PRESERVE src0_sel:WORD_1
	v_exp_f16_sdwa v87, v75 dst_sel:WORD_1 dst_unused:UNUSED_PRESERVE src0_sel:WORD_1
	v_exp_f16_sdwa v88, v76 dst_sel:WORD_1 dst_unused:UNUSED_PRESERVE src0_sel:WORD_1
	v_exp_f16_sdwa v89, v77 dst_sel:WORD_1 dst_unused:UNUSED_PRESERVE src0_sel:WORD_1
	v_pk_add_f16 v74, v164, v154 neg_lo:[0,1] neg_hi:[0,1]
	v_pk_add_f16 v69, v69, v86
	v_pk_add_f16 v66, v66, v89
	v_pk_add_f16 v67, v67, v88
	v_pk_add_f16 v68, v68, v87
	v_pk_fma_f16 v49, v13, v89, v49
	v_pk_fma_f16 v48, v12, v88, v48
	v_pk_fma_f16 v47, v11, v87, v47
	v_pk_fma_f16 v46, v10, v86, v46
	v_pk_add_f16 v75, v163, v155 neg_lo:[0,1] neg_hi:[0,1]
	v_pk_add_f16 v76, v162, v156 neg_lo:[0,1] neg_hi:[0,1]
	v_pk_add_f16 v77, v161, v157 neg_lo:[0,1] neg_hi:[0,1]
	v_exp_f16_sdwa v86, v74 dst_sel:WORD_0 dst_unused:UNUSED_PAD src0_sel:WORD_0
	v_exp_f16_sdwa v87, v75 dst_sel:WORD_0 dst_unused:UNUSED_PAD src0_sel:WORD_0
	v_exp_f16_sdwa v88, v76 dst_sel:WORD_0 dst_unused:UNUSED_PAD src0_sel:WORD_0
	v_exp_f16_sdwa v89, v77 dst_sel:WORD_0 dst_unused:UNUSED_PAD src0_sel:WORD_0
	v_exp_f16_sdwa v86, v74 dst_sel:WORD_1 dst_unused:UNUSED_PRESERVE src0_sel:WORD_1
	v_exp_f16_sdwa v87, v75 dst_sel:WORD_1 dst_unused:UNUSED_PRESERVE src0_sel:WORD_1
	v_exp_f16_sdwa v88, v76 dst_sel:WORD_1 dst_unused:UNUSED_PRESERVE src0_sel:WORD_1
	v_exp_f16_sdwa v89, v77 dst_sel:WORD_1 dst_unused:UNUSED_PRESERVE src0_sel:WORD_1
	v_pk_add_f16 v74, v114, v154 neg_lo:[0,1] neg_hi:[0,1]
	v_pk_add_f16 v69, v69, v86
	v_pk_add_f16 v68, v68, v87
	v_pk_add_f16 v67, v67, v88
	v_pk_add_f16 v66, v66, v89
	v_pk_fma_f16 v46, v14, v86, v46
	v_pk_fma_f16 v47, v15, v87, v47
	v_pk_fma_f16 v48, v16, v88, v48
	v_pk_fma_f16 v49, v17, v89, v49
	v_pk_add_f16 v75, v115, v155 neg_lo:[0,1] neg_hi:[0,1]
	v_pk_add_f16 v76, v116, v156 neg_lo:[0,1] neg_hi:[0,1]
	v_pk_add_f16 v77, v117, v157 neg_lo:[0,1] neg_hi:[0,1]
	v_exp_f16_sdwa v86, v74 dst_sel:WORD_0 dst_unused:UNUSED_PAD src0_sel:WORD_0
	v_exp_f16_sdwa v87, v75 dst_sel:WORD_0 dst_unused:UNUSED_PAD src0_sel:WORD_0
	v_exp_f16_sdwa v88, v76 dst_sel:WORD_0 dst_unused:UNUSED_PAD src0_sel:WORD_0
	v_exp_f16_sdwa v89, v77 dst_sel:WORD_0 dst_unused:UNUSED_PAD src0_sel:WORD_0
	v_exp_f16_sdwa v86, v74 dst_sel:WORD_1 dst_unused:UNUSED_PRESERVE src0_sel:WORD_1
	v_exp_f16_sdwa v87, v75 dst_sel:WORD_1 dst_unused:UNUSED_PRESERVE src0_sel:WORD_1
	v_exp_f16_sdwa v88, v76 dst_sel:WORD_1 dst_unused:UNUSED_PRESERVE src0_sel:WORD_1
	v_exp_f16_sdwa v89, v77 dst_sel:WORD_1 dst_unused:UNUSED_PRESERVE src0_sel:WORD_1
	v_pk_add_f16 v69, v69, v86
	v_pk_add_f16 v68, v68, v87
	v_rcp_f16_e32 v74, v69
	v_rcp_f16_sdwa v69, v69 dst_sel:DWORD dst_unused:UNUSED_PAD src0_sel:WORD_1
	v_pk_add_f16 v67, v67, v88
	v_rcp_f16_e32 v75, v68
	v_rcp_f16_sdwa v68, v68 dst_sel:DWORD dst_unused:UNUSED_PAD src0_sel:WORD_1
	v_pk_add_f16 v66, v66, v89
	v_pk_fma_f16 v46, v18, v86, v46
	v_rcp_f16_e32 v86, v67
	v_rcp_f16_sdwa v67, v67 dst_sel:DWORD dst_unused:UNUSED_PAD src0_sel:WORD_1
	v_pk_fma_f16 v47, v19, v87, v47
	v_rcp_f16_e32 v87, v66
	v_rcp_f16_sdwa v66, v66 dst_sel:DWORD dst_unused:UNUSED_PAD src0_sel:WORD_1
	v_pack_b32_f16 v69, v74, v69
	v_pk_mul_f16 v77, v46, v69
	v_pack_b32_f16 v46, v75, v68
	v_pk_fma_f16 v48, v20, v88, v48
	v_pk_mul_f16 v76, v47, v46
	v_pack_b32_f16 v46, v86, v67
	v_pk_fma_f16 v49, v21, v89, v49
	v_pk_mul_f16 v75, v48, v46
	v_pack_b32_f16 v46, v87, v66
	v_pk_mul_f16 v74, v49, v46
	s_waitcnt vmcnt(6)
	v_pk_mul_f16 v49, v160, v153 op_sel_hi:[0,1]
	v_pk_mul_f16 v46, v160, v150 op_sel_hi:[0,1]
	v_pk_mul_f16 v47, v160, v151 op_sel_hi:[0,1]
	v_pk_mul_f16 v48, v160, v152 op_sel_hi:[0,1]
	v_pk_mul_f16 v69, v158, v153 op_sel_hi:[0,1]
	v_pk_mul_f16 v89, v159, v153 op_sel_hi:[0,1]
	v_pk_fma_f16 v57, v57, v153, v49
	v_pk_fma_f16 v73, v73, v153, v49
	v_pk_fma_f16 v49, v97, v153, v49
	v_pk_mul_f16 v66, v158, v150 op_sel_hi:[0,1]
	v_pk_maximum3_f16 v117, v57, v73, v49
	v_pk_mul_f16 v67, v158, v151 op_sel_hi:[0,1]
	v_pk_mul_f16 v68, v158, v152 op_sel_hi:[0,1]
	v_pk_mul_f16 v86, v159, v150 op_sel_hi:[0,1]
	v_pk_mul_f16 v87, v159, v151 op_sel_hi:[0,1]
	v_pk_mul_f16 v88, v159, v152 op_sel_hi:[0,1]
	v_pk_fma_f16 v56, v56, v152, v48
	v_pk_fma_f16 v55, v55, v151, v47
	v_pk_fma_f16 v54, v54, v150, v46
	v_pk_fma_f16 v72, v72, v152, v48
	v_pk_fma_f16 v71, v71, v151, v47
	v_pk_fma_f16 v70, v70, v150, v46
	v_pk_fma_f16 v48, v96, v152, v48
	v_pk_fma_f16 v47, v95, v151, v47
	v_pk_fma_f16 v46, v94, v150, v46
	v_pk_fma_f16 v90, v29, v153, v69
	v_pk_fma_f16 v94, v41, v153, v69
	v_pk_fma_f16 v69, v61, v153, v69
	v_pk_fma_f16 v98, v81, v153, v89
	v_pk_fma_f16 v110, v109, v153, v89
	v_pk_fma_f16 v89, v125, v153, v89
	v_pk_maximum3_f16 v114, v54, v70, v46
	v_pk_maximum3_f16 v115, v55, v71, v47
	v_pk_maximum3_f16 v116, v56, v72, v48
	v_pk_maximum3_f16 v121, v90, v94, v69
	v_pk_fma_f16 v91, v28, v152, v68
	v_pk_maximum3_f16 v129, v98, v110, v89
	v_pk_fma_f16 v92, v27, v151, v67
	v_pk_maximum3_f16 v117, v117, v121, v129
	v_pk_fma_f16 v93, v26, v150, v66
	v_pk_fma_f16 v95, v40, v152, v68
	v_pk_fma_f16 v96, v39, v151, v67
	v_pk_fma_f16 v97, v38, v150, v66
	v_pk_fma_f16 v68, v60, v152, v68
	v_pk_fma_f16 v67, v59, v151, v67
	v_pk_fma_f16 v66, v58, v150, v66
	v_pk_fma_f16 v99, v80, v152, v88
	v_pk_fma_f16 v100, v79, v151, v87
	v_pk_fma_f16 v101, v78, v150, v86
	v_pk_fma_f16 v111, v108, v152, v88
	v_pk_fma_f16 v112, v107, v151, v87
	v_pk_fma_f16 v113, v106, v150, v86
	v_pk_fma_f16 v88, v124, v152, v88
	v_pk_fma_f16 v87, v123, v151, v87
	v_pk_fma_f16 v86, v122, v150, v86
	v_pk_maximum3_f16 v118, v93, v97, v66
	v_pk_maximum3_f16 v119, v92, v96, v67
	v_pk_maximum3_f16 v120, v91, v95, v68
	v_pk_maximum3_f16 v127, v100, v112, v87
	v_pk_maximum3_f16 v128, v99, v111, v88
	v_pk_maximum3_f16 v126, v101, v113, v86
	v_pk_maximum3_f16 v114, v114, v118, v126
	v_pk_maximum3_f16 v115, v115, v119, v127
	v_pk_maximum3_f16 v116, v116, v120, v128
	v_pk_add_f16 v57, v57, v117 neg_lo:[0,1] neg_hi:[0,1]
	v_pk_add_f16 v54, v54, v114 neg_lo:[0,1] neg_hi:[0,1]
	v_pk_add_f16 v55, v55, v115 neg_lo:[0,1] neg_hi:[0,1]
	v_pk_add_f16 v56, v56, v116 neg_lo:[0,1] neg_hi:[0,1]
	v_pk_add_f16 v70, v70, v114 neg_lo:[0,1] neg_hi:[0,1]
	v_exp_f16_sdwa v118, v54 dst_sel:WORD_0 dst_unused:UNUSED_PAD src0_sel:WORD_0
	v_exp_f16_sdwa v119, v55 dst_sel:WORD_0 dst_unused:UNUSED_PAD src0_sel:WORD_0
	v_exp_f16_sdwa v120, v56 dst_sel:WORD_0 dst_unused:UNUSED_PAD src0_sel:WORD_0
	v_exp_f16_sdwa v121, v57 dst_sel:WORD_0 dst_unused:UNUSED_PAD src0_sel:WORD_0
	v_exp_f16_sdwa v118, v54 dst_sel:WORD_1 dst_unused:UNUSED_PRESERVE src0_sel:WORD_1
	v_exp_f16_sdwa v119, v55 dst_sel:WORD_1 dst_unused:UNUSED_PRESERVE src0_sel:WORD_1
	v_exp_f16_sdwa v120, v56 dst_sel:WORD_1 dst_unused:UNUSED_PRESERVE src0_sel:WORD_1
	v_exp_f16_sdwa v121, v57 dst_sel:WORD_1 dst_unused:UNUSED_PRESERVE src0_sel:WORD_1
	v_pk_add_f16 v71, v71, v115 neg_lo:[0,1] neg_hi:[0,1]
	v_pk_add_f16 v57, v118, 0
	v_pk_fma_f16 v25, v25, v121, 0
	v_pk_add_f16 v54, v121, 0
	v_pk_add_f16 v55, v120, 0
	v_pk_add_f16 v56, v119, 0
	v_pk_fma_f16 v24, v24, v120, 0
	v_pk_fma_f16 v23, v23, v119, 0
	v_pk_fma_f16 v22, v22, v118, 0
	v_pk_add_f16 v72, v72, v116 neg_lo:[0,1] neg_hi:[0,1]
	v_pk_add_f16 v73, v73, v117 neg_lo:[0,1] neg_hi:[0,1]
	v_exp_f16_sdwa v118, v70 dst_sel:WORD_0 dst_unused:UNUSED_PAD src0_sel:WORD_0
	v_exp_f16_sdwa v119, v71 dst_sel:WORD_0 dst_unused:UNUSED_PAD src0_sel:WORD_0
	v_exp_f16_sdwa v120, v72 dst_sel:WORD_0 dst_unused:UNUSED_PAD src0_sel:WORD_0
	v_exp_f16_sdwa v121, v73 dst_sel:WORD_0 dst_unused:UNUSED_PAD src0_sel:WORD_0
	v_exp_f16_sdwa v118, v70 dst_sel:WORD_1 dst_unused:UNUSED_PRESERVE src0_sel:WORD_1
	v_exp_f16_sdwa v119, v71 dst_sel:WORD_1 dst_unused:UNUSED_PRESERVE src0_sel:WORD_1
	v_exp_f16_sdwa v120, v72 dst_sel:WORD_1 dst_unused:UNUSED_PRESERVE src0_sel:WORD_1
	v_exp_f16_sdwa v121, v73 dst_sel:WORD_1 dst_unused:UNUSED_PRESERVE src0_sel:WORD_1
	v_pk_add_f16 v57, v57, v118
	v_pk_fma_f16 v25, v37, v121, v25
	v_pk_add_f16 v37, v49, v117 neg_lo:[0,1] neg_hi:[0,1]
	v_pk_add_f16 v56, v56, v119
	v_pk_add_f16 v55, v55, v120
	v_pk_add_f16 v54, v54, v121
	v_pk_fma_f16 v22, v34, v118, v22
	v_pk_fma_f16 v23, v35, v119, v23
	v_pk_fma_f16 v24, v36, v120, v24
	v_pk_add_f16 v34, v46, v114 neg_lo:[0,1] neg_hi:[0,1]
	v_pk_add_f16 v35, v47, v115 neg_lo:[0,1] neg_hi:[0,1]
	v_pk_add_f16 v36, v48, v116 neg_lo:[0,1] neg_hi:[0,1]
	v_exp_f16_sdwa v46, v34 dst_sel:WORD_0 dst_unused:UNUSED_PAD src0_sel:WORD_0
	v_exp_f16_sdwa v47, v35 dst_sel:WORD_0 dst_unused:UNUSED_PAD src0_sel:WORD_0
	v_exp_f16_sdwa v48, v36 dst_sel:WORD_0 dst_unused:UNUSED_PAD src0_sel:WORD_0
	v_exp_f16_sdwa v49, v37 dst_sel:WORD_0 dst_unused:UNUSED_PAD src0_sel:WORD_0
	v_exp_f16_sdwa v46, v34 dst_sel:WORD_1 dst_unused:UNUSED_PRESERVE src0_sel:WORD_1
	v_exp_f16_sdwa v47, v35 dst_sel:WORD_1 dst_unused:UNUSED_PRESERVE src0_sel:WORD_1
	v_exp_f16_sdwa v48, v36 dst_sel:WORD_1 dst_unused:UNUSED_PRESERVE src0_sel:WORD_1
	v_exp_f16_sdwa v49, v37 dst_sel:WORD_1 dst_unused:UNUSED_PRESERVE src0_sel:WORD_1
	v_pk_add_f16 v37, v57, v46
	v_pk_add_f16 v34, v54, v49
	v_pk_add_f16 v35, v55, v48
	v_pk_add_f16 v36, v56, v47
	v_pk_fma_f16 v25, v53, v49, v25
	v_pk_fma_f16 v24, v52, v48, v24
	v_pk_fma_f16 v23, v51, v47, v23
	v_pk_fma_f16 v22, v50, v46, v22
	v_pk_add_f16 v46, v93, v114 neg_lo:[0,1] neg_hi:[0,1]
	v_pk_add_f16 v47, v92, v115 neg_lo:[0,1] neg_hi:[0,1]
	v_pk_add_f16 v48, v91, v116 neg_lo:[0,1] neg_hi:[0,1]
	v_pk_add_f16 v49, v90, v117 neg_lo:[0,1] neg_hi:[0,1]
	v_exp_f16_sdwa v50, v46 dst_sel:WORD_0 dst_unused:UNUSED_PAD src0_sel:WORD_0
	v_exp_f16_sdwa v51, v47 dst_sel:WORD_0 dst_unused:UNUSED_PAD src0_sel:WORD_0
	v_exp_f16_sdwa v52, v48 dst_sel:WORD_0 dst_unused:UNUSED_PAD src0_sel:WORD_0
	v_exp_f16_sdwa v53, v49 dst_sel:WORD_0 dst_unused:UNUSED_PAD src0_sel:WORD_0
	v_exp_f16_sdwa v50, v46 dst_sel:WORD_1 dst_unused:UNUSED_PRESERVE src0_sel:WORD_1
	v_exp_f16_sdwa v51, v47 dst_sel:WORD_1 dst_unused:UNUSED_PRESERVE src0_sel:WORD_1
	v_exp_f16_sdwa v52, v48 dst_sel:WORD_1 dst_unused:UNUSED_PRESERVE src0_sel:WORD_1
	v_exp_f16_sdwa v53, v49 dst_sel:WORD_1 dst_unused:UNUSED_PRESERVE src0_sel:WORD_1
	v_pk_add_f16 v46, v97, v114 neg_lo:[0,1] neg_hi:[0,1]
	v_pk_add_f16 v37, v37, v50
	v_pk_add_f16 v36, v36, v51
	v_pk_add_f16 v35, v35, v52
	v_pk_add_f16 v34, v34, v53
	v_pk_fma_f16 v22, v10, v50, v22
	v_pk_fma_f16 v23, v11, v51, v23
	v_pk_fma_f16 v24, v12, v52, v24
	v_pk_fma_f16 v25, v13, v53, v25
	v_pk_add_f16 v47, v96, v115 neg_lo:[0,1] neg_hi:[0,1]
	v_pk_add_f16 v48, v95, v116 neg_lo:[0,1] neg_hi:[0,1]
	v_pk_add_f16 v49, v94, v117 neg_lo:[0,1] neg_hi:[0,1]
	v_exp_f16_sdwa v50, v46 dst_sel:WORD_0 dst_unused:UNUSED_PAD src0_sel:WORD_0
	v_exp_f16_sdwa v51, v47 dst_sel:WORD_0 dst_unused:UNUSED_PAD src0_sel:WORD_0
	v_exp_f16_sdwa v52, v48 dst_sel:WORD_0 dst_unused:UNUSED_PAD src0_sel:WORD_0
	v_exp_f16_sdwa v53, v49 dst_sel:WORD_0 dst_unused:UNUSED_PAD src0_sel:WORD_0
	v_exp_f16_sdwa v50, v46 dst_sel:WORD_1 dst_unused:UNUSED_PRESERVE src0_sel:WORD_1
	v_exp_f16_sdwa v51, v47 dst_sel:WORD_1 dst_unused:UNUSED_PRESERVE src0_sel:WORD_1
	v_exp_f16_sdwa v52, v48 dst_sel:WORD_1 dst_unused:UNUSED_PRESERVE src0_sel:WORD_1
	v_exp_f16_sdwa v53, v49 dst_sel:WORD_1 dst_unused:UNUSED_PRESERVE src0_sel:WORD_1
	v_pk_add_f16 v46, v66, v114 neg_lo:[0,1] neg_hi:[0,1]
	v_pk_add_f16 v37, v37, v50
	v_pk_add_f16 v34, v34, v53
	v_pk_add_f16 v35, v35, v52
	v_pk_add_f16 v36, v36, v51
	v_pk_fma_f16 v25, v17, v53, v25
	v_pk_fma_f16 v24, v16, v52, v24
	v_pk_fma_f16 v23, v15, v51, v23
	v_pk_fma_f16 v22, v14, v50, v22
	v_pk_add_f16 v47, v67, v115 neg_lo:[0,1] neg_hi:[0,1]
	v_pk_add_f16 v48, v68, v116 neg_lo:[0,1] neg_hi:[0,1]
	v_pk_add_f16 v49, v69, v117 neg_lo:[0,1] neg_hi:[0,1]
	v_exp_f16_sdwa v50, v46 dst_sel:WORD_0 dst_unused:UNUSED_PAD src0_sel:WORD_0
	v_exp_f16_sdwa v51, v47 dst_sel:WORD_0 dst_unused:UNUSED_PAD src0_sel:WORD_0
	v_exp_f16_sdwa v52, v48 dst_sel:WORD_0 dst_unused:UNUSED_PAD src0_sel:WORD_0
	v_exp_f16_sdwa v53, v49 dst_sel:WORD_0 dst_unused:UNUSED_PAD src0_sel:WORD_0
	v_exp_f16_sdwa v50, v46 dst_sel:WORD_1 dst_unused:UNUSED_PRESERVE src0_sel:WORD_1
	v_exp_f16_sdwa v51, v47 dst_sel:WORD_1 dst_unused:UNUSED_PRESERVE src0_sel:WORD_1
	v_exp_f16_sdwa v52, v48 dst_sel:WORD_1 dst_unused:UNUSED_PRESERVE src0_sel:WORD_1
	v_exp_f16_sdwa v53, v49 dst_sel:WORD_1 dst_unused:UNUSED_PRESERVE src0_sel:WORD_1
	v_pk_add_f16 v46, v101, v114 neg_lo:[0,1] neg_hi:[0,1]
	v_pk_add_f16 v37, v37, v50
	v_pk_add_f16 v36, v36, v51
	v_pk_add_f16 v35, v35, v52
	v_pk_add_f16 v34, v34, v53
	v_pk_fma_f16 v22, v18, v50, v22
	v_pk_fma_f16 v23, v19, v51, v23
	v_pk_fma_f16 v24, v20, v52, v24
	v_pk_fma_f16 v25, v21, v53, v25
	v_pk_add_f16 v47, v100, v115 neg_lo:[0,1] neg_hi:[0,1]
	v_pk_add_f16 v48, v99, v116 neg_lo:[0,1] neg_hi:[0,1]
	v_pk_add_f16 v49, v98, v117 neg_lo:[0,1] neg_hi:[0,1]
	v_exp_f16_sdwa v50, v46 dst_sel:WORD_0 dst_unused:UNUSED_PAD src0_sel:WORD_0
	v_exp_f16_sdwa v51, v47 dst_sel:WORD_0 dst_unused:UNUSED_PAD src0_sel:WORD_0
	v_exp_f16_sdwa v52, v48 dst_sel:WORD_0 dst_unused:UNUSED_PAD src0_sel:WORD_0
	v_exp_f16_sdwa v53, v49 dst_sel:WORD_0 dst_unused:UNUSED_PAD src0_sel:WORD_0
	v_exp_f16_sdwa v50, v46 dst_sel:WORD_1 dst_unused:UNUSED_PRESERVE src0_sel:WORD_1
	v_exp_f16_sdwa v51, v47 dst_sel:WORD_1 dst_unused:UNUSED_PRESERVE src0_sel:WORD_1
	v_exp_f16_sdwa v52, v48 dst_sel:WORD_1 dst_unused:UNUSED_PRESERVE src0_sel:WORD_1
	v_exp_f16_sdwa v53, v49 dst_sel:WORD_1 dst_unused:UNUSED_PRESERVE src0_sel:WORD_1
	v_pk_add_f16 v46, v113, v114 neg_lo:[0,1] neg_hi:[0,1]
	v_pk_add_f16 v37, v37, v50
	v_pk_add_f16 v34, v34, v53
	v_pk_add_f16 v35, v35, v52
	v_pk_add_f16 v36, v36, v51
	v_pk_fma_f16 v25, v33, v53, v25
	v_pk_fma_f16 v24, v32, v52, v24
	v_pk_fma_f16 v23, v31, v51, v23
	v_pk_fma_f16 v22, v30, v50, v22
	v_pk_add_f16 v47, v112, v115 neg_lo:[0,1] neg_hi:[0,1]
	v_pk_add_f16 v48, v111, v116 neg_lo:[0,1] neg_hi:[0,1]
	v_pk_add_f16 v49, v110, v117 neg_lo:[0,1] neg_hi:[0,1]
	v_exp_f16_sdwa v50, v46 dst_sel:WORD_0 dst_unused:UNUSED_PAD src0_sel:WORD_0
	v_exp_f16_sdwa v51, v47 dst_sel:WORD_0 dst_unused:UNUSED_PAD src0_sel:WORD_0
	v_exp_f16_sdwa v52, v48 dst_sel:WORD_0 dst_unused:UNUSED_PAD src0_sel:WORD_0
	v_exp_f16_sdwa v53, v49 dst_sel:WORD_0 dst_unused:UNUSED_PAD src0_sel:WORD_0
	v_exp_f16_sdwa v50, v46 dst_sel:WORD_1 dst_unused:UNUSED_PRESERVE src0_sel:WORD_1
	v_exp_f16_sdwa v51, v47 dst_sel:WORD_1 dst_unused:UNUSED_PRESERVE src0_sel:WORD_1
	v_exp_f16_sdwa v52, v48 dst_sel:WORD_1 dst_unused:UNUSED_PRESERVE src0_sel:WORD_1
	v_exp_f16_sdwa v53, v49 dst_sel:WORD_1 dst_unused:UNUSED_PRESERVE src0_sel:WORD_1
	v_pk_add_f16 v46, v86, v114 neg_lo:[0,1] neg_hi:[0,1]
	v_pk_add_f16 v37, v37, v50
	v_pk_add_f16 v36, v36, v51
	v_pk_add_f16 v35, v35, v52
	v_pk_add_f16 v34, v34, v53
	v_pk_fma_f16 v22, v42, v50, v22
	v_pk_fma_f16 v23, v43, v51, v23
	v_pk_fma_f16 v24, v44, v52, v24
	v_pk_fma_f16 v25, v45, v53, v25
	v_pk_add_f16 v47, v87, v115 neg_lo:[0,1] neg_hi:[0,1]
	v_pk_add_f16 v48, v88, v116 neg_lo:[0,1] neg_hi:[0,1]
	v_pk_add_f16 v49, v89, v117 neg_lo:[0,1] neg_hi:[0,1]
	v_exp_f16_sdwa v50, v46 dst_sel:WORD_0 dst_unused:UNUSED_PAD src0_sel:WORD_0
	v_exp_f16_sdwa v51, v47 dst_sel:WORD_0 dst_unused:UNUSED_PAD src0_sel:WORD_0
	v_exp_f16_sdwa v52, v48 dst_sel:WORD_0 dst_unused:UNUSED_PAD src0_sel:WORD_0
	v_exp_f16_sdwa v53, v49 dst_sel:WORD_0 dst_unused:UNUSED_PAD src0_sel:WORD_0
	v_exp_f16_sdwa v50, v46 dst_sel:WORD_1 dst_unused:UNUSED_PRESERVE src0_sel:WORD_1
	v_exp_f16_sdwa v51, v47 dst_sel:WORD_1 dst_unused:UNUSED_PRESERVE src0_sel:WORD_1
	v_exp_f16_sdwa v52, v48 dst_sel:WORD_1 dst_unused:UNUSED_PRESERVE src0_sel:WORD_1
	v_exp_f16_sdwa v53, v49 dst_sel:WORD_1 dst_unused:UNUSED_PRESERVE src0_sel:WORD_1
	v_pk_add_f16 v37, v37, v50
	v_pk_add_f16 v36, v36, v51
	v_rcp_f16_e32 v46, v37
	v_rcp_f16_sdwa v37, v37 dst_sel:DWORD dst_unused:UNUSED_PAD src0_sel:WORD_1
	v_pk_add_f16 v35, v35, v52
	v_rcp_f16_e32 v47, v36
	v_rcp_f16_sdwa v36, v36 dst_sel:DWORD dst_unused:UNUSED_PAD src0_sel:WORD_1
	v_pk_add_f16 v34, v34, v53
	v_rcp_f16_e32 v48, v35
	v_rcp_f16_sdwa v35, v35 dst_sel:DWORD dst_unused:UNUSED_PAD src0_sel:WORD_1
	v_rcp_f16_e32 v49, v34
	v_rcp_f16_sdwa v34, v34 dst_sel:DWORD dst_unused:UNUSED_PAD src0_sel:WORD_1
	v_pk_fma_f16 v22, v62, v50, v22
	v_pack_b32_f16 v37, v46, v37
	v_pk_fma_f16 v23, v63, v51, v23
	v_pk_mul_f16 v57, v22, v37
	v_pack_b32_f16 v22, v47, v36
	v_pk_fma_f16 v24, v64, v52, v24
	v_pk_mul_f16 v56, v23, v22
	v_pack_b32_f16 v22, v48, v35
	v_pk_fma_f16 v25, v65, v53, v25
	v_pk_mul_f16 v55, v24, v22
	v_pack_b32_f16 v22, v49, v34
	v_pk_mul_f16 v54, v25, v22
	s_waitcnt vmcnt(0)
	v_pk_mul_f16 v22, v160, v146 op_sel_hi:[0,1]
	v_pk_mul_f16 v23, v160, v147 op_sel_hi:[0,1]
	v_pk_mul_f16 v24, v160, v148 op_sel_hi:[0,1]
	v_pk_mul_f16 v25, v160, v149 op_sel_hi:[0,1]
	v_pk_mul_f16 v46, v159, v146 op_sel_hi:[0,1]
	v_pk_mul_f16 v47, v159, v147 op_sel_hi:[0,1]
	v_pk_mul_f16 v48, v159, v148 op_sel_hi:[0,1]
	v_pk_mul_f16 v49, v159, v149 op_sel_hi:[0,1]
	v_pk_mul_f16 v34, v158, v146 op_sel_hi:[0,1]
	v_pk_mul_f16 v35, v158, v147 op_sel_hi:[0,1]
	v_pk_mul_f16 v36, v158, v148 op_sel_hi:[0,1]
	v_pk_mul_f16 v37, v158, v149 op_sel_hi:[0,1]
	v_pk_fma_f16 v29, v29, v149, v25
	v_pk_fma_f16 v28, v28, v148, v24
	v_pk_fma_f16 v27, v27, v147, v23
	v_pk_fma_f16 v26, v26, v146, v22
	v_pk_fma_f16 v41, v41, v149, v25
	v_pk_fma_f16 v40, v40, v148, v24
	v_pk_fma_f16 v39, v39, v147, v23
	v_pk_fma_f16 v38, v38, v146, v22
	v_pk_fma_f16 v25, v61, v149, v25
	v_pk_fma_f16 v24, v60, v148, v24
	v_pk_fma_f16 v23, v59, v147, v23
	v_pk_fma_f16 v22, v58, v146, v22
	v_pk_fma_f16 v66, v137, v149, v49
	v_pk_fma_f16 v67, v136, v148, v48
	v_pk_fma_f16 v68, v135, v147, v47
	v_pk_fma_f16 v69, v134, v146, v46
	v_pk_fma_f16 v70, v145, v149, v49
	v_pk_fma_f16 v71, v144, v148, v48
	v_pk_fma_f16 v72, v143, v147, v47
	v_pk_fma_f16 v73, v142, v146, v46
	v_pk_fma_f16 v9, v9, v149, v49
	v_pk_fma_f16 v8, v8, v148, v48
	v_pk_fma_f16 v7, v7, v147, v47
	v_pk_fma_f16 v6, v6, v146, v46
	v_pk_maximum3_f16 v46, v26, v38, v22
	v_pk_maximum3_f16 v47, v27, v39, v23
	v_pk_maximum3_f16 v48, v28, v40, v24
	v_pk_maximum3_f16 v49, v29, v41, v25
	v_pk_fma_f16 v50, v81, v149, v37
	v_pk_fma_f16 v51, v80, v148, v36
	v_pk_fma_f16 v52, v79, v147, v35
	v_pk_fma_f16 v53, v78, v146, v34
	v_pk_fma_f16 v58, v109, v149, v37
	v_pk_fma_f16 v59, v108, v148, v36
	v_pk_fma_f16 v60, v107, v147, v35
	v_pk_fma_f16 v61, v106, v146, v34
	v_pk_fma_f16 v37, v125, v149, v37
	v_pk_fma_f16 v36, v124, v148, v36
	v_pk_fma_f16 v35, v123, v147, v35
	v_pk_fma_f16 v34, v122, v146, v34
	v_pk_maximum3_f16 v79, v52, v60, v35
	v_pk_maximum3_f16 v80, v51, v59, v36
	v_pk_maximum3_f16 v81, v50, v58, v37
	v_pk_maximum3_f16 v86, v69, v73, v6
	v_pk_maximum3_f16 v87, v68, v72, v7
	v_pk_maximum3_f16 v78, v53, v61, v34
	v_pk_maximum3_f16 v88, v67, v71, v8
	v_pk_maximum3_f16 v89, v66, v70, v9
	v_pk_maximum3_f16 v46, v46, v78, v86
	v_pk_maximum3_f16 v47, v47, v79, v87
	v_pk_maximum3_f16 v48, v48, v80, v88
	v_pk_maximum3_f16 v49, v49, v81, v89
	s_nop 0
	v_pk_add_f16 v26, v26, v46 neg_lo:[0,1] neg_hi:[0,1]
	v_pk_add_f16 v27, v27, v47 neg_lo:[0,1] neg_hi:[0,1]
	v_pk_add_f16 v28, v28, v48 neg_lo:[0,1] neg_hi:[0,1]
	v_pk_add_f16 v29, v29, v49 neg_lo:[0,1] neg_hi:[0,1]
	v_pk_add_f16 v38, v38, v46 neg_lo:[0,1] neg_hi:[0,1]
	v_exp_f16_sdwa v78, v26 dst_sel:WORD_0 dst_unused:UNUSED_PAD src0_sel:WORD_0
	v_exp_f16_sdwa v79, v27 dst_sel:WORD_0 dst_unused:UNUSED_PAD src0_sel:WORD_0
	v_exp_f16_sdwa v80, v28 dst_sel:WORD_0 dst_unused:UNUSED_PAD src0_sel:WORD_0
	v_exp_f16_sdwa v81, v29 dst_sel:WORD_0 dst_unused:UNUSED_PAD src0_sel:WORD_0
	v_exp_f16_sdwa v78, v26 dst_sel:WORD_1 dst_unused:UNUSED_PRESERVE src0_sel:WORD_1
	v_exp_f16_sdwa v79, v27 dst_sel:WORD_1 dst_unused:UNUSED_PRESERVE src0_sel:WORD_1
	v_exp_f16_sdwa v80, v28 dst_sel:WORD_1 dst_unused:UNUSED_PRESERVE src0_sel:WORD_1
	v_exp_f16_sdwa v81, v29 dst_sel:WORD_1 dst_unused:UNUSED_PRESERVE src0_sel:WORD_1
	v_pk_add_f16 v39, v39, v47 neg_lo:[0,1] neg_hi:[0,1]
	v_pk_add_f16 v26, v78, 0
	v_pk_add_f16 v27, v79, 0
	v_pk_add_f16 v28, v80, 0
	v_pk_add_f16 v29, v81, 0
	v_pk_fma_f16 v10, v10, v78, 0
	v_pk_fma_f16 v11, v11, v79, 0
	v_pk_fma_f16 v12, v12, v80, 0
	v_pk_fma_f16 v13, v13, v81, 0
	v_pk_add_f16 v40, v40, v48 neg_lo:[0,1] neg_hi:[0,1]
	v_pk_add_f16 v41, v41, v49 neg_lo:[0,1] neg_hi:[0,1]
	v_pk_add_f16 v6, v6, v46 neg_lo:[0,1] neg_hi:[0,1]
	v_exp_f16_sdwa v78, v38 dst_sel:WORD_0 dst_unused:UNUSED_PAD src0_sel:WORD_0
	v_exp_f16_sdwa v79, v39 dst_sel:WORD_0 dst_unused:UNUSED_PAD src0_sel:WORD_0
	v_exp_f16_sdwa v80, v40 dst_sel:WORD_0 dst_unused:UNUSED_PAD src0_sel:WORD_0
	v_exp_f16_sdwa v81, v41 dst_sel:WORD_0 dst_unused:UNUSED_PAD src0_sel:WORD_0
	v_exp_f16_sdwa v78, v38 dst_sel:WORD_1 dst_unused:UNUSED_PRESERVE src0_sel:WORD_1
	v_exp_f16_sdwa v79, v39 dst_sel:WORD_1 dst_unused:UNUSED_PRESERVE src0_sel:WORD_1
	v_exp_f16_sdwa v80, v40 dst_sel:WORD_1 dst_unused:UNUSED_PRESERVE src0_sel:WORD_1
	v_exp_f16_sdwa v81, v41 dst_sel:WORD_1 dst_unused:UNUSED_PRESERVE src0_sel:WORD_1
	v_pk_add_f16 v7, v7, v47 neg_lo:[0,1] neg_hi:[0,1]
	v_pk_add_f16 v29, v29, v81
	v_pk_add_f16 v28, v28, v80
	v_pk_add_f16 v27, v27, v79
	v_pk_add_f16 v26, v26, v78
	v_pk_fma_f16 v13, v17, v81, v13
	v_pk_fma_f16 v12, v16, v80, v12
	v_pk_fma_f16 v11, v15, v79, v11
	v_pk_fma_f16 v10, v14, v78, v10
	v_pk_add_f16 v14, v22, v46 neg_lo:[0,1] neg_hi:[0,1]
	v_pk_add_f16 v15, v23, v47 neg_lo:[0,1] neg_hi:[0,1]
	v_pk_add_f16 v16, v24, v48 neg_lo:[0,1] neg_hi:[0,1]
	v_pk_add_f16 v17, v25, v49 neg_lo:[0,1] neg_hi:[0,1]
	v_pk_add_f16 v8, v8, v48 neg_lo:[0,1] neg_hi:[0,1]
	v_exp_f16_sdwa v22, v14 dst_sel:WORD_0 dst_unused:UNUSED_PAD src0_sel:WORD_0
	v_exp_f16_sdwa v23, v15 dst_sel:WORD_0 dst_unused:UNUSED_PAD src0_sel:WORD_0
	v_exp_f16_sdwa v24, v16 dst_sel:WORD_0 dst_unused:UNUSED_PAD src0_sel:WORD_0
	v_exp_f16_sdwa v25, v17 dst_sel:WORD_0 dst_unused:UNUSED_PAD src0_sel:WORD_0
	v_exp_f16_sdwa v22, v14 dst_sel:WORD_1 dst_unused:UNUSED_PRESERVE src0_sel:WORD_1
	v_exp_f16_sdwa v23, v15 dst_sel:WORD_1 dst_unused:UNUSED_PRESERVE src0_sel:WORD_1
	v_exp_f16_sdwa v24, v16 dst_sel:WORD_1 dst_unused:UNUSED_PRESERVE src0_sel:WORD_1
	v_exp_f16_sdwa v25, v17 dst_sel:WORD_1 dst_unused:UNUSED_PRESERVE src0_sel:WORD_1
	v_pk_add_f16 v9, v9, v49 neg_lo:[0,1] neg_hi:[0,1]
	v_pk_add_f16 v14, v26, v22
	v_pk_add_f16 v15, v27, v23
	v_pk_add_f16 v16, v28, v24
	v_pk_add_f16 v17, v29, v25
	v_pk_fma_f16 v10, v18, v22, v10
	v_pk_fma_f16 v11, v19, v23, v11
	v_pk_fma_f16 v12, v20, v24, v12
	v_pk_fma_f16 v13, v21, v25, v13
	v_pk_add_f16 v18, v53, v46 neg_lo:[0,1] neg_hi:[0,1]
	v_pk_add_f16 v19, v52, v47 neg_lo:[0,1] neg_hi:[0,1]
	v_pk_add_f16 v20, v51, v48 neg_lo:[0,1] neg_hi:[0,1]
	v_pk_add_f16 v21, v50, v49 neg_lo:[0,1] neg_hi:[0,1]
	v_exp_f16_sdwa v22, v18 dst_sel:WORD_0 dst_unused:UNUSED_PAD src0_sel:WORD_0
	v_exp_f16_sdwa v23, v19 dst_sel:WORD_0 dst_unused:UNUSED_PAD src0_sel:WORD_0
	v_exp_f16_sdwa v24, v20 dst_sel:WORD_0 dst_unused:UNUSED_PAD src0_sel:WORD_0
	v_exp_f16_sdwa v25, v21 dst_sel:WORD_0 dst_unused:UNUSED_PAD src0_sel:WORD_0
	v_exp_f16_sdwa v22, v18 dst_sel:WORD_1 dst_unused:UNUSED_PRESERVE src0_sel:WORD_1
	v_exp_f16_sdwa v23, v19 dst_sel:WORD_1 dst_unused:UNUSED_PRESERVE src0_sel:WORD_1
	v_exp_f16_sdwa v24, v20 dst_sel:WORD_1 dst_unused:UNUSED_PRESERVE src0_sel:WORD_1
	v_exp_f16_sdwa v25, v21 dst_sel:WORD_1 dst_unused:UNUSED_PRESERVE src0_sel:WORD_1
	v_pk_add_f16 v18, v61, v46 neg_lo:[0,1] neg_hi:[0,1]
	v_pk_add_f16 v17, v17, v25
	v_pk_add_f16 v16, v16, v24
	v_pk_add_f16 v15, v15, v23
	v_pk_add_f16 v14, v14, v22
	v_pk_fma_f16 v13, v33, v25, v13
	v_pk_fma_f16 v12, v32, v24, v12
	v_pk_fma_f16 v11, v31, v23, v11
	v_pk_fma_f16 v10, v30, v22, v10
	v_pk_add_f16 v19, v60, v47 neg_lo:[0,1] neg_hi:[0,1]
	v_pk_add_f16 v20, v59, v48 neg_lo:[0,1] neg_hi:[0,1]
	v_pk_add_f16 v21, v58, v49 neg_lo:[0,1] neg_hi:[0,1]
	v_exp_f16_sdwa v30, v6 dst_sel:WORD_0 dst_unused:UNUSED_PAD src0_sel:WORD_0
	v_exp_f16_sdwa v31, v7 dst_sel:WORD_0 dst_unused:UNUSED_PAD src0_sel:WORD_0
	v_exp_f16_sdwa v32, v8 dst_sel:WORD_0 dst_unused:UNUSED_PAD src0_sel:WORD_0
	v_exp_f16_sdwa v33, v9 dst_sel:WORD_0 dst_unused:UNUSED_PAD src0_sel:WORD_0
	v_exp_f16_sdwa v30, v6 dst_sel:WORD_1 dst_unused:UNUSED_PRESERVE src0_sel:WORD_1
	v_exp_f16_sdwa v31, v7 dst_sel:WORD_1 dst_unused:UNUSED_PRESERVE src0_sel:WORD_1
	v_exp_f16_sdwa v32, v8 dst_sel:WORD_1 dst_unused:UNUSED_PRESERVE src0_sel:WORD_1
	v_exp_f16_sdwa v33, v9 dst_sel:WORD_1 dst_unused:UNUSED_PRESERVE src0_sel:WORD_1
	v_exp_f16_sdwa v22, v18 dst_sel:WORD_0 dst_unused:UNUSED_PAD src0_sel:WORD_0
	v_exp_f16_sdwa v23, v19 dst_sel:WORD_0 dst_unused:UNUSED_PAD src0_sel:WORD_0
	v_exp_f16_sdwa v24, v20 dst_sel:WORD_0 dst_unused:UNUSED_PAD src0_sel:WORD_0
	v_exp_f16_sdwa v25, v21 dst_sel:WORD_0 dst_unused:UNUSED_PAD src0_sel:WORD_0
	v_exp_f16_sdwa v22, v18 dst_sel:WORD_1 dst_unused:UNUSED_PRESERVE src0_sel:WORD_1
	v_exp_f16_sdwa v23, v19 dst_sel:WORD_1 dst_unused:UNUSED_PRESERVE src0_sel:WORD_1
	v_exp_f16_sdwa v24, v20 dst_sel:WORD_1 dst_unused:UNUSED_PRESERVE src0_sel:WORD_1
	v_exp_f16_sdwa v25, v21 dst_sel:WORD_1 dst_unused:UNUSED_PRESERVE src0_sel:WORD_1
	v_pk_add_f16 v18, v34, v46 neg_lo:[0,1] neg_hi:[0,1]
	v_pk_add_f16 v14, v14, v22
	v_pk_add_f16 v15, v15, v23
	v_pk_add_f16 v16, v16, v24
	v_pk_add_f16 v17, v17, v25
	v_pk_fma_f16 v10, v42, v22, v10
	v_pk_fma_f16 v11, v43, v23, v11
	v_pk_fma_f16 v12, v44, v24, v12
	v_pk_fma_f16 v13, v45, v25, v13
	v_pk_add_f16 v19, v35, v47 neg_lo:[0,1] neg_hi:[0,1]
	v_pk_add_f16 v20, v36, v48 neg_lo:[0,1] neg_hi:[0,1]
	v_pk_add_f16 v21, v37, v49 neg_lo:[0,1] neg_hi:[0,1]
	v_exp_f16_sdwa v22, v18 dst_sel:WORD_0 dst_unused:UNUSED_PAD src0_sel:WORD_0
	v_exp_f16_sdwa v23, v19 dst_sel:WORD_0 dst_unused:UNUSED_PAD src0_sel:WORD_0
	v_exp_f16_sdwa v24, v20 dst_sel:WORD_0 dst_unused:UNUSED_PAD src0_sel:WORD_0
	v_exp_f16_sdwa v25, v21 dst_sel:WORD_0 dst_unused:UNUSED_PAD src0_sel:WORD_0
	v_exp_f16_sdwa v22, v18 dst_sel:WORD_1 dst_unused:UNUSED_PRESERVE src0_sel:WORD_1
	v_exp_f16_sdwa v23, v19 dst_sel:WORD_1 dst_unused:UNUSED_PRESERVE src0_sel:WORD_1
	v_exp_f16_sdwa v24, v20 dst_sel:WORD_1 dst_unused:UNUSED_PRESERVE src0_sel:WORD_1
	v_exp_f16_sdwa v25, v21 dst_sel:WORD_1 dst_unused:UNUSED_PRESERVE src0_sel:WORD_1
	v_pk_add_f16 v18, v69, v46 neg_lo:[0,1] neg_hi:[0,1]
	v_pk_add_f16 v17, v17, v25
	v_pk_add_f16 v16, v16, v24
	v_pk_add_f16 v15, v15, v23
	v_pk_add_f16 v14, v14, v22
	v_pk_fma_f16 v13, v65, v25, v13
	v_pk_fma_f16 v12, v64, v24, v12
	v_pk_fma_f16 v11, v63, v23, v11
	v_pk_fma_f16 v10, v62, v22, v10
	v_pk_add_f16 v19, v68, v47 neg_lo:[0,1] neg_hi:[0,1]
	v_pk_add_f16 v20, v67, v48 neg_lo:[0,1] neg_hi:[0,1]
	v_pk_add_f16 v21, v66, v49 neg_lo:[0,1] neg_hi:[0,1]
	v_exp_f16_sdwa v22, v18 dst_sel:WORD_0 dst_unused:UNUSED_PAD src0_sel:WORD_0
	v_exp_f16_sdwa v23, v19 dst_sel:WORD_0 dst_unused:UNUSED_PAD src0_sel:WORD_0
	v_exp_f16_sdwa v24, v20 dst_sel:WORD_0 dst_unused:UNUSED_PAD src0_sel:WORD_0
	v_exp_f16_sdwa v25, v21 dst_sel:WORD_0 dst_unused:UNUSED_PAD src0_sel:WORD_0
	v_exp_f16_sdwa v22, v18 dst_sel:WORD_1 dst_unused:UNUSED_PRESERVE src0_sel:WORD_1
	v_exp_f16_sdwa v23, v19 dst_sel:WORD_1 dst_unused:UNUSED_PRESERVE src0_sel:WORD_1
	v_exp_f16_sdwa v24, v20 dst_sel:WORD_1 dst_unused:UNUSED_PRESERVE src0_sel:WORD_1
	v_exp_f16_sdwa v25, v21 dst_sel:WORD_1 dst_unused:UNUSED_PRESERVE src0_sel:WORD_1
	v_pk_add_f16 v18, v73, v46 neg_lo:[0,1] neg_hi:[0,1]
	v_pk_add_f16 v14, v14, v22
	v_pk_add_f16 v15, v15, v23
	v_pk_add_f16 v16, v16, v24
	v_pk_add_f16 v17, v17, v25
	v_pk_fma_f16 v10, v82, v22, v10
	v_pk_fma_f16 v11, v83, v23, v11
	v_pk_fma_f16 v12, v84, v24, v12
	v_pk_fma_f16 v13, v85, v25, v13
	v_pk_add_f16 v19, v72, v47 neg_lo:[0,1] neg_hi:[0,1]
	v_pk_add_f16 v20, v71, v48 neg_lo:[0,1] neg_hi:[0,1]
	v_pk_add_f16 v21, v70, v49 neg_lo:[0,1] neg_hi:[0,1]
	v_exp_f16_sdwa v22, v18 dst_sel:WORD_0 dst_unused:UNUSED_PAD src0_sel:WORD_0
	v_exp_f16_sdwa v23, v19 dst_sel:WORD_0 dst_unused:UNUSED_PAD src0_sel:WORD_0
	v_exp_f16_sdwa v24, v20 dst_sel:WORD_0 dst_unused:UNUSED_PAD src0_sel:WORD_0
	v_exp_f16_sdwa v25, v21 dst_sel:WORD_0 dst_unused:UNUSED_PAD src0_sel:WORD_0
	v_exp_f16_sdwa v22, v18 dst_sel:WORD_1 dst_unused:UNUSED_PRESERVE src0_sel:WORD_1
	v_exp_f16_sdwa v23, v19 dst_sel:WORD_1 dst_unused:UNUSED_PRESERVE src0_sel:WORD_1
	v_exp_f16_sdwa v24, v20 dst_sel:WORD_1 dst_unused:UNUSED_PRESERVE src0_sel:WORD_1
	v_exp_f16_sdwa v25, v21 dst_sel:WORD_1 dst_unused:UNUSED_PRESERVE src0_sel:WORD_1
	s_nop 0
	v_pk_add_f16 v17, v17, v25
	v_pk_add_f16 v16, v16, v24
	v_pk_add_f16 v15, v15, v23
	v_pk_add_f16 v14, v14, v22
	v_pk_fma_f16 v21, v105, v25, v13
	v_pk_fma_f16 v20, v104, v24, v12
	v_pk_fma_f16 v19, v103, v23, v11
	v_pk_fma_f16 v18, v102, v22, v10
	v_mov_b32_e32 v13, v5
	v_mov_b32_e32 v12, v4
	v_mov_b32_e32 v11, v3
	v_mov_b32_e32 v10, v2
.LBB4_80:
	v_lshlrev_b64 v[6:7], 9, v[168:169]
	v_or_b32_e32 v6, v6, v198
	v_lshl_add_u64 v[2:3], s[20:21], 0, v[6:7]
	global_load_dwordx4 v[2:5], v[2:3], off nt
	v_lshl_add_u64 v[6:7], s[22:23], 0, v[6:7]
	global_load_dwordx4 v[6:9], v[6:7], off nt
	v_add_u32_e32 v168, v185, v199
	v_lshlrev_b64 v[26:27], 9, v[168:169]
	v_or_b32_e32 v26, v26, v198
	v_lshl_add_u64 v[22:23], s[20:21], 0, v[26:27]
	global_load_dwordx4 v[22:25], v[22:23], off nt
	v_lshl_add_u64 v[26:27], s[22:23], 0, v[26:27]
	global_load_dwordx4 v[26:29], v[26:27], off nt
	v_pk_add_f16 v17, v17, v33
	v_pk_add_f16 v16, v16, v32
	v_pk_add_f16 v15, v15, v31
	v_pk_add_f16 v14, v14, v30
	v_pk_fma_f16 v42, v13, v33, v21
	v_pk_fma_f16 v43, v12, v32, v20
	v_rcp_f16_e32 v12, v14
	v_rcp_f16_sdwa v13, v14 dst_sel:DWORD dst_unused:UNUSED_PAD src0_sel:WORD_1
	v_rcp_f16_e32 v14, v15
	v_rcp_f16_sdwa v15, v15 dst_sel:DWORD dst_unused:UNUSED_PAD src0_sel:WORD_1
	v_rcp_f16_e32 v46, v16
	v_rcp_f16_sdwa v16, v16 dst_sel:DWORD dst_unused:UNUSED_PAD src0_sel:WORD_1
	v_rcp_f16_e32 v47, v17
	v_rcp_f16_sdwa v17, v17 dst_sel:DWORD dst_unused:UNUSED_PAD src0_sel:WORD_1
	v_add_u32_e32 v168, v187, v199
	v_pk_fma_f16 v44, v10, v30, v18
	v_pk_fma_f16 v45, v11, v31, v19
	v_lshlrev_b64 v[10:11], 9, v[168:169]
	v_or_b32_e32 v10, v10, v198
	v_lshl_add_u64 v[38:39], s[20:21], 0, v[10:11]
	v_lshl_add_u64 v[40:41], s[22:23], 0, v[10:11]
	v_pack_b32_f16 v48, v14, v15
	v_pack_b32_f16 v49, v12, v13
	v_pack_b32_f16 v46, v46, v16
	v_pack_b32_f16 v47, v47, v17
	global_load_dwordx4 v[10:13], v[38:39], off nt
	global_load_dwordx4 v[14:17], v[40:41], off nt
	v_cvt_f32_f16_sdwa v21, v139 dst_sel:DWORD dst_unused:UNUSED_PAD src0_sel:WORD_1
	v_cvt_f32_f16_e32 v20, v139
	v_cvt_f32_f16_sdwa v19, v138 dst_sel:DWORD dst_unused:UNUSED_PAD src0_sel:WORD_1
	v_cvt_f32_f16_e32 v18, v138
	v_cvt_f32_f16_sdwa v33, v141 dst_sel:DWORD dst_unused:UNUSED_PAD src0_sel:WORD_1
	v_cvt_f32_f16_e32 v32, v141
	v_pk_mul_f16 v58, v43, v46
	v_pk_mul_f16 v59, v42, v47
	v_cvt_f32_f16_sdwa v31, v140 dst_sel:DWORD dst_unused:UNUSED_PAD src0_sel:WORD_1
	v_cvt_f32_f16_e32 v30, v140
	v_pk_mul_f16 v52, v45, v48
	v_pk_mul_f16 v53, v44, v49
	v_add_u32_e32 v168, v190, v199
	v_lshlrev_b64 v[36:37], 9, v[168:169]
	v_or_b32_e32 v36, v36, v198
	v_lshl_or_b32 v50, s46, 6, v178
	v_lshlrev_b32_e32 v51, 9, v50
	v_add_u32_e32 v203, v184, v51
	v_cvt_f32_f16_sdwa v35, v77 dst_sel:DWORD dst_unused:UNUSED_PAD src0_sel:WORD_1
	v_cvt_f32_f16_e32 v34, v77
	v_add_lshl_u32 v202, v188, v50, 9
	s_mov_b64 s[4:5], -1
	s_and_b64 vcc, exec, s[26:27]
	s_waitcnt vmcnt(5)
	v_cvt_f32_f16_e32 v38, v2
	v_cvt_f32_f16_sdwa v39, v2 dst_sel:DWORD dst_unused:UNUSED_PAD src0_sel:WORD_1
	v_cvt_f32_f16_e32 v2, v3
	v_cvt_f32_f16_sdwa v3, v3 dst_sel:DWORD dst_unused:UNUSED_PAD src0_sel:WORD_1
	s_waitcnt vmcnt(4)
	v_cvt_f32_f16_e32 v40, v6
	v_cvt_f32_f16_sdwa v41, v6 dst_sel:DWORD dst_unused:UNUSED_PAD src0_sel:WORD_1
	v_cvt_f32_f16_e32 v6, v7
	v_cvt_f32_f16_sdwa v7, v7 dst_sel:DWORD dst_unused:UNUSED_PAD src0_sel:WORD_1
	v_cvt_f32_f16_e32 v42, v4
	v_cvt_f32_f16_sdwa v43, v4 dst_sel:DWORD dst_unused:UNUSED_PAD src0_sel:WORD_1
	v_cvt_f32_f16_e32 v4, v5
	v_cvt_f32_f16_sdwa v5, v5 dst_sel:DWORD dst_unused:UNUSED_PAD src0_sel:WORD_1
	v_cvt_f32_f16_e32 v44, v8
	v_cvt_f32_f16_sdwa v45, v8 dst_sel:DWORD dst_unused:UNUSED_PAD src0_sel:WORD_1
	v_cvt_f32_f16_e32 v8, v9
	v_cvt_f32_f16_sdwa v9, v9 dst_sel:DWORD dst_unused:UNUSED_PAD src0_sel:WORD_1
	v_pk_add_f32 v[2:3], v[20:21], v[2:3]
	v_pk_add_f32 v[18:19], v[18:19], v[38:39]
	v_pk_add_f32 v[4:5], v[32:33], v[4:5]
	v_pk_add_f32 v[6:7], v[2:3], v[6:7]
	v_pk_add_f32 v[20:21], v[30:31], v[42:43]
	v_pk_add_f32 v[18:19], v[18:19], v[40:41]
	v_pk_add_f32 v[8:9], v[4:5], v[8:9]
	v_cvt_pk_f16_f32 v3, v6, v7
	v_lshl_add_u64 v[6:7], s[20:21], 0, v[36:37]
	v_pk_add_f32 v[20:21], v[20:21], v[44:45]
	v_cvt_pk_f16_f32 v2, v18, v19
	v_cvt_pk_f16_f32 v5, v8, v9
	global_load_dwordx4 v[6:9], v[6:7], off nt
	v_lshl_add_u64 v[18:19], s[22:23], 0, v[36:37]
	v_cvt_pk_f16_f32 v4, v20, v21
	global_load_dwordx4 v[18:21], v[18:19], off nt
	s_waitcnt vmcnt(5)
	v_cvt_f32_f16_e32 v46, v22
	v_cvt_f32_f16_sdwa v47, v22 dst_sel:DWORD dst_unused:UNUSED_PAD src0_sel:WORD_1
	ds_write_b128 v203, v[2:5]
	v_cvt_f32_f16_sdwa v5, v76 dst_sel:DWORD dst_unused:UNUSED_PAD src0_sel:WORD_1
	v_cvt_f32_f16_e32 v4, v76
	v_cvt_f32_f16_e32 v22, v23
	v_cvt_f32_f16_sdwa v23, v23 dst_sel:DWORD dst_unused:UNUSED_PAD src0_sel:WORD_1
	s_waitcnt vmcnt(4)
	v_cvt_f32_f16_e32 v48, v26
	v_cvt_f32_f16_sdwa v49, v26 dst_sel:DWORD dst_unused:UNUSED_PAD src0_sel:WORD_1
	v_cvt_f32_f16_e32 v26, v27
	v_cvt_f32_f16_sdwa v27, v27 dst_sel:DWORD dst_unused:UNUSED_PAD src0_sel:WORD_1
	v_cvt_f32_f16_sdwa v31, v75 dst_sel:DWORD dst_unused:UNUSED_PAD src0_sel:WORD_1
	v_cvt_f32_f16_e32 v30, v75
	v_cvt_f32_f16_e32 v32, v24
	v_cvt_f32_f16_sdwa v33, v24 dst_sel:DWORD dst_unused:UNUSED_PAD src0_sel:WORD_1
	v_pk_add_f32 v[4:5], v[4:5], v[22:23]
	v_cvt_f32_f16_e32 v22, v28
	v_pk_add_f32 v[4:5], v[4:5], v[26:27]
	v_cvt_f32_f16_sdwa v23, v28 dst_sel:DWORD dst_unused:UNUSED_PAD src0_sel:WORD_1
	v_cvt_f32_f16_sdwa v27, v74 dst_sel:DWORD dst_unused:UNUSED_PAD src0_sel:WORD_1
	v_cvt_f32_f16_e32 v26, v74
	v_cvt_f32_f16_e32 v24, v25
	v_cvt_f32_f16_sdwa v25, v25 dst_sel:DWORD dst_unused:UNUSED_PAD src0_sel:WORD_1
	v_pk_add_f32 v[2:3], v[34:35], v[46:47]
	v_cvt_f32_f16_e32 v28, v29
	v_cvt_f32_f16_sdwa v29, v29 dst_sel:DWORD dst_unused:UNUSED_PAD src0_sel:WORD_1
	v_pk_add_f32 v[2:3], v[2:3], v[48:49]
	s_nop 0
	v_cvt_pk_f16_f32 v2, v2, v3
	v_cvt_pk_f16_f32 v3, v4, v5
	v_pk_add_f32 v[4:5], v[30:31], v[32:33]
	s_nop 0
	v_pk_add_f32 v[4:5], v[4:5], v[22:23]
	v_pk_add_f32 v[22:23], v[26:27], v[24:25]
	v_cvt_pk_f16_f32 v4, v4, v5
	v_pk_add_f32 v[22:23], v[22:23], v[28:29]
	s_waitcnt vmcnt(3)
	v_cvt_f32_f16_e32 v24, v10
	v_cvt_pk_f16_f32 v5, v22, v23
	v_add_u32_e32 v22, v186, v50
	v_lshlrev_b32_e32 v204, 9, v22
	v_bitop3_b32 v22, v22, v179, 15 bitop3:0x6c
	v_lshlrev_b32_e32 v205, 4, v22
	v_cvt_f32_f16_sdwa v25, v10 dst_sel:DWORD dst_unused:UNUSED_PAD src0_sel:WORD_1
	v_or_b32_e32 v10, v205, v204
	v_cvt_f32_f16_sdwa v23, v57 dst_sel:DWORD dst_unused:UNUSED_PAD src0_sel:WORD_1
	v_cvt_f32_f16_e32 v22, v57
	ds_write_b128 v10, v[2:5]
	v_cvt_f32_f16_sdwa v5, v56 dst_sel:DWORD dst_unused:UNUSED_PAD src0_sel:WORD_1
	v_cvt_f32_f16_e32 v4, v56
	v_cvt_f32_f16_e32 v10, v11
	v_cvt_f32_f16_sdwa v11, v11 dst_sel:DWORD dst_unused:UNUSED_PAD src0_sel:WORD_1
	s_waitcnt vmcnt(2)
	v_cvt_f32_f16_e32 v26, v14
	v_cvt_f32_f16_sdwa v27, v14 dst_sel:DWORD dst_unused:UNUSED_PAD src0_sel:WORD_1
	v_cvt_f32_f16_e32 v14, v15
	v_cvt_f32_f16_sdwa v15, v15 dst_sel:DWORD dst_unused:UNUSED_PAD src0_sel:WORD_1
	v_pk_add_f32 v[2:3], v[22:23], v[24:25]
	v_cvt_f32_f16_sdwa v23, v55 dst_sel:DWORD dst_unused:UNUSED_PAD src0_sel:WORD_1
	v_cvt_f32_f16_e32 v22, v55
	v_cvt_f32_f16_e32 v24, v12
	v_cvt_f32_f16_sdwa v25, v12 dst_sel:DWORD dst_unused:UNUSED_PAD src0_sel:WORD_1
	v_pk_add_f32 v[4:5], v[4:5], v[10:11]
	v_cvt_f32_f16_e32 v10, v16
	v_pk_add_f32 v[4:5], v[4:5], v[14:15]
	v_cvt_f32_f16_sdwa v11, v16 dst_sel:DWORD dst_unused:UNUSED_PAD src0_sel:WORD_1
	v_cvt_f32_f16_sdwa v15, v54 dst_sel:DWORD dst_unused:UNUSED_PAD src0_sel:WORD_1
	v_cvt_f32_f16_e32 v14, v54
	v_cvt_f32_f16_e32 v12, v13
	v_cvt_f32_f16_sdwa v13, v13 dst_sel:DWORD dst_unused:UNUSED_PAD src0_sel:WORD_1
	v_cvt_f32_f16_e32 v16, v17
	v_cvt_f32_f16_sdwa v17, v17 dst_sel:DWORD dst_unused:UNUSED_PAD src0_sel:WORD_1
	v_pk_add_f32 v[2:3], v[2:3], v[26:27]
	s_nop 0
	v_cvt_pk_f16_f32 v2, v2, v3
	v_cvt_pk_f16_f32 v3, v4, v5
	v_pk_add_f32 v[4:5], v[22:23], v[24:25]
	s_nop 0
	v_pk_add_f32 v[4:5], v[4:5], v[10:11]
	v_pk_add_f32 v[10:11], v[14:15], v[12:13]
	v_cvt_pk_f16_f32 v4, v4, v5
	v_pk_add_f32 v[10:11], v[10:11], v[16:17]
	s_waitcnt vmcnt(1)
	v_cvt_f32_f16_e32 v12, v6
	v_cvt_pk_f16_f32 v5, v10, v11
	v_cvt_f32_f16_e32 v10, v53
	v_cvt_f32_f16_sdwa v11, v53 dst_sel:DWORD dst_unused:UNUSED_PAD src0_sel:WORD_1
	v_cvt_f32_f16_sdwa v13, v6 dst_sel:DWORD dst_unused:UNUSED_PAD src0_sel:WORD_1
	s_waitcnt vmcnt(0)
	v_cvt_f32_f16_e32 v14, v18
	v_cvt_f32_f16_sdwa v15, v18 dst_sel:DWORD dst_unused:UNUSED_PAD src0_sel:WORD_1
	v_or_b32_e32 v6, v189, v202
	ds_write_b128 v6, v[2:5]
	v_cvt_f32_f16_e32 v4, v52
	v_cvt_f32_f16_sdwa v5, v52 dst_sel:DWORD dst_unused:UNUSED_PAD src0_sel:WORD_1
	v_cvt_f32_f16_e32 v6, v7
	v_cvt_f32_f16_sdwa v7, v7 dst_sel:DWORD dst_unused:UNUSED_PAD src0_sel:WORD_1
	v_pk_add_f32 v[2:3], v[10:11], v[12:13]
	v_cvt_f32_f16_e32 v10, v19
	v_cvt_f32_f16_sdwa v11, v19 dst_sel:DWORD dst_unused:UNUSED_PAD src0_sel:WORD_1
	v_pk_add_f32 v[2:3], v[2:3], v[14:15]
	v_cvt_f32_f16_e32 v12, v58
	v_cvt_f32_f16_sdwa v13, v58 dst_sel:DWORD dst_unused:UNUSED_PAD src0_sel:WORD_1
	v_cvt_f32_f16_e32 v14, v8
	v_cvt_f32_f16_sdwa v15, v8 dst_sel:DWORD dst_unused:UNUSED_PAD src0_sel:WORD_1
	v_pk_add_f32 v[4:5], v[4:5], v[6:7]
	v_cvt_f32_f16_e32 v6, v20
	v_pk_add_f32 v[4:5], v[4:5], v[10:11]
	v_cvt_f32_f16_sdwa v7, v20 dst_sel:DWORD dst_unused:UNUSED_PAD src0_sel:WORD_1
	v_cvt_f32_f16_e32 v10, v59
	v_cvt_f32_f16_sdwa v11, v59 dst_sel:DWORD dst_unused:UNUSED_PAD src0_sel:WORD_1
	v_cvt_f32_f16_e32 v8, v9
	v_cvt_f32_f16_sdwa v9, v9 dst_sel:DWORD dst_unused:UNUSED_PAD src0_sel:WORD_1
	v_cvt_pk_f16_f32 v2, v2, v3
	v_cvt_pk_f16_f32 v3, v4, v5
	v_pk_add_f32 v[4:5], v[12:13], v[14:15]
	v_cvt_f32_f16_e32 v12, v21
	v_cvt_f32_f16_sdwa v13, v21 dst_sel:DWORD dst_unused:UNUSED_PAD src0_sel:WORD_1
	v_pk_add_f32 v[4:5], v[4:5], v[6:7]
	v_pk_add_f32 v[6:7], v[10:11], v[8:9]
	v_cvt_pk_f16_f32 v4, v4, v5
	v_pk_add_f32 v[6:7], v[6:7], v[12:13]
	s_nop 0
	v_cvt_pk_f16_f32 v5, v6, v7
	v_add_lshl_u32 v6, v191, v50, 9
	v_add_u32_e32 v168, v192, v6
	ds_write_b128 v168, v[2:5]
	global_load_dwordx4 v[2:5], v[174:175], off
	global_load_dwordx4 v[8:11], v[176:177], off
	global_load_dwordx4 v[12:15], v[174:175], off offset:16
	global_load_dwordx4 v[16:19], v[176:177], off offset:16
	s_cbranch_vccz .LBB4_118
	global_load_dwordx3 v[154:156], v169, s[18:19]
	s_mov_b32 s14, s38
	s_mov_b32 s15, s39
	v_cmp_lt_u32_e64 s[64:65], 0, v199
	v_cmp_gt_u32_e64 s[66:67], 63, v199
	v_cmp_lt_u32_e64 s[68:69], 0, v180
	v_cmp_gt_u32_e64 s[70:71], 60, v180
	buffer_load_dwordx4 v[210:213], v200, s[12:15], 0 offen sc1
	s_and_b64 s[72:73], s[68:69], s[64:65]
	s_and_b64 s[74:75], s[68:69], s[66:67]
	s_and_b64 s[76:77], s[70:71], s[64:65]
	s_and_b64 s[78:79], s[70:71], s[66:67]
	v_add_u32_e32 v245, 0xfffe7c00, v200
	v_add_u32_e32 v246, 0xfffe8000, v200
	s_mov_b64 exec, s[72:73]
	buffer_load_dwordx4 v[122:125], v245, s[12:15], 0 offen
	buffer_load_dwordx4 v[82:85], v245, s[12:15], 0 offen offset:512
	s_mov_b64 exec, -1
	s_mov_b64 exec, s[68:69]
	buffer_load_dwordx4 v[138:141], v246, s[12:15], 0 offen offset:512
	buffer_load_dwordx4 v[106:109], v246, s[12:15], 0 offen offset:1024
	s_mov_b64 exec, -1
	s_mov_b64 exec, s[74:75]
	buffer_load_dwordx4 v[146:149], v246, s[12:15], 0 offen offset:2048
	buffer_load_dwordx4 v[126:129], v246, s[12:15], 0 offen offset:2560
	s_mov_b64 exec, -1
	v_add_u32_e32 v245, 0xfffffc00, v200
	s_mov_b64 exec, s[64:65]
	buffer_load_dwordx4 v[94:97], v245, s[12:15], 0 offen
	buffer_load_dwordx4 v[54:57], v245, s[12:15], 0 offen offset:512
	s_mov_b64 exec, -1
	buffer_load_dwordx4 v[118:121], v200, s[12:15], 0 offen offset:512
	buffer_load_dwordx4 v[74:77], v200, s[12:15], 0 offen offset:1024
	s_mov_b64 exec, s[66:67]
	buffer_load_dwordx4 v[134:137], v200, s[12:15], 0 offen offset:2048
	buffer_load_dwordx4 v[98:101], v200, s[12:15], 0 offen offset:2560
	s_mov_b64 exec, -1
	v_add_u32_e32 v245, 0x17c00, v200
	v_add_u32_e32 v246, 0x18000, v200
	s_mov_b64 exec, s[64:65]
	buffer_load_dwordx4 v[62:65], v245, s[12:15], 0 offen
	buffer_load_dwordx4 v[30:33], v245, s[12:15], 0 offen offset:512
	s_mov_b64 exec, -1
	buffer_load_dwordx4 v[78:81], v246, s[12:15], 0 offen offset:512
	buffer_load_dwordx4 v[42:45], v246, s[12:15], 0 offen offset:1024
	s_mov_b64 exec, s[66:67]
	buffer_load_dwordx4 v[102:105], v246, s[12:15], 0 offen offset:2048
	buffer_load_dwordx4 v[58:61], v246, s[12:15], 0 offen offset:2560
	s_mov_b64 exec, -1
	v_add_u32_e32 v245, 0x18000, v200
	buffer_load_dwordx4 v[162:165], v245, s[12:15], 0 offen sc1
	v_add_u32_e32 v246, 0x30000, v200
	buffer_load_dwordx4 v[158:161], v246, s[12:15], 0 offen sc1
	v_add_u32_e32 v245, 0x2fc00, v200
	v_add_u32_e32 v246, 0x30000, v200
	v_add_u32_e32 v247, 0x47c00, v200
	v_add_u32_e32 v248, 0x48000, v200
	v_add_u32_e32 v249, 0x5fc00, v200
	v_add_u32_e32 v250, 0x60000, v200
	s_waitcnt vmcnt(22)
	v_cvt_pk_f16_f32 v6, v2, v3
	v_cvt_pk_f16_f32 v2, v8, v9
	v_cvt_pk_f16_f32 v7, v4, v5
	v_cvt_pk_f16_f32 v3, v10, v11
	v_cvt_pk_f16_f32 v8, v12, v13
	v_cvt_pk_f16_f32 v4, v16, v17
	v_cvt_pk_f16_f32 v9, v14, v15
	v_cvt_pk_f16_f32 v5, v18, v19
	s_not_b64 exec, s[72:73]
	s_cbranch_execz .Lmyf_C3_0
	v_mov_b32_e32 v122, v6
	v_mov_b32_e32 v123, v7
	v_mov_b32_e32 v124, v8
	v_mov_b32_e32 v125, v9
	v_mov_b32_e32 v82, v2
	v_mov_b32_e32 v83, v3
	v_mov_b32_e32 v84, v4
	v_mov_b32_e32 v85, v5

.Lmyf_C3_7:
	s_mov_b64 exec, -1
	s_waitcnt vmcnt(21)
	v_cvt_f16_f32_e32 v206, v155
	v_cvt_f16_f32_e32 v208, v154
	v_cvt_f16_f32_e32 v207, v156
	v_add_u32_e32 v251, 0x48000, v200
	buffer_load_dwordx4 v[154:157], v251, s[12:15], 0 offen sc1
	s_mov_b64 s[4:5], 0
	s_waitcnt vmcnt(3)
	v_pk_mul_f16 v216, v208, v213 op_sel_hi:[0,1]
	v_pk_mul_f16 v220, v206, v213 op_sel_hi:[0,1]
	v_pk_mul_f16 v224, v207, v213 op_sel_hi:[0,1]
	v_pk_mul_f16 v209, v208, v210 op_sel_hi:[0,1]
	v_pk_mul_f16 v214, v208, v211 op_sel_hi:[0,1]
	v_pk_mul_f16 v215, v208, v212 op_sel_hi:[0,1]
	v_pk_mul_f16 v217, v206, v210 op_sel_hi:[0,1]
	s_mov_b64 exec, s[64:65]
	buffer_load_dwordx4 v[34:37], v245, s[12:15], 0 offen
	buffer_load_dwordx4 v[18:21], v245, s[12:15], 0 offen offset:512
	s_mov_b64 exec, -1
	v_pk_mul_f16 v218, v206, v211 op_sel_hi:[0,1]
	v_pk_mul_f16 v219, v206, v212 op_sel_hi:[0,1]
	v_pk_mul_f16 v221, v207, v210 op_sel_hi:[0,1]
	v_pk_mul_f16 v222, v207, v211 op_sel_hi:[0,1]
	v_pk_mul_f16 v223, v207, v212 op_sel_hi:[0,1]
	v_pk_fma_f16 v125, v125, v213, v216
	v_pk_fma_f16 v141, v141, v213, v220
	v_pk_fma_f16 v149, v149, v213, v224
	v_pk_fma_f16 v225, v97, v213, v216
	v_pk_fma_f16 v229, v121, v213, v220
	v_pk_fma_f16 v233, v137, v213, v224
	v_pk_fma_f16 v216, v65, v213, v216
	v_pk_fma_f16 v220, v81, v213, v220
	buffer_load_dwordx4 v[46:49], v246, s[12:15], 0 offen offset:512
	buffer_load_dwordx4 v[22:25], v246, s[12:15], 0 offen offset:1024
	v_pk_fma_f16 v213, v105, v213, v224
	v_pk_maximum3_f16 v224, v125, v141, v149
	v_pk_fma_f16 v124, v124, v212, v215
	v_pk_fma_f16 v123, v123, v211, v214
	v_pk_fma_f16 v122, v122, v210, v209
	v_pk_fma_f16 v140, v140, v212, v219
	v_pk_fma_f16 v139, v139, v211, v218
	v_pk_fma_f16 v138, v138, v210, v217
	v_pk_fma_f16 v148, v148, v212, v223
	v_pk_fma_f16 v147, v147, v211, v222
	v_pk_fma_f16 v146, v146, v210, v221
	v_pk_fma_f16 v226, v96, v212, v215
	v_pk_fma_f16 v227, v95, v211, v214
	v_pk_fma_f16 v228, v94, v210, v209
	v_pk_fma_f16 v230, v120, v212, v219
	v_pk_fma_f16 v231, v119, v211, v218
	s_mov_b64 exec, s[66:67]
	buffer_load_dwordx4 v[66:69], v246, s[12:15], 0 offen offset:2048
	buffer_load_dwordx4 v[26:29], v246, s[12:15], 0 offen offset:2560
	s_mov_b64 exec, -1
	v_pk_fma_f16 v232, v118, v210, v217
	v_pk_fma_f16 v234, v136, v212, v223
	v_pk_fma_f16 v235, v135, v211, v222
	v_pk_fma_f16 v236, v134, v210, v221
	v_pk_fma_f16 v215, v64, v212, v215
	v_pk_fma_f16 v214, v63, v211, v214
	v_pk_fma_f16 v209, v62, v210, v209
	v_pk_fma_f16 v219, v80, v212, v219
	v_pk_fma_f16 v218, v79, v211, v218
	v_pk_fma_f16 v217, v78, v210, v217
	v_pk_fma_f16 v212, v104, v212, v223
	v_pk_fma_f16 v211, v103, v211, v222
	v_pk_fma_f16 v210, v102, v210, v221
	v_pk_maximum3_f16 v221, v122, v138, v146
	v_pk_maximum3_f16 v222, v123, v139, v147
	v_pk_maximum3_f16 v223, v124, v140, v148
	v_pk_maximum3_f16 v240, v225, v229, v233
	v_pk_maximum3_f16 v244, v216, v220, v213
	v_pk_maximum3_f16 v237, v228, v232, v236
	v_pk_maximum3_f16 v238, v227, v231, v235
	v_pk_maximum3_f16 v239, v226, v230, v234
	v_pk_maximum3_f16 v241, v209, v217, v210
	v_pk_maximum3_f16 v242, v214, v218, v211
	v_pk_maximum3_f16 v224, v224, v240, v244
	v_pk_maximum3_f16 v243, v215, v219, v212
	v_pk_maximum3_f16 v221, v221, v237, v241
	v_pk_maximum3_f16 v222, v222, v238, v242
	v_pk_maximum3_f16 v223, v223, v239, v243
	v_pk_add_f16 v125, v125, v224 neg_lo:[0,1] neg_hi:[0,1]
	s_mov_b64 exec, s[64:65]
	buffer_load_dwordx4 v[86:89], v247, s[12:15], 0 offen
	buffer_load_dwordx4 v[38:41], v247, s[12:15], 0 offen offset:512
	s_mov_b64 exec, -1
	v_pk_add_f16 v122, v122, v221 neg_lo:[0,1] neg_hi:[0,1]
	v_pk_add_f16 v123, v123, v222 neg_lo:[0,1] neg_hi:[0,1]
	v_pk_add_f16 v124, v124, v223 neg_lo:[0,1] neg_hi:[0,1]
	v_pk_add_f16 v138, v138, v221 neg_lo:[0,1] neg_hi:[0,1]
	v_exp_f16_sdwa v237, v122 dst_sel:WORD_0 dst_unused:UNUSED_PAD src0_sel:WORD_0
	v_exp_f16_sdwa v238, v123 dst_sel:WORD_0 dst_unused:UNUSED_PAD src0_sel:WORD_0
	v_exp_f16_sdwa v239, v124 dst_sel:WORD_0 dst_unused:UNUSED_PAD src0_sel:WORD_0
	v_exp_f16_sdwa v240, v125 dst_sel:WORD_0 dst_unused:UNUSED_PAD src0_sel:WORD_0
	v_exp_f16_sdwa v237, v122 dst_sel:WORD_1 dst_unused:UNUSED_PRESERVE src0_sel:WORD_1
	v_exp_f16_sdwa v238, v123 dst_sel:WORD_1 dst_unused:UNUSED_PRESERVE src0_sel:WORD_1
	v_exp_f16_sdwa v239, v124 dst_sel:WORD_1 dst_unused:UNUSED_PRESERVE src0_sel:WORD_1
	v_exp_f16_sdwa v240, v125 dst_sel:WORD_1 dst_unused:UNUSED_PRESERVE src0_sel:WORD_1
	v_pk_add_f16 v139, v139, v222 neg_lo:[0,1] neg_hi:[0,1]
	v_pk_add_f16 v125, v237, 0
	v_pk_fma_f16 v85, v85, v240, 0
	v_pk_add_f16 v122, v240, 0
	v_pk_add_f16 v123, v239, 0
	v_pk_add_f16 v124, v238, 0
	v_pk_fma_f16 v84, v84, v239, 0
	v_pk_fma_f16 v83, v83, v238, 0
	v_pk_fma_f16 v82, v82, v237, 0
	v_pk_add_f16 v140, v140, v223 neg_lo:[0,1] neg_hi:[0,1]
	buffer_load_dwordx4 v[114:117], v248, s[12:15], 0 offen offset:512
	buffer_load_dwordx4 v[50:53], v248, s[12:15], 0 offen offset:1024
	v_pk_add_f16 v141, v141, v224 neg_lo:[0,1] neg_hi:[0,1]
	v_exp_f16_sdwa v237, v138 dst_sel:WORD_0 dst_unused:UNUSED_PAD src0_sel:WORD_0
	v_exp_f16_sdwa v238, v139 dst_sel:WORD_0 dst_unused:UNUSED_PAD src0_sel:WORD_0
	v_exp_f16_sdwa v239, v140 dst_sel:WORD_0 dst_unused:UNUSED_PAD src0_sel:WORD_0
	v_exp_f16_sdwa v240, v141 dst_sel:WORD_0 dst_unused:UNUSED_PAD src0_sel:WORD_0
	v_exp_f16_sdwa v237, v138 dst_sel:WORD_1 dst_unused:UNUSED_PRESERVE src0_sel:WORD_1
	v_exp_f16_sdwa v238, v139 dst_sel:WORD_1 dst_unused:UNUSED_PRESERVE src0_sel:WORD_1
	v_exp_f16_sdwa v239, v140 dst_sel:WORD_1 dst_unused:UNUSED_PRESERVE src0_sel:WORD_1
	v_exp_f16_sdwa v240, v141 dst_sel:WORD_1 dst_unused:UNUSED_PRESERVE src0_sel:WORD_1
	v_pk_add_f16 v125, v125, v237
	v_pk_fma_f16 v85, v109, v240, v85
	v_pk_add_f16 v109, v149, v224 neg_lo:[0,1] neg_hi:[0,1]
	v_pk_add_f16 v124, v124, v238
	v_pk_add_f16 v123, v123, v239
	v_pk_add_f16 v122, v122, v240
	v_pk_fma_f16 v82, v106, v237, v82
	v_pk_fma_f16 v83, v107, v238, v83
	v_pk_fma_f16 v84, v108, v239, v84
	v_pk_add_f16 v106, v146, v221 neg_lo:[0,1] neg_hi:[0,1]
	v_pk_add_f16 v107, v147, v222 neg_lo:[0,1] neg_hi:[0,1]
	v_pk_add_f16 v108, v148, v223 neg_lo:[0,1] neg_hi:[0,1]
	v_exp_f16_sdwa v138, v106 dst_sel:WORD_0 dst_unused:UNUSED_PAD src0_sel:WORD_0
	v_exp_f16_sdwa v139, v107 dst_sel:WORD_0 dst_unused:UNUSED_PAD src0_sel:WORD_0
	v_exp_f16_sdwa v140, v108 dst_sel:WORD_0 dst_unused:UNUSED_PAD src0_sel:WORD_0
	v_exp_f16_sdwa v141, v109 dst_sel:WORD_0 dst_unused:UNUSED_PAD src0_sel:WORD_0
	v_exp_f16_sdwa v138, v106 dst_sel:WORD_1 dst_unused:UNUSED_PRESERVE src0_sel:WORD_1
	v_exp_f16_sdwa v139, v107 dst_sel:WORD_1 dst_unused:UNUSED_PRESERVE src0_sel:WORD_1
	v_exp_f16_sdwa v140, v108 dst_sel:WORD_1 dst_unused:UNUSED_PRESERVE src0_sel:WORD_1
	v_exp_f16_sdwa v141, v109 dst_sel:WORD_1 dst_unused:UNUSED_PRESERVE src0_sel:WORD_1
	v_pk_add_f16 v109, v125, v138
	v_pk_add_f16 v106, v122, v141
	s_mov_b64 exec, s[66:67]
	buffer_load_dwordx4 v[130:133], v248, s[12:15], 0 offen offset:2048
	buffer_load_dwordx4 v[70:73], v248, s[12:15], 0 offen offset:2560
	s_mov_b64 exec, -1
	v_pk_add_f16 v107, v123, v140
	v_pk_add_f16 v108, v124, v139
	v_pk_fma_f16 v85, v129, v141, v85
	v_pk_fma_f16 v84, v128, v140, v84
	v_pk_fma_f16 v83, v127, v139, v83
	v_pk_fma_f16 v82, v126, v138, v82
	v_pk_add_f16 v122, v228, v221 neg_lo:[0,1] neg_hi:[0,1]
	v_pk_add_f16 v123, v227, v222 neg_lo:[0,1] neg_hi:[0,1]
	v_pk_add_f16 v124, v226, v223 neg_lo:[0,1] neg_hi:[0,1]
	v_pk_add_f16 v125, v225, v224 neg_lo:[0,1] neg_hi:[0,1]
	v_exp_f16_sdwa v126, v122 dst_sel:WORD_0 dst_unused:UNUSED_PAD src0_sel:WORD_0
	v_exp_f16_sdwa v127, v123 dst_sel:WORD_0 dst_unused:UNUSED_PAD src0_sel:WORD_0
	v_exp_f16_sdwa v128, v124 dst_sel:WORD_0 dst_unused:UNUSED_PAD src0_sel:WORD_0
	v_exp_f16_sdwa v129, v125 dst_sel:WORD_0 dst_unused:UNUSED_PAD src0_sel:WORD_0
	v_exp_f16_sdwa v126, v122 dst_sel:WORD_1 dst_unused:UNUSED_PRESERVE src0_sel:WORD_1
	v_exp_f16_sdwa v127, v123 dst_sel:WORD_1 dst_unused:UNUSED_PRESERVE src0_sel:WORD_1
	v_exp_f16_sdwa v128, v124 dst_sel:WORD_1 dst_unused:UNUSED_PRESERVE src0_sel:WORD_1
	v_exp_f16_sdwa v129, v125 dst_sel:WORD_1 dst_unused:UNUSED_PRESERVE src0_sel:WORD_1
	v_pk_add_f16 v122, v232, v221 neg_lo:[0,1] neg_hi:[0,1]
	v_pk_add_f16 v109, v109, v126
	v_pk_add_f16 v108, v108, v127
	v_pk_add_f16 v107, v107, v128
	s_mov_b64 exec, s[76:77]
	buffer_load_dwordx4 v[142:145], v249, s[12:15], 0 offen
	buffer_load_dwordx4 v[90:93], v249, s[12:15], 0 offen offset:512
	s_mov_b64 exec, -1
	v_pk_add_f16 v106, v106, v129
	v_pk_fma_f16 v82, v54, v126, v82
	v_pk_fma_f16 v83, v55, v127, v83
	v_pk_fma_f16 v84, v56, v128, v84
	v_pk_fma_f16 v85, v57, v129, v85
	v_pk_add_f16 v123, v231, v222 neg_lo:[0,1] neg_hi:[0,1]
	v_pk_add_f16 v124, v230, v223 neg_lo:[0,1] neg_hi:[0,1]
	v_pk_add_f16 v125, v229, v224 neg_lo:[0,1] neg_hi:[0,1]
	v_exp_f16_sdwa v126, v122 dst_sel:WORD_0 dst_unused:UNUSED_PAD src0_sel:WORD_0
	v_exp_f16_sdwa v127, v123 dst_sel:WORD_0 dst_unused:UNUSED_PAD src0_sel:WORD_0
	v_exp_f16_sdwa v128, v124 dst_sel:WORD_0 dst_unused:UNUSED_PAD src0_sel:WORD_0
	v_exp_f16_sdwa v129, v125 dst_sel:WORD_0 dst_unused:UNUSED_PAD src0_sel:WORD_0
	v_exp_f16_sdwa v126, v122 dst_sel:WORD_1 dst_unused:UNUSED_PRESERVE src0_sel:WORD_1
	v_exp_f16_sdwa v127, v123 dst_sel:WORD_1 dst_unused:UNUSED_PRESERVE src0_sel:WORD_1
	v_exp_f16_sdwa v128, v124 dst_sel:WORD_1 dst_unused:UNUSED_PRESERVE src0_sel:WORD_1
	v_exp_f16_sdwa v129, v125 dst_sel:WORD_1 dst_unused:UNUSED_PRESERVE src0_sel:WORD_1
	v_pk_add_f16 v122, v236, v221 neg_lo:[0,1] neg_hi:[0,1]
	v_pk_add_f16 v109, v109, v126
	v_pk_add_f16 v106, v106, v129
	v_pk_add_f16 v107, v107, v128
	v_pk_add_f16 v108, v108, v127
	v_pk_fma_f16 v85, v77, v129, v85
	v_pk_fma_f16 v84, v76, v128, v84
	s_mov_b64 exec, s[70:71]
	buffer_load_dwordx4 v[150:153], v250, s[12:15], 0 offen offset:512
	buffer_load_dwordx4 v[110:113], v250, s[12:15], 0 offen offset:1024
	s_mov_b64 exec, -1
	v_pk_fma_f16 v83, v75, v127, v83
	v_pk_fma_f16 v82, v74, v126, v82
	v_pk_add_f16 v123, v235, v222 neg_lo:[0,1] neg_hi:[0,1]
	v_pk_add_f16 v124, v234, v223 neg_lo:[0,1] neg_hi:[0,1]
	v_pk_add_f16 v125, v233, v224 neg_lo:[0,1] neg_hi:[0,1]
	v_exp_f16_sdwa v126, v122 dst_sel:WORD_0 dst_unused:UNUSED_PAD src0_sel:WORD_0
	v_exp_f16_sdwa v127, v123 dst_sel:WORD_0 dst_unused:UNUSED_PAD src0_sel:WORD_0
	v_exp_f16_sdwa v128, v124 dst_sel:WORD_0 dst_unused:UNUSED_PAD src0_sel:WORD_0
	v_exp_f16_sdwa v129, v125 dst_sel:WORD_0 dst_unused:UNUSED_PAD src0_sel:WORD_0
	v_exp_f16_sdwa v126, v122 dst_sel:WORD_1 dst_unused:UNUSED_PRESERVE src0_sel:WORD_1
	v_exp_f16_sdwa v127, v123 dst_sel:WORD_1 dst_unused:UNUSED_PRESERVE src0_sel:WORD_1
	v_exp_f16_sdwa v128, v124 dst_sel:WORD_1 dst_unused:UNUSED_PRESERVE src0_sel:WORD_1
	v_exp_f16_sdwa v129, v125 dst_sel:WORD_1 dst_unused:UNUSED_PRESERVE src0_sel:WORD_1
	v_pk_add_f16 v122, v209, v221 neg_lo:[0,1] neg_hi:[0,1]
	v_pk_add_f16 v109, v109, v126
	v_pk_add_f16 v108, v108, v127
	v_pk_add_f16 v107, v107, v128
	v_pk_add_f16 v106, v106, v129
	v_pk_fma_f16 v82, v98, v126, v82
	v_pk_fma_f16 v83, v99, v127, v83
	v_pk_fma_f16 v84, v100, v128, v84
	v_pk_fma_f16 v85, v101, v129, v85
	s_mov_b64 exec, s[78:79]
	buffer_load_dwordx4 v[14:17], v250, s[12:15], 0 offen offset:2048
	buffer_load_dwordx4 v[10:13], v250, s[12:15], 0 offen offset:2560
	s_mov_b64 exec, -1
	v_pk_add_f16 v123, v214, v222 neg_lo:[0,1] neg_hi:[0,1]
	v_pk_add_f16 v124, v215, v223 neg_lo:[0,1] neg_hi:[0,1]
	v_pk_add_f16 v125, v216, v224 neg_lo:[0,1] neg_hi:[0,1]
	v_exp_f16_sdwa v126, v122 dst_sel:WORD_0 dst_unused:UNUSED_PAD src0_sel:WORD_0
	v_exp_f16_sdwa v127, v123 dst_sel:WORD_0 dst_unused:UNUSED_PAD src0_sel:WORD_0
	v_exp_f16_sdwa v128, v124 dst_sel:WORD_0 dst_unused:UNUSED_PAD src0_sel:WORD_0
	v_exp_f16_sdwa v129, v125 dst_sel:WORD_0 dst_unused:UNUSED_PAD src0_sel:WORD_0
	v_exp_f16_sdwa v126, v122 dst_sel:WORD_1 dst_unused:UNUSED_PRESERVE src0_sel:WORD_1
	v_exp_f16_sdwa v127, v123 dst_sel:WORD_1 dst_unused:UNUSED_PRESERVE src0_sel:WORD_1
	v_exp_f16_sdwa v128, v124 dst_sel:WORD_1 dst_unused:UNUSED_PRESERVE src0_sel:WORD_1
	v_exp_f16_sdwa v129, v125 dst_sel:WORD_1 dst_unused:UNUSED_PRESERVE src0_sel:WORD_1
	v_pk_add_f16 v122, v217, v221 neg_lo:[0,1] neg_hi:[0,1]
	v_pk_add_f16 v109, v109, v126
	v_pk_add_f16 v106, v106, v129
	v_pk_add_f16 v107, v107, v128
	v_pk_add_f16 v108, v108, v127
	v_pk_fma_f16 v85, v33, v129, v85
	v_pk_fma_f16 v84, v32, v128, v84
	v_pk_fma_f16 v83, v31, v127, v83
	v_pk_fma_f16 v82, v30, v126, v82
	v_pk_add_f16 v123, v218, v222 neg_lo:[0,1] neg_hi:[0,1]
	v_pk_add_f16 v124, v219, v223 neg_lo:[0,1] neg_hi:[0,1]
	v_pk_add_f16 v125, v220, v224 neg_lo:[0,1] neg_hi:[0,1]
	v_exp_f16_sdwa v126, v122 dst_sel:WORD_0 dst_unused:UNUSED_PAD src0_sel:WORD_0
	v_exp_f16_sdwa v127, v123 dst_sel:WORD_0 dst_unused:UNUSED_PAD src0_sel:WORD_0
	v_exp_f16_sdwa v128, v124 dst_sel:WORD_0 dst_unused:UNUSED_PAD src0_sel:WORD_0
	v_exp_f16_sdwa v129, v125 dst_sel:WORD_0 dst_unused:UNUSED_PAD src0_sel:WORD_0
	v_exp_f16_sdwa v126, v122 dst_sel:WORD_1 dst_unused:UNUSED_PRESERVE src0_sel:WORD_1
	v_exp_f16_sdwa v127, v123 dst_sel:WORD_1 dst_unused:UNUSED_PRESERVE src0_sel:WORD_1
	v_exp_f16_sdwa v128, v124 dst_sel:WORD_1 dst_unused:UNUSED_PRESERVE src0_sel:WORD_1
	v_exp_f16_sdwa v129, v125 dst_sel:WORD_1 dst_unused:UNUSED_PRESERVE src0_sel:WORD_1
	v_pk_add_f16 v122, v210, v221 neg_lo:[0,1] neg_hi:[0,1]
	v_pk_add_f16 v109, v109, v126
	v_pk_add_f16 v108, v108, v127
	v_pk_add_f16 v107, v107, v128
	v_pk_add_f16 v106, v106, v129
	v_pk_fma_f16 v82, v42, v126, v82
	v_pk_fma_f16 v83, v43, v127, v83
	v_pk_fma_f16 v84, v44, v128, v84
	v_pk_fma_f16 v85, v45, v129, v85
	v_pk_add_f16 v123, v211, v222 neg_lo:[0,1] neg_hi:[0,1]
	v_pk_add_f16 v124, v212, v223 neg_lo:[0,1] neg_hi:[0,1]
	v_pk_add_f16 v125, v213, v224 neg_lo:[0,1] neg_hi:[0,1]
	v_exp_f16_sdwa v126, v122 dst_sel:WORD_0 dst_unused:UNUSED_PAD src0_sel:WORD_0
	v_exp_f16_sdwa v127, v123 dst_sel:WORD_0 dst_unused:UNUSED_PAD src0_sel:WORD_0
	v_exp_f16_sdwa v128, v124 dst_sel:WORD_0 dst_unused:UNUSED_PAD src0_sel:WORD_0
	v_exp_f16_sdwa v129, v125 dst_sel:WORD_0 dst_unused:UNUSED_PAD src0_sel:WORD_0
	v_exp_f16_sdwa v126, v122 dst_sel:WORD_1 dst_unused:UNUSED_PRESERVE src0_sel:WORD_1
	v_exp_f16_sdwa v127, v123 dst_sel:WORD_1 dst_unused:UNUSED_PRESERVE src0_sel:WORD_1
	v_exp_f16_sdwa v128, v124 dst_sel:WORD_1 dst_unused:UNUSED_PRESERVE src0_sel:WORD_1
	v_exp_f16_sdwa v129, v125 dst_sel:WORD_1 dst_unused:UNUSED_PRESERVE src0_sel:WORD_1
	v_pk_add_f16 v109, v109, v126
	v_pk_add_f16 v108, v108, v127
	v_rcp_f16_e32 v122, v109
	v_rcp_f16_sdwa v109, v109 dst_sel:DWORD dst_unused:UNUSED_PAD src0_sel:WORD_1
	v_pk_add_f16 v107, v107, v128
	v_rcp_f16_e32 v123, v108
	v_rcp_f16_sdwa v108, v108 dst_sel:DWORD dst_unused:UNUSED_PAD src0_sel:WORD_1
	v_pk_add_f16 v106, v106, v129
	v_rcp_f16_e32 v124, v107
	v_rcp_f16_sdwa v107, v107 dst_sel:DWORD dst_unused:UNUSED_PAD src0_sel:WORD_1
	v_rcp_f16_e32 v125, v106
	v_rcp_f16_sdwa v106, v106 dst_sel:DWORD dst_unused:UNUSED_PAD src0_sel:WORD_1
	v_pk_fma_f16 v82, v58, v126, v82
	v_pack_b32_f16 v109, v122, v109
	v_pk_fma_f16 v83, v59, v127, v83
	v_pk_mul_f16 v141, v82, v109
	v_pack_b32_f16 v82, v123, v108
	v_pk_fma_f16 v84, v60, v128, v84
	v_pk_mul_f16 v140, v83, v82
	v_pack_b32_f16 v82, v124, v107
	v_pk_fma_f16 v85, v61, v129, v85
	v_pk_mul_f16 v139, v84, v82
	v_pack_b32_f16 v82, v125, v106
	v_pk_mul_f16 v138, v85, v82
	s_waitcnt vmcnt(12)
	v_pk_mul_f16 v85, v208, v165 op_sel_hi:[0,1]
	v_pk_mul_f16 v109, v206, v165 op_sel_hi:[0,1]
	v_pk_mul_f16 v122, v207, v162 op_sel_hi:[0,1]
	v_pk_mul_f16 v125, v207, v165 op_sel_hi:[0,1]
	v_pk_mul_f16 v82, v208, v162 op_sel_hi:[0,1]
	v_pk_mul_f16 v83, v208, v163 op_sel_hi:[0,1]
	v_pk_mul_f16 v84, v208, v164 op_sel_hi:[0,1]
	v_pk_mul_f16 v106, v206, v162 op_sel_hi:[0,1]
	v_pk_mul_f16 v107, v206, v163 op_sel_hi:[0,1]
	v_pk_mul_f16 v108, v206, v164 op_sel_hi:[0,1]
	v_pk_mul_f16 v123, v207, v163 op_sel_hi:[0,1]
	v_pk_mul_f16 v124, v207, v164 op_sel_hi:[0,1]
	v_pk_fma_f16 v97, v97, v165, v85
	v_pk_fma_f16 v121, v121, v165, v109
	v_pk_fma_f16 v126, v137, v165, v125
	v_pk_fma_f16 v129, v134, v162, v122
	v_pk_fma_f16 v134, v65, v165, v85
	v_pk_fma_f16 v146, v81, v165, v109
	v_pk_fma_f16 v209, v105, v165, v125
	v_pk_fma_f16 v85, v37, v165, v85
	v_pk_fma_f16 v109, v49, v165, v109
	v_pk_fma_f16 v125, v69, v165, v125
	v_pk_maximum3_f16 v165, v97, v121, v126
	v_pk_fma_f16 v96, v96, v164, v84
	v_pk_fma_f16 v95, v95, v163, v83
	v_pk_fma_f16 v94, v94, v162, v82
	v_pk_fma_f16 v120, v120, v164, v108
	v_pk_fma_f16 v119, v119, v163, v107
	v_pk_fma_f16 v118, v118, v162, v106
	v_pk_fma_f16 v127, v136, v164, v124
	v_pk_fma_f16 v128, v135, v163, v123
	v_pk_fma_f16 v135, v64, v164, v84
	v_pk_fma_f16 v136, v63, v163, v83
	v_pk_fma_f16 v137, v62, v162, v82
	v_pk_fma_f16 v147, v80, v164, v108
	v_pk_fma_f16 v148, v79, v163, v107
	v_pk_fma_f16 v149, v78, v162, v106
	v_pk_fma_f16 v210, v104, v164, v124
	v_pk_fma_f16 v211, v103, v163, v123
	v_pk_fma_f16 v212, v102, v162, v122
	v_pk_fma_f16 v84, v36, v164, v84
	v_pk_fma_f16 v83, v35, v163, v83
	v_pk_fma_f16 v82, v34, v162, v82
	v_pk_fma_f16 v108, v48, v164, v108
	v_pk_fma_f16 v107, v47, v163, v107
	v_pk_fma_f16 v106, v46, v162, v106
	v_pk_fma_f16 v124, v68, v164, v124
	v_pk_fma_f16 v123, v67, v163, v123
	v_pk_fma_f16 v122, v66, v162, v122
	v_pk_maximum3_f16 v162, v94, v118, v129
	v_pk_maximum3_f16 v163, v95, v119, v128
	v_pk_maximum3_f16 v164, v96, v120, v127
	v_pk_maximum3_f16 v216, v134, v146, v209
	v_pk_maximum3_f16 v220, v85, v109, v125
	v_pk_maximum3_f16 v213, v137, v149, v212
	v_pk_maximum3_f16 v214, v136, v148, v211
	v_pk_maximum3_f16 v215, v135, v147, v210
	v_pk_maximum3_f16 v217, v82, v106, v122
	v_pk_maximum3_f16 v218, v83, v107, v123
	v_pk_maximum3_f16 v165, v165, v216, v220
	v_pk_maximum3_f16 v219, v84, v108, v124
	v_pk_maximum3_f16 v162, v162, v213, v217
	v_pk_maximum3_f16 v163, v163, v214, v218
	v_pk_maximum3_f16 v164, v164, v215, v219
	v_pk_add_f16 v97, v97, v165 neg_lo:[0,1] neg_hi:[0,1]
	v_pk_add_f16 v94, v94, v162 neg_lo:[0,1] neg_hi:[0,1]
	v_pk_add_f16 v95, v95, v163 neg_lo:[0,1] neg_hi:[0,1]
	v_pk_add_f16 v96, v96, v164 neg_lo:[0,1] neg_hi:[0,1]
	v_pk_add_f16 v118, v118, v162 neg_lo:[0,1] neg_hi:[0,1]
	v_exp_f16_sdwa v213, v94 dst_sel:WORD_0 dst_unused:UNUSED_PAD src0_sel:WORD_0
	v_exp_f16_sdwa v214, v95 dst_sel:WORD_0 dst_unused:UNUSED_PAD src0_sel:WORD_0
	v_exp_f16_sdwa v215, v96 dst_sel:WORD_0 dst_unused:UNUSED_PAD src0_sel:WORD_0
	v_exp_f16_sdwa v216, v97 dst_sel:WORD_0 dst_unused:UNUSED_PAD src0_sel:WORD_0
	v_exp_f16_sdwa v213, v94 dst_sel:WORD_1 dst_unused:UNUSED_PRESERVE src0_sel:WORD_1
	v_exp_f16_sdwa v214, v95 dst_sel:WORD_1 dst_unused:UNUSED_PRESERVE src0_sel:WORD_1
	v_exp_f16_sdwa v215, v96 dst_sel:WORD_1 dst_unused:UNUSED_PRESERVE src0_sel:WORD_1
	v_exp_f16_sdwa v216, v97 dst_sel:WORD_1 dst_unused:UNUSED_PRESERVE src0_sel:WORD_1
	v_pk_add_f16 v119, v119, v163 neg_lo:[0,1] neg_hi:[0,1]
	v_pk_add_f16 v97, v213, 0
	v_pk_fma_f16 v57, v57, v216, 0
	v_pk_add_f16 v94, v216, 0
	v_pk_add_f16 v95, v215, 0
	v_pk_add_f16 v96, v214, 0
	v_pk_fma_f16 v56, v56, v215, 0
	v_pk_fma_f16 v55, v55, v214, 0
	v_pk_fma_f16 v54, v54, v213, 0
	v_pk_add_f16 v120, v120, v164 neg_lo:[0,1] neg_hi:[0,1]
	v_pk_add_f16 v121, v121, v165 neg_lo:[0,1] neg_hi:[0,1]
	v_pk_add_f16 v82, v82, v162 neg_lo:[0,1] neg_hi:[0,1]
	v_exp_f16_sdwa v213, v118 dst_sel:WORD_0 dst_unused:UNUSED_PAD src0_sel:WORD_0
	v_exp_f16_sdwa v214, v119 dst_sel:WORD_0 dst_unused:UNUSED_PAD src0_sel:WORD_0
	v_exp_f16_sdwa v215, v120 dst_sel:WORD_0 dst_unused:UNUSED_PAD src0_sel:WORD_0
	v_exp_f16_sdwa v216, v121 dst_sel:WORD_0 dst_unused:UNUSED_PAD src0_sel:WORD_0
	v_exp_f16_sdwa v213, v118 dst_sel:WORD_1 dst_unused:UNUSED_PRESERVE src0_sel:WORD_1
	v_exp_f16_sdwa v214, v119 dst_sel:WORD_1 dst_unused:UNUSED_PRESERVE src0_sel:WORD_1
	v_exp_f16_sdwa v215, v120 dst_sel:WORD_1 dst_unused:UNUSED_PRESERVE src0_sel:WORD_1
	v_exp_f16_sdwa v216, v121 dst_sel:WORD_1 dst_unused:UNUSED_PRESERVE src0_sel:WORD_1
	v_pk_add_f16 v83, v83, v163 neg_lo:[0,1] neg_hi:[0,1]
	v_pk_add_f16 v97, v97, v213
	v_pk_fma_f16 v57, v77, v216, v57
	v_pk_add_f16 v77, v126, v165 neg_lo:[0,1] neg_hi:[0,1]
	v_pk_add_f16 v96, v96, v214
	v_pk_add_f16 v95, v95, v215
	v_pk_add_f16 v94, v94, v216
	v_pk_fma_f16 v54, v74, v213, v54
	v_pk_fma_f16 v55, v75, v214, v55
	v_pk_fma_f16 v56, v76, v215, v56
	v_pk_add_f16 v74, v129, v162 neg_lo:[0,1] neg_hi:[0,1]
	v_pk_add_f16 v75, v128, v163 neg_lo:[0,1] neg_hi:[0,1]
	v_pk_add_f16 v76, v127, v164 neg_lo:[0,1] neg_hi:[0,1]
	v_pk_add_f16 v84, v84, v164 neg_lo:[0,1] neg_hi:[0,1]
	v_exp_f16_sdwa v118, v74 dst_sel:WORD_0 dst_unused:UNUSED_PAD src0_sel:WORD_0
	v_exp_f16_sdwa v119, v75 dst_sel:WORD_0 dst_unused:UNUSED_PAD src0_sel:WORD_0
	v_exp_f16_sdwa v120, v76 dst_sel:WORD_0 dst_unused:UNUSED_PAD src0_sel:WORD_0
	v_exp_f16_sdwa v121, v77 dst_sel:WORD_0 dst_unused:UNUSED_PAD src0_sel:WORD_0
	v_exp_f16_sdwa v118, v74 dst_sel:WORD_1 dst_unused:UNUSED_PRESERVE src0_sel:WORD_1
	v_exp_f16_sdwa v119, v75 dst_sel:WORD_1 dst_unused:UNUSED_PRESERVE src0_sel:WORD_1
	v_exp_f16_sdwa v120, v76 dst_sel:WORD_1 dst_unused:UNUSED_PRESERVE src0_sel:WORD_1
	v_exp_f16_sdwa v121, v77 dst_sel:WORD_1 dst_unused:UNUSED_PRESERVE src0_sel:WORD_1
	v_pk_add_f16 v85, v85, v165 neg_lo:[0,1] neg_hi:[0,1]
	v_pk_add_f16 v77, v97, v118
	v_pk_add_f16 v74, v94, v121
	v_pk_add_f16 v75, v95, v120
	v_pk_add_f16 v76, v96, v119
	v_pk_fma_f16 v57, v101, v121, v57
	v_pk_fma_f16 v56, v100, v120, v56
	v_pk_fma_f16 v55, v99, v119, v55
	v_pk_fma_f16 v54, v98, v118, v54
	v_pk_add_f16 v94, v137, v162 neg_lo:[0,1] neg_hi:[0,1]
	v_pk_add_f16 v95, v136, v163 neg_lo:[0,1] neg_hi:[0,1]
	v_pk_add_f16 v96, v135, v164 neg_lo:[0,1] neg_hi:[0,1]
	v_pk_add_f16 v97, v134, v165 neg_lo:[0,1] neg_hi:[0,1]
	v_exp_f16_sdwa v98, v94 dst_sel:WORD_0 dst_unused:UNUSED_PAD src0_sel:WORD_0
	v_exp_f16_sdwa v99, v95 dst_sel:WORD_0 dst_unused:UNUSED_PAD src0_sel:WORD_0
	v_exp_f16_sdwa v100, v96 dst_sel:WORD_0 dst_unused:UNUSED_PAD src0_sel:WORD_0
	v_exp_f16_sdwa v101, v97 dst_sel:WORD_0 dst_unused:UNUSED_PAD src0_sel:WORD_0
	v_exp_f16_sdwa v98, v94 dst_sel:WORD_1 dst_unused:UNUSED_PRESERVE src0_sel:WORD_1
	v_exp_f16_sdwa v99, v95 dst_sel:WORD_1 dst_unused:UNUSED_PRESERVE src0_sel:WORD_1
	v_exp_f16_sdwa v100, v96 dst_sel:WORD_1 dst_unused:UNUSED_PRESERVE src0_sel:WORD_1
	v_exp_f16_sdwa v101, v97 dst_sel:WORD_1 dst_unused:UNUSED_PRESERVE src0_sel:WORD_1
	v_pk_add_f16 v94, v149, v162 neg_lo:[0,1] neg_hi:[0,1]
	v_pk_add_f16 v77, v77, v98
	v_pk_add_f16 v76, v76, v99
	v_pk_add_f16 v75, v75, v100
	v_pk_add_f16 v74, v74, v101
	v_pk_fma_f16 v54, v30, v98, v54
	v_pk_fma_f16 v55, v31, v99, v55
	v_pk_fma_f16 v56, v32, v100, v56
	v_pk_fma_f16 v57, v33, v101, v57
	v_pk_add_f16 v95, v148, v163 neg_lo:[0,1] neg_hi:[0,1]
	v_pk_add_f16 v96, v147, v164 neg_lo:[0,1] neg_hi:[0,1]
	v_pk_add_f16 v97, v146, v165 neg_lo:[0,1] neg_hi:[0,1]
	v_exp_f16_sdwa v98, v94 dst_sel:WORD_0 dst_unused:UNUSED_PAD src0_sel:WORD_0
	v_exp_f16_sdwa v99, v95 dst_sel:WORD_0 dst_unused:UNUSED_PAD src0_sel:WORD_0
	v_exp_f16_sdwa v100, v96 dst_sel:WORD_0 dst_unused:UNUSED_PAD src0_sel:WORD_0
	v_exp_f16_sdwa v101, v97 dst_sel:WORD_0 dst_unused:UNUSED_PAD src0_sel:WORD_0
	v_exp_f16_sdwa v98, v94 dst_sel:WORD_1 dst_unused:UNUSED_PRESERVE src0_sel:WORD_1
	v_exp_f16_sdwa v99, v95 dst_sel:WORD_1 dst_unused:UNUSED_PRESERVE src0_sel:WORD_1
	v_exp_f16_sdwa v100, v96 dst_sel:WORD_1 dst_unused:UNUSED_PRESERVE src0_sel:WORD_1
	v_exp_f16_sdwa v101, v97 dst_sel:WORD_1 dst_unused:UNUSED_PRESERVE src0_sel:WORD_1
	v_pk_add_f16 v94, v212, v162 neg_lo:[0,1] neg_hi:[0,1]
	v_pk_add_f16 v77, v77, v98
	v_pk_add_f16 v74, v74, v101
	v_pk_add_f16 v75, v75, v100
	v_pk_add_f16 v76, v76, v99
	v_pk_fma_f16 v57, v45, v101, v57
	v_pk_fma_f16 v56, v44, v100, v56
	v_pk_fma_f16 v55, v43, v99, v55
	v_pk_fma_f16 v54, v42, v98, v54
	v_pk_add_f16 v95, v211, v163 neg_lo:[0,1] neg_hi:[0,1]
	v_pk_add_f16 v96, v210, v164 neg_lo:[0,1] neg_hi:[0,1]
	v_pk_add_f16 v97, v209, v165 neg_lo:[0,1] neg_hi:[0,1]
	v_exp_f16_sdwa v98, v94 dst_sel:WORD_0 dst_unused:UNUSED_PAD src0_sel:WORD_0
	v_exp_f16_sdwa v99, v95 dst_sel:WORD_0 dst_unused:UNUSED_PAD src0_sel:WORD_0
	v_exp_f16_sdwa v100, v96 dst_sel:WORD_0 dst_unused:UNUSED_PAD src0_sel:WORD_0
	v_exp_f16_sdwa v101, v97 dst_sel:WORD_0 dst_unused:UNUSED_PAD src0_sel:WORD_0
	v_exp_f16_sdwa v98, v94 dst_sel:WORD_1 dst_unused:UNUSED_PRESERVE src0_sel:WORD_1
	v_exp_f16_sdwa v99, v95 dst_sel:WORD_1 dst_unused:UNUSED_PRESERVE src0_sel:WORD_1
	v_exp_f16_sdwa v100, v96 dst_sel:WORD_1 dst_unused:UNUSED_PRESERVE src0_sel:WORD_1
	v_exp_f16_sdwa v101, v97 dst_sel:WORD_1 dst_unused:UNUSED_PRESERVE src0_sel:WORD_1
	v_exp_f16_sdwa v94, v82 dst_sel:WORD_0 dst_unused:UNUSED_PAD src0_sel:WORD_0
	v_exp_f16_sdwa v95, v83 dst_sel:WORD_0 dst_unused:UNUSED_PAD src0_sel:WORD_0
	v_exp_f16_sdwa v96, v84 dst_sel:WORD_0 dst_unused:UNUSED_PAD src0_sel:WORD_0
	v_exp_f16_sdwa v97, v85 dst_sel:WORD_0 dst_unused:UNUSED_PAD src0_sel:WORD_0
	v_exp_f16_sdwa v94, v82 dst_sel:WORD_1 dst_unused:UNUSED_PRESERVE src0_sel:WORD_1
	v_exp_f16_sdwa v95, v83 dst_sel:WORD_1 dst_unused:UNUSED_PRESERVE src0_sel:WORD_1
	v_exp_f16_sdwa v96, v84 dst_sel:WORD_1 dst_unused:UNUSED_PRESERVE src0_sel:WORD_1
	v_exp_f16_sdwa v97, v85 dst_sel:WORD_1 dst_unused:UNUSED_PRESERVE src0_sel:WORD_1
	v_pk_add_f16 v82, v106, v162 neg_lo:[0,1] neg_hi:[0,1]
	v_pk_add_f16 v77, v77, v98
	v_pk_add_f16 v76, v76, v99
	v_pk_add_f16 v75, v75, v100
	v_pk_add_f16 v74, v74, v101
	v_pk_fma_f16 v54, v58, v98, v54
	v_pk_fma_f16 v55, v59, v99, v55
	v_pk_fma_f16 v56, v60, v100, v56
	v_pk_fma_f16 v57, v61, v101, v57
	v_pk_add_f16 v77, v77, v94
	v_pk_add_f16 v74, v74, v97
	v_pk_add_f16 v75, v75, v96
	v_pk_add_f16 v76, v76, v95
	v_pk_fma_f16 v57, v21, v97, v57
	v_pk_fma_f16 v56, v20, v96, v56
	v_pk_fma_f16 v55, v19, v95, v55
	v_pk_fma_f16 v54, v18, v94, v54
	v_pk_add_f16 v83, v107, v163 neg_lo:[0,1] neg_hi:[0,1]
	v_pk_add_f16 v84, v108, v164 neg_lo:[0,1] neg_hi:[0,1]
	v_pk_add_f16 v85, v109, v165 neg_lo:[0,1] neg_hi:[0,1]
	v_exp_f16_sdwa v94, v82 dst_sel:WORD_0 dst_unused:UNUSED_PAD src0_sel:WORD_0
	v_exp_f16_sdwa v95, v83 dst_sel:WORD_0 dst_unused:UNUSED_PAD src0_sel:WORD_0
	v_exp_f16_sdwa v96, v84 dst_sel:WORD_0 dst_unused:UNUSED_PAD src0_sel:WORD_0
	v_exp_f16_sdwa v97, v85 dst_sel:WORD_0 dst_unused:UNUSED_PAD src0_sel:WORD_0
	v_exp_f16_sdwa v94, v82 dst_sel:WORD_1 dst_unused:UNUSED_PRESERVE src0_sel:WORD_1
	v_exp_f16_sdwa v95, v83 dst_sel:WORD_1 dst_unused:UNUSED_PRESERVE src0_sel:WORD_1
	v_exp_f16_sdwa v96, v84 dst_sel:WORD_1 dst_unused:UNUSED_PRESERVE src0_sel:WORD_1
	v_exp_f16_sdwa v97, v85 dst_sel:WORD_1 dst_unused:UNUSED_PRESERVE src0_sel:WORD_1
	v_pk_add_f16 v82, v122, v162 neg_lo:[0,1] neg_hi:[0,1]
	v_pk_add_f16 v77, v77, v94
	v_pk_add_f16 v76, v76, v95
	v_pk_add_f16 v75, v75, v96
	v_pk_add_f16 v74, v74, v97
	v_pk_fma_f16 v54, v22, v94, v54
	v_pk_fma_f16 v55, v23, v95, v55
	v_pk_fma_f16 v56, v24, v96, v56
	v_pk_fma_f16 v57, v25, v97, v57
	v_pk_add_f16 v83, v123, v163 neg_lo:[0,1] neg_hi:[0,1]
	v_pk_add_f16 v84, v124, v164 neg_lo:[0,1] neg_hi:[0,1]
	v_pk_add_f16 v85, v125, v165 neg_lo:[0,1] neg_hi:[0,1]
	v_exp_f16_sdwa v94, v82 dst_sel:WORD_0 dst_unused:UNUSED_PAD src0_sel:WORD_0
	v_exp_f16_sdwa v95, v83 dst_sel:WORD_0 dst_unused:UNUSED_PAD src0_sel:WORD_0
	v_exp_f16_sdwa v96, v84 dst_sel:WORD_0 dst_unused:UNUSED_PAD src0_sel:WORD_0
	v_exp_f16_sdwa v97, v85 dst_sel:WORD_0 dst_unused:UNUSED_PAD src0_sel:WORD_0
	v_exp_f16_sdwa v94, v82 dst_sel:WORD_1 dst_unused:UNUSED_PRESERVE src0_sel:WORD_1
	v_exp_f16_sdwa v95, v83 dst_sel:WORD_1 dst_unused:UNUSED_PRESERVE src0_sel:WORD_1
	v_exp_f16_sdwa v96, v84 dst_sel:WORD_1 dst_unused:UNUSED_PRESERVE src0_sel:WORD_1
	v_exp_f16_sdwa v97, v85 dst_sel:WORD_1 dst_unused:UNUSED_PRESERVE src0_sel:WORD_1
	v_pk_add_f16 v77, v77, v94
	v_pk_add_f16 v76, v76, v95
	v_rcp_f16_e32 v82, v77
	v_rcp_f16_sdwa v77, v77 dst_sel:DWORD dst_unused:UNUSED_PAD src0_sel:WORD_1
	v_pk_add_f16 v75, v75, v96
	v_rcp_f16_e32 v83, v76
	v_rcp_f16_sdwa v76, v76 dst_sel:DWORD dst_unused:UNUSED_PAD src0_sel:WORD_1
	v_pk_add_f16 v74, v74, v97
	v_rcp_f16_e32 v84, v75
	v_rcp_f16_sdwa v75, v75 dst_sel:DWORD dst_unused:UNUSED_PAD src0_sel:WORD_1
	v_rcp_f16_e32 v85, v74
	v_rcp_f16_sdwa v74, v74 dst_sel:DWORD dst_unused:UNUSED_PAD src0_sel:WORD_1
	v_pk_fma_f16 v54, v26, v94, v54
	v_pack_b32_f16 v77, v82, v77
	v_pk_fma_f16 v57, v29, v97, v57
	v_pk_fma_f16 v55, v27, v95, v55
	v_pk_mul_f16 v97, v54, v77
	v_pack_b32_f16 v54, v83, v76
	v_pk_fma_f16 v56, v28, v96, v56
	v_pk_mul_f16 v96, v55, v54
	v_pack_b32_f16 v54, v84, v75
	v_pk_mul_f16 v95, v56, v54
	v_pack_b32_f16 v54, v85, v74
	v_pk_mul_f16 v94, v57, v54
	s_waitcnt vmcnt(6)
	v_pk_mul_f16 v57, v208, v161 op_sel_hi:[0,1]
	v_pk_mul_f16 v77, v206, v161 op_sel_hi:[0,1]
	v_pk_mul_f16 v85, v207, v161 op_sel_hi:[0,1]
	v_pk_mul_f16 v54, v208, v158 op_sel_hi:[0,1]
	v_pk_mul_f16 v55, v208, v159 op_sel_hi:[0,1]
	v_pk_mul_f16 v56, v208, v160 op_sel_hi:[0,1]
	v_pk_mul_f16 v74, v206, v158 op_sel_hi:[0,1]
	v_pk_mul_f16 v75, v206, v159 op_sel_hi:[0,1]
	v_pk_mul_f16 v76, v206, v160 op_sel_hi:[0,1]
	v_pk_mul_f16 v82, v207, v158 op_sel_hi:[0,1]
	v_pk_mul_f16 v83, v207, v159 op_sel_hi:[0,1]
	v_pk_mul_f16 v84, v207, v160 op_sel_hi:[0,1]
	v_pk_fma_f16 v65, v65, v161, v57
	v_pk_fma_f16 v81, v81, v161, v77
	v_pk_fma_f16 v98, v105, v161, v85
	v_pk_fma_f16 v64, v64, v160, v56
	v_pk_maximum3_f16 v125, v65, v81, v98
	v_pk_fma_f16 v63, v63, v159, v55
	v_pk_fma_f16 v62, v62, v158, v54
	v_pk_fma_f16 v80, v80, v160, v76
	v_pk_fma_f16 v79, v79, v159, v75
	v_pk_fma_f16 v78, v78, v158, v74
	v_pk_fma_f16 v99, v104, v160, v84
	v_pk_fma_f16 v100, v103, v159, v83
	v_pk_fma_f16 v101, v102, v158, v82
	v_pk_fma_f16 v102, v37, v161, v57
	v_pk_fma_f16 v106, v49, v161, v77
	v_pk_fma_f16 v118, v69, v161, v85
	v_pk_fma_f16 v57, v89, v161, v57
	v_pk_fma_f16 v77, v117, v161, v77
	v_pk_fma_f16 v85, v133, v161, v85
	v_pk_maximum3_f16 v122, v62, v78, v101
	v_pk_maximum3_f16 v123, v63, v79, v100
	v_pk_maximum3_f16 v124, v64, v80, v99
	v_pk_maximum3_f16 v129, v102, v106, v118
	v_pk_fma_f16 v103, v36, v160, v56
	v_pk_maximum3_f16 v137, v57, v77, v85
	v_pk_fma_f16 v104, v35, v159, v55
	v_pk_maximum3_f16 v125, v125, v129, v137
	v_pk_fma_f16 v105, v34, v158, v54
	v_pk_fma_f16 v107, v48, v160, v76
	v_pk_fma_f16 v108, v47, v159, v75
	v_pk_fma_f16 v109, v46, v158, v74
	v_pk_fma_f16 v119, v68, v160, v84
	v_pk_fma_f16 v120, v67, v159, v83
	v_pk_fma_f16 v121, v66, v158, v82
	v_pk_fma_f16 v56, v88, v160, v56
	v_pk_fma_f16 v55, v87, v159, v55
	v_pk_fma_f16 v54, v86, v158, v54
	v_pk_fma_f16 v76, v116, v160, v76
	v_pk_fma_f16 v75, v115, v159, v75
	v_pk_fma_f16 v74, v114, v158, v74
	v_pk_fma_f16 v84, v132, v160, v84
	v_pk_fma_f16 v83, v131, v159, v83
	v_pk_fma_f16 v82, v130, v158, v82
	v_pk_maximum3_f16 v126, v105, v109, v121
	v_pk_maximum3_f16 v127, v104, v108, v120
	v_pk_maximum3_f16 v128, v103, v107, v119
	v_pk_maximum3_f16 v135, v55, v75, v83
	v_pk_maximum3_f16 v136, v56, v76, v84
	v_pk_maximum3_f16 v134, v54, v74, v82
	v_pk_maximum3_f16 v122, v122, v126, v134
	v_pk_maximum3_f16 v123, v123, v127, v135
	v_pk_maximum3_f16 v124, v124, v128, v136
	v_pk_add_f16 v65, v65, v125 neg_lo:[0,1] neg_hi:[0,1]
	v_pk_add_f16 v62, v62, v122 neg_lo:[0,1] neg_hi:[0,1]
	v_pk_add_f16 v63, v63, v123 neg_lo:[0,1] neg_hi:[0,1]
	v_pk_add_f16 v64, v64, v124 neg_lo:[0,1] neg_hi:[0,1]
	v_pk_add_f16 v78, v78, v122 neg_lo:[0,1] neg_hi:[0,1]
	v_exp_f16_sdwa v126, v62 dst_sel:WORD_0 dst_unused:UNUSED_PAD src0_sel:WORD_0
	v_exp_f16_sdwa v127, v63 dst_sel:WORD_0 dst_unused:UNUSED_PAD src0_sel:WORD_0
	v_exp_f16_sdwa v128, v64 dst_sel:WORD_0 dst_unused:UNUSED_PAD src0_sel:WORD_0
	v_exp_f16_sdwa v129, v65 dst_sel:WORD_0 dst_unused:UNUSED_PAD src0_sel:WORD_0
	v_exp_f16_sdwa v126, v62 dst_sel:WORD_1 dst_unused:UNUSED_PRESERVE src0_sel:WORD_1
	v_exp_f16_sdwa v127, v63 dst_sel:WORD_1 dst_unused:UNUSED_PRESERVE src0_sel:WORD_1
	v_exp_f16_sdwa v128, v64 dst_sel:WORD_1 dst_unused:UNUSED_PRESERVE src0_sel:WORD_1
	v_exp_f16_sdwa v129, v65 dst_sel:WORD_1 dst_unused:UNUSED_PRESERVE src0_sel:WORD_1
	v_pk_add_f16 v79, v79, v123 neg_lo:[0,1] neg_hi:[0,1]
	v_pk_add_f16 v65, v126, 0
	v_pk_fma_f16 v33, v33, v129, 0
	v_pk_add_f16 v62, v129, 0
	v_pk_add_f16 v63, v128, 0
	v_pk_add_f16 v64, v127, 0
	v_pk_fma_f16 v32, v32, v128, 0
	v_pk_fma_f16 v31, v31, v127, 0
	v_pk_fma_f16 v30, v30, v126, 0
	v_pk_add_f16 v80, v80, v124 neg_lo:[0,1] neg_hi:[0,1]
	v_pk_add_f16 v81, v81, v125 neg_lo:[0,1] neg_hi:[0,1]
	v_pk_add_f16 v54, v54, v122 neg_lo:[0,1] neg_hi:[0,1]
	v_exp_f16_sdwa v126, v78 dst_sel:WORD_0 dst_unused:UNUSED_PAD src0_sel:WORD_0
	v_exp_f16_sdwa v127, v79 dst_sel:WORD_0 dst_unused:UNUSED_PAD src0_sel:WORD_0
	v_exp_f16_sdwa v128, v80 dst_sel:WORD_0 dst_unused:UNUSED_PAD src0_sel:WORD_0
	v_exp_f16_sdwa v129, v81 dst_sel:WORD_0 dst_unused:UNUSED_PAD src0_sel:WORD_0
	v_exp_f16_sdwa v126, v78 dst_sel:WORD_1 dst_unused:UNUSED_PRESERVE src0_sel:WORD_1
	v_exp_f16_sdwa v127, v79 dst_sel:WORD_1 dst_unused:UNUSED_PRESERVE src0_sel:WORD_1
	v_exp_f16_sdwa v128, v80 dst_sel:WORD_1 dst_unused:UNUSED_PRESERVE src0_sel:WORD_1
	v_exp_f16_sdwa v129, v81 dst_sel:WORD_1 dst_unused:UNUSED_PRESERVE src0_sel:WORD_1
	v_pk_add_f16 v55, v55, v123 neg_lo:[0,1] neg_hi:[0,1]
	v_pk_add_f16 v65, v65, v126
	v_pk_fma_f16 v33, v45, v129, v33
	v_pk_add_f16 v45, v98, v125 neg_lo:[0,1] neg_hi:[0,1]
	v_pk_add_f16 v64, v64, v127
	v_pk_add_f16 v63, v63, v128
	v_pk_add_f16 v62, v62, v129
	v_pk_fma_f16 v30, v42, v126, v30
	v_pk_fma_f16 v31, v43, v127, v31
	v_pk_fma_f16 v32, v44, v128, v32
	v_pk_add_f16 v42, v101, v122 neg_lo:[0,1] neg_hi:[0,1]
	v_pk_add_f16 v43, v100, v123 neg_lo:[0,1] neg_hi:[0,1]
	v_pk_add_f16 v44, v99, v124 neg_lo:[0,1] neg_hi:[0,1]
	v_pk_add_f16 v56, v56, v124 neg_lo:[0,1] neg_hi:[0,1]
	v_exp_f16_sdwa v78, v42 dst_sel:WORD_0 dst_unused:UNUSED_PAD src0_sel:WORD_0
	v_exp_f16_sdwa v79, v43 dst_sel:WORD_0 dst_unused:UNUSED_PAD src0_sel:WORD_0
	v_exp_f16_sdwa v80, v44 dst_sel:WORD_0 dst_unused:UNUSED_PAD src0_sel:WORD_0
	v_exp_f16_sdwa v81, v45 dst_sel:WORD_0 dst_unused:UNUSED_PAD src0_sel:WORD_0
	v_exp_f16_sdwa v78, v42 dst_sel:WORD_1 dst_unused:UNUSED_PRESERVE src0_sel:WORD_1
	v_exp_f16_sdwa v79, v43 dst_sel:WORD_1 dst_unused:UNUSED_PRESERVE src0_sel:WORD_1
	v_exp_f16_sdwa v80, v44 dst_sel:WORD_1 dst_unused:UNUSED_PRESERVE src0_sel:WORD_1
	v_exp_f16_sdwa v81, v45 dst_sel:WORD_1 dst_unused:UNUSED_PRESERVE src0_sel:WORD_1
	v_pk_add_f16 v57, v57, v125 neg_lo:[0,1] neg_hi:[0,1]
	v_pk_add_f16 v45, v65, v78
	v_pk_add_f16 v42, v62, v81
	v_pk_add_f16 v43, v63, v80
	v_pk_add_f16 v44, v64, v79
	v_pk_fma_f16 v33, v61, v81, v33
	v_pk_fma_f16 v32, v60, v80, v32
	v_pk_fma_f16 v31, v59, v79, v31
	v_pk_fma_f16 v30, v58, v78, v30
	v_pk_add_f16 v58, v105, v122 neg_lo:[0,1] neg_hi:[0,1]
	v_pk_add_f16 v59, v104, v123 neg_lo:[0,1] neg_hi:[0,1]
	v_pk_add_f16 v60, v103, v124 neg_lo:[0,1] neg_hi:[0,1]
	v_pk_add_f16 v61, v102, v125 neg_lo:[0,1] neg_hi:[0,1]
	v_exp_f16_sdwa v62, v58 dst_sel:WORD_0 dst_unused:UNUSED_PAD src0_sel:WORD_0
	v_exp_f16_sdwa v63, v59 dst_sel:WORD_0 dst_unused:UNUSED_PAD src0_sel:WORD_0
	v_exp_f16_sdwa v64, v60 dst_sel:WORD_0 dst_unused:UNUSED_PAD src0_sel:WORD_0
	v_exp_f16_sdwa v65, v61 dst_sel:WORD_0 dst_unused:UNUSED_PAD src0_sel:WORD_0
	v_exp_f16_sdwa v62, v58 dst_sel:WORD_1 dst_unused:UNUSED_PRESERVE src0_sel:WORD_1
	v_exp_f16_sdwa v63, v59 dst_sel:WORD_1 dst_unused:UNUSED_PRESERVE src0_sel:WORD_1
	v_exp_f16_sdwa v64, v60 dst_sel:WORD_1 dst_unused:UNUSED_PRESERVE src0_sel:WORD_1
	v_exp_f16_sdwa v65, v61 dst_sel:WORD_1 dst_unused:UNUSED_PRESERVE src0_sel:WORD_1
	v_pk_add_f16 v58, v109, v122 neg_lo:[0,1] neg_hi:[0,1]
	v_pk_add_f16 v45, v45, v62
	v_pk_add_f16 v44, v44, v63
	v_pk_add_f16 v43, v43, v64
	v_pk_add_f16 v42, v42, v65
	v_pk_fma_f16 v30, v18, v62, v30
	v_pk_fma_f16 v31, v19, v63, v31
	v_pk_fma_f16 v32, v20, v64, v32
	v_pk_fma_f16 v33, v21, v65, v33
	v_pk_add_f16 v59, v108, v123 neg_lo:[0,1] neg_hi:[0,1]
	v_pk_add_f16 v60, v107, v124 neg_lo:[0,1] neg_hi:[0,1]
	v_pk_add_f16 v61, v106, v125 neg_lo:[0,1] neg_hi:[0,1]
	v_exp_f16_sdwa v62, v58 dst_sel:WORD_0 dst_unused:UNUSED_PAD src0_sel:WORD_0
	v_exp_f16_sdwa v63, v59 dst_sel:WORD_0 dst_unused:UNUSED_PAD src0_sel:WORD_0
	v_exp_f16_sdwa v64, v60 dst_sel:WORD_0 dst_unused:UNUSED_PAD src0_sel:WORD_0
	v_exp_f16_sdwa v65, v61 dst_sel:WORD_0 dst_unused:UNUSED_PAD src0_sel:WORD_0
	v_exp_f16_sdwa v62, v58 dst_sel:WORD_1 dst_unused:UNUSED_PRESERVE src0_sel:WORD_1
	v_exp_f16_sdwa v63, v59 dst_sel:WORD_1 dst_unused:UNUSED_PRESERVE src0_sel:WORD_1
	v_exp_f16_sdwa v64, v60 dst_sel:WORD_1 dst_unused:UNUSED_PRESERVE src0_sel:WORD_1
	v_exp_f16_sdwa v65, v61 dst_sel:WORD_1 dst_unused:UNUSED_PRESERVE src0_sel:WORD_1
	v_pk_add_f16 v58, v121, v122 neg_lo:[0,1] neg_hi:[0,1]
	v_pk_add_f16 v45, v45, v62
	v_pk_add_f16 v42, v42, v65
	v_pk_add_f16 v43, v43, v64
	v_pk_add_f16 v44, v44, v63
	v_pk_fma_f16 v33, v25, v65, v33
	v_pk_fma_f16 v32, v24, v64, v32
	v_pk_fma_f16 v31, v23, v63, v31
	v_pk_fma_f16 v30, v22, v62, v30
	v_pk_add_f16 v59, v120, v123 neg_lo:[0,1] neg_hi:[0,1]
	v_pk_add_f16 v60, v119, v124 neg_lo:[0,1] neg_hi:[0,1]
	v_pk_add_f16 v61, v118, v125 neg_lo:[0,1] neg_hi:[0,1]
	v_exp_f16_sdwa v62, v58 dst_sel:WORD_0 dst_unused:UNUSED_PAD src0_sel:WORD_0
	v_exp_f16_sdwa v63, v59 dst_sel:WORD_0 dst_unused:UNUSED_PAD src0_sel:WORD_0
	v_exp_f16_sdwa v64, v60 dst_sel:WORD_0 dst_unused:UNUSED_PAD src0_sel:WORD_0
	v_exp_f16_sdwa v65, v61 dst_sel:WORD_0 dst_unused:UNUSED_PAD src0_sel:WORD_0
	v_exp_f16_sdwa v62, v58 dst_sel:WORD_1 dst_unused:UNUSED_PRESERVE src0_sel:WORD_1
	v_exp_f16_sdwa v63, v59 dst_sel:WORD_1 dst_unused:UNUSED_PRESERVE src0_sel:WORD_1
	v_exp_f16_sdwa v64, v60 dst_sel:WORD_1 dst_unused:UNUSED_PRESERVE src0_sel:WORD_1
	v_exp_f16_sdwa v65, v61 dst_sel:WORD_1 dst_unused:UNUSED_PRESERVE src0_sel:WORD_1
	v_exp_f16_sdwa v58, v54 dst_sel:WORD_0 dst_unused:UNUSED_PAD src0_sel:WORD_0
	v_exp_f16_sdwa v59, v55 dst_sel:WORD_0 dst_unused:UNUSED_PAD src0_sel:WORD_0
	v_exp_f16_sdwa v60, v56 dst_sel:WORD_0 dst_unused:UNUSED_PAD src0_sel:WORD_0
	v_exp_f16_sdwa v61, v57 dst_sel:WORD_0 dst_unused:UNUSED_PAD src0_sel:WORD_0
	v_exp_f16_sdwa v58, v54 dst_sel:WORD_1 dst_unused:UNUSED_PRESERVE src0_sel:WORD_1
	v_exp_f16_sdwa v59, v55 dst_sel:WORD_1 dst_unused:UNUSED_PRESERVE src0_sel:WORD_1
	v_exp_f16_sdwa v60, v56 dst_sel:WORD_1 dst_unused:UNUSED_PRESERVE src0_sel:WORD_1
	v_exp_f16_sdwa v61, v57 dst_sel:WORD_1 dst_unused:UNUSED_PRESERVE src0_sel:WORD_1
	v_pk_add_f16 v54, v74, v122 neg_lo:[0,1] neg_hi:[0,1]
	v_pk_add_f16 v45, v45, v62
	v_pk_add_f16 v44, v44, v63
	v_pk_add_f16 v43, v43, v64
	v_pk_add_f16 v42, v42, v65
	v_pk_fma_f16 v30, v26, v62, v30
	v_pk_fma_f16 v31, v27, v63, v31
	v_pk_fma_f16 v32, v28, v64, v32
	v_pk_fma_f16 v33, v29, v65, v33
	v_pk_add_f16 v45, v45, v58
	v_pk_add_f16 v42, v42, v61
	v_pk_add_f16 v43, v43, v60
	v_pk_add_f16 v44, v44, v59
	v_pk_fma_f16 v33, v41, v61, v33
	v_pk_fma_f16 v32, v40, v60, v32
	v_pk_fma_f16 v31, v39, v59, v31
	v_pk_fma_f16 v30, v38, v58, v30
	v_pk_add_f16 v55, v75, v123 neg_lo:[0,1] neg_hi:[0,1]
	v_pk_add_f16 v56, v76, v124 neg_lo:[0,1] neg_hi:[0,1]
	v_pk_add_f16 v57, v77, v125 neg_lo:[0,1] neg_hi:[0,1]
	v_exp_f16_sdwa v58, v54 dst_sel:WORD_0 dst_unused:UNUSED_PAD src0_sel:WORD_0
	v_exp_f16_sdwa v59, v55 dst_sel:WORD_0 dst_unused:UNUSED_PAD src0_sel:WORD_0
	v_exp_f16_sdwa v60, v56 dst_sel:WORD_0 dst_unused:UNUSED_PAD src0_sel:WORD_0
	v_exp_f16_sdwa v61, v57 dst_sel:WORD_0 dst_unused:UNUSED_PAD src0_sel:WORD_0
	v_exp_f16_sdwa v58, v54 dst_sel:WORD_1 dst_unused:UNUSED_PRESERVE src0_sel:WORD_1
	v_exp_f16_sdwa v59, v55 dst_sel:WORD_1 dst_unused:UNUSED_PRESERVE src0_sel:WORD_1
	v_exp_f16_sdwa v60, v56 dst_sel:WORD_1 dst_unused:UNUSED_PRESERVE src0_sel:WORD_1
	v_exp_f16_sdwa v61, v57 dst_sel:WORD_1 dst_unused:UNUSED_PRESERVE src0_sel:WORD_1
	v_pk_add_f16 v54, v82, v122 neg_lo:[0,1] neg_hi:[0,1]
	v_pk_add_f16 v45, v45, v58
	v_pk_add_f16 v44, v44, v59
	v_pk_add_f16 v43, v43, v60
	v_pk_add_f16 v42, v42, v61
	v_pk_fma_f16 v30, v50, v58, v30
	v_pk_fma_f16 v31, v51, v59, v31
	v_pk_fma_f16 v32, v52, v60, v32
	v_pk_fma_f16 v33, v53, v61, v33
	v_pk_add_f16 v55, v83, v123 neg_lo:[0,1] neg_hi:[0,1]
	v_pk_add_f16 v56, v84, v124 neg_lo:[0,1] neg_hi:[0,1]
	v_pk_add_f16 v57, v85, v125 neg_lo:[0,1] neg_hi:[0,1]
	v_exp_f16_sdwa v58, v54 dst_sel:WORD_0 dst_unused:UNUSED_PAD src0_sel:WORD_0
	v_exp_f16_sdwa v59, v55 dst_sel:WORD_0 dst_unused:UNUSED_PAD src0_sel:WORD_0
	v_exp_f16_sdwa v60, v56 dst_sel:WORD_0 dst_unused:UNUSED_PAD src0_sel:WORD_0
	v_exp_f16_sdwa v61, v57 dst_sel:WORD_0 dst_unused:UNUSED_PAD src0_sel:WORD_0
	v_exp_f16_sdwa v58, v54 dst_sel:WORD_1 dst_unused:UNUSED_PRESERVE src0_sel:WORD_1
	v_exp_f16_sdwa v59, v55 dst_sel:WORD_1 dst_unused:UNUSED_PRESERVE src0_sel:WORD_1
	v_exp_f16_sdwa v60, v56 dst_sel:WORD_1 dst_unused:UNUSED_PRESERVE src0_sel:WORD_1
	v_exp_f16_sdwa v61, v57 dst_sel:WORD_1 dst_unused:UNUSED_PRESERVE src0_sel:WORD_1
	v_pk_add_f16 v45, v45, v58
	v_pk_add_f16 v44, v44, v59
	v_rcp_f16_e32 v54, v45
	v_rcp_f16_sdwa v45, v45 dst_sel:DWORD dst_unused:UNUSED_PAD src0_sel:WORD_1
	v_pk_add_f16 v43, v43, v60
	v_rcp_f16_e32 v55, v44
	v_rcp_f16_sdwa v44, v44 dst_sel:DWORD dst_unused:UNUSED_PAD src0_sel:WORD_1
	v_pk_add_f16 v42, v42, v61
	v_rcp_f16_e32 v56, v43
	v_rcp_f16_sdwa v43, v43 dst_sel:DWORD dst_unused:UNUSED_PAD src0_sel:WORD_1
	v_rcp_f16_e32 v57, v42
	v_rcp_f16_sdwa v42, v42 dst_sel:DWORD dst_unused:UNUSED_PAD src0_sel:WORD_1
	v_pk_fma_f16 v30, v70, v58, v30
	v_pack_b32_f16 v45, v54, v45
	v_pk_fma_f16 v31, v71, v59, v31
	v_pk_mul_f16 v45, v30, v45
	v_pack_b32_f16 v30, v55, v44
	v_pk_fma_f16 v32, v72, v60, v32
	v_pk_mul_f16 v44, v31, v30
	v_pack_b32_f16 v30, v56, v43
	v_pk_fma_f16 v33, v73, v61, v33
	v_pk_mul_f16 v43, v32, v30
	v_pack_b32_f16 v30, v57, v42
	v_pk_mul_f16 v42, v33, v30
	s_waitcnt vmcnt(0)
	v_pk_mul_f16 v30, v208, v154 op_sel_hi:[0,1]
	v_pk_mul_f16 v31, v208, v155 op_sel_hi:[0,1]
	v_pk_mul_f16 v32, v208, v156 op_sel_hi:[0,1]
	v_pk_mul_f16 v33, v208, v157 op_sel_hi:[0,1]
	v_pk_mul_f16 v54, v206, v154 op_sel_hi:[0,1]
	v_pk_mul_f16 v55, v206, v155 op_sel_hi:[0,1]
	v_pk_mul_f16 v56, v206, v156 op_sel_hi:[0,1]
	v_pk_mul_f16 v57, v206, v157 op_sel_hi:[0,1]
	v_pk_mul_f16 v58, v207, v154 op_sel_hi:[0,1]
	v_pk_mul_f16 v59, v207, v155 op_sel_hi:[0,1]
	v_pk_mul_f16 v60, v207, v156 op_sel_hi:[0,1]
	v_pk_mul_f16 v61, v207, v157 op_sel_hi:[0,1]
	v_pk_fma_f16 v37, v37, v157, v33
	v_pk_fma_f16 v36, v36, v156, v32
	v_pk_fma_f16 v35, v35, v155, v31
	v_pk_fma_f16 v34, v34, v154, v30
	v_pk_fma_f16 v49, v49, v157, v57
	v_pk_fma_f16 v48, v48, v156, v56
	v_pk_fma_f16 v47, v47, v155, v55
	v_pk_fma_f16 v46, v46, v154, v54
	v_pk_fma_f16 v62, v69, v157, v61
	v_pk_fma_f16 v63, v68, v156, v60
	v_pk_fma_f16 v64, v67, v155, v59
	v_pk_fma_f16 v65, v66, v154, v58
	v_pk_fma_f16 v66, v89, v157, v33
	v_pk_fma_f16 v67, v88, v156, v32
	v_pk_fma_f16 v68, v87, v155, v31
	v_pk_fma_f16 v69, v86, v154, v30
	v_pk_fma_f16 v74, v117, v157, v57
	v_pk_fma_f16 v75, v116, v156, v56
	v_pk_fma_f16 v76, v115, v155, v55
	v_pk_fma_f16 v77, v114, v154, v54
	v_pk_fma_f16 v78, v133, v157, v61
	v_pk_fma_f16 v79, v132, v156, v60
	v_pk_fma_f16 v80, v131, v155, v59
	v_pk_fma_f16 v81, v130, v154, v58
	v_pk_fma_f16 v61, v17, v157, v61
	v_pk_fma_f16 v60, v16, v156, v60
	v_pk_fma_f16 v59, v15, v155, v59
	v_pk_fma_f16 v58, v14, v154, v58
	v_pk_maximum3_f16 v14, v34, v46, v65
	v_pk_maximum3_f16 v15, v35, v47, v64
	v_pk_maximum3_f16 v16, v36, v48, v63
	v_pk_maximum3_f16 v17, v37, v49, v62
	v_pk_maximum3_f16 v82, v69, v77, v81
	v_pk_maximum3_f16 v83, v68, v76, v80
	v_pk_maximum3_f16 v84, v67, v75, v79
	v_pk_maximum3_f16 v85, v66, v74, v78
	v_pk_fma_f16 v33, v145, v157, v33
	v_pk_fma_f16 v32, v144, v156, v32
	v_pk_fma_f16 v31, v143, v155, v31
	v_pk_fma_f16 v30, v142, v154, v30
	v_pk_fma_f16 v57, v153, v157, v57
	v_pk_fma_f16 v56, v152, v156, v56
	v_pk_fma_f16 v55, v151, v155, v55
	v_pk_fma_f16 v54, v150, v154, v54
	v_pk_maximum3_f16 v87, v31, v55, v59
	v_pk_maximum3_f16 v88, v32, v56, v60
	v_pk_maximum3_f16 v89, v33, v57, v61
	v_pk_maximum3_f16 v86, v30, v54, v58
	v_pk_maximum3_f16 v15, v15, v83, v87
	v_pk_maximum3_f16 v16, v16, v84, v88
	v_pk_maximum3_f16 v17, v17, v85, v89
	v_pk_maximum3_f16 v14, v14, v82, v86
	v_xor_b32_e32 v82, 0x80008000, v17
	v_xor_b32_e32 v83, 0x80008000, v16
	v_xor_b32_e32 v84, 0x80008000, v15
	v_xor_b32_e32 v85, 0x80008000, v14
	v_pk_add_f16 v14, v34, v85
	v_pk_add_f16 v15, v35, v84
	v_pk_add_f16 v16, v36, v83
	v_pk_add_f16 v17, v37, v82
	v_exp_f16_sdwa v34, v14 dst_sel:WORD_0 dst_unused:UNUSED_PAD src0_sel:WORD_0
	v_exp_f16_sdwa v35, v15 dst_sel:WORD_0 dst_unused:UNUSED_PAD src0_sel:WORD_0
	v_exp_f16_sdwa v36, v16 dst_sel:WORD_0 dst_unused:UNUSED_PAD src0_sel:WORD_0
	v_exp_f16_sdwa v37, v17 dst_sel:WORD_0 dst_unused:UNUSED_PAD src0_sel:WORD_0
	v_exp_f16_sdwa v34, v14 dst_sel:WORD_1 dst_unused:UNUSED_PRESERVE src0_sel:WORD_1
	v_exp_f16_sdwa v35, v15 dst_sel:WORD_1 dst_unused:UNUSED_PRESERVE src0_sel:WORD_1
	v_exp_f16_sdwa v36, v16 dst_sel:WORD_1 dst_unused:UNUSED_PRESERVE src0_sel:WORD_1
	v_exp_f16_sdwa v37, v17 dst_sel:WORD_1 dst_unused:UNUSED_PRESERVE src0_sel:WORD_1
	v_pk_add_f16 v14, v34, 0
	v_pk_add_f16 v15, v35, 0
	v_pk_add_f16 v16, v36, 0
	v_pk_add_f16 v17, v37, 0
	v_pk_fma_f16 v18, v18, v34, 0
	v_pk_fma_f16 v19, v19, v35, 0
	v_pk_fma_f16 v20, v20, v36, 0
	v_pk_fma_f16 v21, v21, v37, 0
	v_pk_add_f16 v34, v46, v85
	v_pk_add_f16 v35, v47, v84
	v_pk_add_f16 v36, v48, v83
	v_pk_add_f16 v37, v49, v82
	v_exp_f16_sdwa v46, v34 dst_sel:WORD_0 dst_unused:UNUSED_PAD src0_sel:WORD_0
	v_exp_f16_sdwa v47, v35 dst_sel:WORD_0 dst_unused:UNUSED_PAD src0_sel:WORD_0
	v_exp_f16_sdwa v48, v36 dst_sel:WORD_0 dst_unused:UNUSED_PAD src0_sel:WORD_0
	v_exp_f16_sdwa v49, v37 dst_sel:WORD_0 dst_unused:UNUSED_PAD src0_sel:WORD_0
	v_exp_f16_sdwa v46, v34 dst_sel:WORD_1 dst_unused:UNUSED_PRESERVE src0_sel:WORD_1
	v_exp_f16_sdwa v47, v35 dst_sel:WORD_1 dst_unused:UNUSED_PRESERVE src0_sel:WORD_1
	v_exp_f16_sdwa v48, v36 dst_sel:WORD_1 dst_unused:UNUSED_PRESERVE src0_sel:WORD_1
	v_exp_f16_sdwa v49, v37 dst_sel:WORD_1 dst_unused:UNUSED_PRESERVE src0_sel:WORD_1
	s_nop 0
	v_pk_add_f16 v17, v17, v49
	v_pk_add_f16 v16, v16, v48
	v_pk_add_f16 v15, v15, v47
	v_pk_add_f16 v14, v14, v46
	v_pk_fma_f16 v21, v25, v49, v21
	v_pk_fma_f16 v20, v24, v48, v20
	v_pk_fma_f16 v19, v23, v47, v19
	v_pk_fma_f16 v18, v22, v46, v18
	v_pk_add_f16 v22, v65, v85
	v_pk_add_f16 v23, v64, v84
	v_pk_add_f16 v24, v63, v83
	v_pk_add_f16 v25, v62, v82
	v_exp_f16_sdwa v34, v22 dst_sel:WORD_0 dst_unused:UNUSED_PAD src0_sel:WORD_0
	v_exp_f16_sdwa v35, v23 dst_sel:WORD_0 dst_unused:UNUSED_PAD src0_sel:WORD_0
	v_exp_f16_sdwa v36, v24 dst_sel:WORD_0 dst_unused:UNUSED_PAD src0_sel:WORD_0
	v_exp_f16_sdwa v37, v25 dst_sel:WORD_0 dst_unused:UNUSED_PAD src0_sel:WORD_0
	v_exp_f16_sdwa v34, v22 dst_sel:WORD_1 dst_unused:UNUSED_PRESERVE src0_sel:WORD_1
	v_exp_f16_sdwa v35, v23 dst_sel:WORD_1 dst_unused:UNUSED_PRESERVE src0_sel:WORD_1
	v_exp_f16_sdwa v36, v24 dst_sel:WORD_1 dst_unused:UNUSED_PRESERVE src0_sel:WORD_1
	v_exp_f16_sdwa v37, v25 dst_sel:WORD_1 dst_unused:UNUSED_PRESERVE src0_sel:WORD_1
	v_pk_add_f16 v22, v69, v85
	v_pk_add_f16 v14, v14, v34
	v_pk_add_f16 v15, v15, v35
	v_pk_add_f16 v16, v16, v36
	v_pk_add_f16 v17, v17, v37
	v_pk_fma_f16 v18, v26, v34, v18
	v_pk_fma_f16 v19, v27, v35, v19
	v_pk_fma_f16 v20, v28, v36, v20
	v_pk_fma_f16 v21, v29, v37, v21
	v_pk_add_f16 v23, v68, v84
	v_pk_add_f16 v24, v67, v83
	v_pk_add_f16 v25, v66, v82
	v_exp_f16_sdwa v26, v22 dst_sel:WORD_0 dst_unused:UNUSED_PAD src0_sel:WORD_0
	v_exp_f16_sdwa v27, v23 dst_sel:WORD_0 dst_unused:UNUSED_PAD src0_sel:WORD_0
	v_exp_f16_sdwa v28, v24 dst_sel:WORD_0 dst_unused:UNUSED_PAD src0_sel:WORD_0
	v_exp_f16_sdwa v29, v25 dst_sel:WORD_0 dst_unused:UNUSED_PAD src0_sel:WORD_0
	v_exp_f16_sdwa v26, v22 dst_sel:WORD_1 dst_unused:UNUSED_PRESERVE src0_sel:WORD_1
	v_exp_f16_sdwa v27, v23 dst_sel:WORD_1 dst_unused:UNUSED_PRESERVE src0_sel:WORD_1
	v_exp_f16_sdwa v28, v24 dst_sel:WORD_1 dst_unused:UNUSED_PRESERVE src0_sel:WORD_1
	v_exp_f16_sdwa v29, v25 dst_sel:WORD_1 dst_unused:UNUSED_PRESERVE src0_sel:WORD_1
	v_pk_add_f16 v22, v77, v85
	v_pk_add_f16 v17, v17, v29
	v_pk_add_f16 v16, v16, v28
	v_pk_add_f16 v15, v15, v27
	v_pk_add_f16 v14, v14, v26
	v_pk_fma_f16 v21, v41, v29, v21
	v_pk_fma_f16 v20, v40, v28, v20
	v_pk_fma_f16 v19, v39, v27, v19
	v_pk_fma_f16 v18, v38, v26, v18
	v_pk_add_f16 v23, v76, v84
	v_pk_add_f16 v24, v75, v83
	v_pk_add_f16 v25, v74, v82
	v_exp_f16_sdwa v26, v22 dst_sel:WORD_0 dst_unused:UNUSED_PAD src0_sel:WORD_0
	v_exp_f16_sdwa v27, v23 dst_sel:WORD_0 dst_unused:UNUSED_PAD src0_sel:WORD_0
	v_exp_f16_sdwa v28, v24 dst_sel:WORD_0 dst_unused:UNUSED_PAD src0_sel:WORD_0
	v_exp_f16_sdwa v29, v25 dst_sel:WORD_0 dst_unused:UNUSED_PAD src0_sel:WORD_0
	v_exp_f16_sdwa v26, v22 dst_sel:WORD_1 dst_unused:UNUSED_PRESERVE src0_sel:WORD_1
	v_exp_f16_sdwa v27, v23 dst_sel:WORD_1 dst_unused:UNUSED_PRESERVE src0_sel:WORD_1
	v_exp_f16_sdwa v28, v24 dst_sel:WORD_1 dst_unused:UNUSED_PRESERVE src0_sel:WORD_1
	v_exp_f16_sdwa v29, v25 dst_sel:WORD_1 dst_unused:UNUSED_PRESERVE src0_sel:WORD_1
	v_pk_add_f16 v22, v81, v85
	v_pk_add_f16 v14, v14, v26
	v_pk_add_f16 v15, v15, v27
	v_pk_add_f16 v16, v16, v28
	v_pk_add_f16 v17, v17, v29
	v_pk_fma_f16 v18, v50, v26, v18
	v_pk_fma_f16 v19, v51, v27, v19
	v_pk_fma_f16 v20, v52, v28, v20
	v_pk_fma_f16 v21, v53, v29, v21
	v_pk_add_f16 v23, v80, v84
	v_pk_add_f16 v24, v79, v83
	v_pk_add_f16 v25, v78, v82
	v_exp_f16_sdwa v26, v22 dst_sel:WORD_0 dst_unused:UNUSED_PAD src0_sel:WORD_0
	v_exp_f16_sdwa v27, v23 dst_sel:WORD_0 dst_unused:UNUSED_PAD src0_sel:WORD_0
	v_exp_f16_sdwa v28, v24 dst_sel:WORD_0 dst_unused:UNUSED_PAD src0_sel:WORD_0
	v_exp_f16_sdwa v29, v25 dst_sel:WORD_0 dst_unused:UNUSED_PAD src0_sel:WORD_0
	v_exp_f16_sdwa v26, v22 dst_sel:WORD_1 dst_unused:UNUSED_PRESERVE src0_sel:WORD_1
	v_exp_f16_sdwa v27, v23 dst_sel:WORD_1 dst_unused:UNUSED_PRESERVE src0_sel:WORD_1
	v_exp_f16_sdwa v28, v24 dst_sel:WORD_1 dst_unused:UNUSED_PRESERVE src0_sel:WORD_1
	v_exp_f16_sdwa v29, v25 dst_sel:WORD_1 dst_unused:UNUSED_PRESERVE src0_sel:WORD_1
	v_pk_add_f16 v22, v30, v85
	v_pk_add_f16 v17, v17, v29
	v_pk_add_f16 v16, v16, v28
	v_pk_add_f16 v15, v15, v27
	v_pk_add_f16 v14, v14, v26
	v_pk_fma_f16 v21, v73, v29, v21
	v_pk_fma_f16 v20, v72, v28, v20
	v_pk_fma_f16 v19, v71, v27, v19
	v_pk_fma_f16 v18, v70, v26, v18
	v_pk_add_f16 v23, v31, v84
	v_pk_add_f16 v24, v32, v83
	v_pk_add_f16 v25, v33, v82
	v_exp_f16_sdwa v26, v22 dst_sel:WORD_0 dst_unused:UNUSED_PAD src0_sel:WORD_0
	v_exp_f16_sdwa v27, v23 dst_sel:WORD_0 dst_unused:UNUSED_PAD src0_sel:WORD_0
	v_exp_f16_sdwa v28, v24 dst_sel:WORD_0 dst_unused:UNUSED_PAD src0_sel:WORD_0
	v_exp_f16_sdwa v29, v25 dst_sel:WORD_0 dst_unused:UNUSED_PAD src0_sel:WORD_0
	v_exp_f16_sdwa v26, v22 dst_sel:WORD_1 dst_unused:UNUSED_PRESERVE src0_sel:WORD_1
	v_exp_f16_sdwa v27, v23 dst_sel:WORD_1 dst_unused:UNUSED_PRESERVE src0_sel:WORD_1
	v_exp_f16_sdwa v28, v24 dst_sel:WORD_1 dst_unused:UNUSED_PRESERVE src0_sel:WORD_1
	v_exp_f16_sdwa v29, v25 dst_sel:WORD_1 dst_unused:UNUSED_PRESERVE src0_sel:WORD_1
	v_pk_add_f16 v22, v54, v85
	v_pk_add_f16 v14, v14, v26
	v_pk_add_f16 v15, v15, v27
	v_pk_add_f16 v16, v16, v28
	v_pk_add_f16 v17, v17, v29
	v_pk_fma_f16 v18, v90, v26, v18
	v_pk_fma_f16 v19, v91, v27, v19
	v_pk_fma_f16 v20, v92, v28, v20
	v_pk_fma_f16 v21, v93, v29, v21
	v_pk_add_f16 v23, v55, v84
	v_pk_add_f16 v24, v56, v83
	v_pk_add_f16 v25, v57, v82
	v_exp_f16_sdwa v26, v22 dst_sel:WORD_0 dst_unused:UNUSED_PAD src0_sel:WORD_0
	v_exp_f16_sdwa v27, v23 dst_sel:WORD_0 dst_unused:UNUSED_PAD src0_sel:WORD_0
	v_exp_f16_sdwa v28, v24 dst_sel:WORD_0 dst_unused:UNUSED_PAD src0_sel:WORD_0
	v_exp_f16_sdwa v29, v25 dst_sel:WORD_0 dst_unused:UNUSED_PAD src0_sel:WORD_0
	v_exp_f16_sdwa v26, v22 dst_sel:WORD_1 dst_unused:UNUSED_PRESERVE src0_sel:WORD_1
	v_exp_f16_sdwa v27, v23 dst_sel:WORD_1 dst_unused:UNUSED_PRESERVE src0_sel:WORD_1
	v_exp_f16_sdwa v28, v24 dst_sel:WORD_1 dst_unused:UNUSED_PRESERVE src0_sel:WORD_1
	v_exp_f16_sdwa v29, v25 dst_sel:WORD_1 dst_unused:UNUSED_PRESERVE src0_sel:WORD_1
	s_nop 0
	v_pk_add_f16 v17, v17, v29
	v_pk_add_f16 v16, v16, v28
	v_pk_add_f16 v15, v15, v27
	v_pk_add_f16 v14, v14, v26
	v_pk_fma_f16 v21, v113, v29, v21
	v_pk_fma_f16 v20, v112, v28, v20
	v_pk_fma_f16 v19, v111, v27, v19
	v_pk_fma_f16 v18, v110, v26, v18
	v_pk_add_f16 v26, v58, v85
	v_pk_add_f16 v27, v59, v84
	v_pk_add_f16 v28, v60, v83
	v_pk_add_f16 v29, v61, v82
	v_exp_f16_sdwa v22, v26 dst_sel:WORD_0 dst_unused:UNUSED_PAD src0_sel:WORD_0
	v_exp_f16_sdwa v23, v27 dst_sel:WORD_0 dst_unused:UNUSED_PAD src0_sel:WORD_0
	v_exp_f16_sdwa v24, v28 dst_sel:WORD_0 dst_unused:UNUSED_PAD src0_sel:WORD_0
	v_exp_f16_sdwa v25, v29 dst_sel:WORD_0 dst_unused:UNUSED_PAD src0_sel:WORD_0
	v_exp_f16_sdwa v22, v26 dst_sel:WORD_1 dst_unused:UNUSED_PRESERVE src0_sel:WORD_1
	v_exp_f16_sdwa v23, v27 dst_sel:WORD_1 dst_unused:UNUSED_PRESERVE src0_sel:WORD_1
	v_exp_f16_sdwa v24, v28 dst_sel:WORD_1 dst_unused:UNUSED_PRESERVE src0_sel:WORD_1
	v_exp_f16_sdwa v25, v29 dst_sel:WORD_1 dst_unused:UNUSED_PRESERVE src0_sel:WORD_1
	s_nop 0
.LBB4_118:
	s_and_b64 vcc, exec, s[4:5]
	s_cbranch_vccz .LBB4_3
	global_load_dwordx3 v[146:148], v169, s[16:17]
	s_mov_b32 s14, s38
	s_mov_b32 s15, s39
	v_cmp_lt_u32_e64 s[64:65], 0, v199
	v_cmp_gt_u32_e64 s[66:67], 63, v199
	v_cmp_lt_u32_e64 s[68:69], 0, v180
	v_cmp_gt_u32_e64 s[70:71], 60, v180
	buffer_load_dwordx4 v[162:165], v200, s[12:15], 0 offen sc1
	s_and_b64 s[72:73], s[68:69], s[64:65]
	s_and_b64 s[74:75], s[68:69], s[66:67]
	s_and_b64 s[76:77], s[70:71], s[64:65]
	s_and_b64 s[78:79], s[70:71], s[66:67]
	v_add_u32_e32 v245, 0xfffe7c00, v200
	v_add_u32_e32 v246, 0xfffe8000, v200
	s_mov_b64 exec, s[72:73]
	buffer_load_dwordx4 v[114:117], v245, s[12:15], 0 offen
	buffer_load_dwordx4 v[70:73], v245, s[12:15], 0 offen offset:512
	s_mov_b64 exec, -1
	s_mov_b64 exec, s[68:69]
	buffer_load_dwordx4 v[130:133], v246, s[12:15], 0 offen offset:512
	buffer_load_dwordx4 v[94:97], v246, s[12:15], 0 offen offset:1024
	s_mov_b64 exec, -1
	s_mov_b64 exec, s[74:75]
	buffer_load_dwordx4 v[138:141], v246, s[12:15], 0 offen offset:2048
	buffer_load_dwordx4 v[118:121], v246, s[12:15], 0 offen offset:2560
	s_mov_b64 exec, -1
	v_add_u32_e32 v245, 0xfffffc00, v200
	s_mov_b64 exec, s[64:65]
	buffer_load_dwordx4 v[86:89], v245, s[12:15], 0 offen
	buffer_load_dwordx4 v[42:45], v245, s[12:15], 0 offen offset:512
	s_mov_b64 exec, -1
	buffer_load_dwordx4 v[110:113], v200, s[12:15], 0 offen offset:512
	buffer_load_dwordx4 v[66:69], v200, s[12:15], 0 offen offset:1024
	s_mov_b64 exec, s[66:67]
	buffer_load_dwordx4 v[126:129], v200, s[12:15], 0 offen offset:2048
	buffer_load_dwordx4 v[90:93], v200, s[12:15], 0 offen offset:2560
	s_mov_b64 exec, -1
	v_add_u32_e32 v245, 0x17c00, v200
	v_add_u32_e32 v246, 0x18000, v200
	s_mov_b64 exec, s[64:65]
	buffer_load_dwordx4 v[54:57], v245, s[12:15], 0 offen
	buffer_load_dwordx4 v[22:25], v245, s[12:15], 0 offen offset:512
	s_mov_b64 exec, -1
	buffer_load_dwordx4 v[74:77], v246, s[12:15], 0 offen offset:512
	buffer_load_dwordx4 v[34:37], v246, s[12:15], 0 offen offset:1024
	s_mov_b64 exec, s[66:67]
	buffer_load_dwordx4 v[98:101], v246, s[12:15], 0 offen offset:2048
	buffer_load_dwordx4 v[50:53], v246, s[12:15], 0 offen offset:2560
	s_mov_b64 exec, -1
	v_add_u32_e32 v245, 0x18000, v200
	buffer_load_dwordx4 v[154:157], v245, s[12:15], 0 offen sc1
	v_add_u32_e32 v246, 0x30000, v200
	buffer_load_dwordx4 v[150:153], v246, s[12:15], 0 offen sc1
	v_add_u32_e32 v245, 0x2fc00, v200
	v_add_u32_e32 v246, 0x30000, v200
	v_add_u32_e32 v247, 0x47c00, v200
	v_add_u32_e32 v248, 0x48000, v200
	v_add_u32_e32 v249, 0x5fc00, v200
	v_add_u32_e32 v250, 0x60000, v200
	s_waitcnt vmcnt(22)
	v_cvt_pk_f16_f32 v6, v2, v3
	v_cvt_pk_f16_f32 v2, v8, v9
	v_cvt_pk_f16_f32 v7, v4, v5
	v_cvt_pk_f16_f32 v3, v10, v11
	v_cvt_pk_f16_f32 v8, v12, v13
	v_cvt_pk_f16_f32 v4, v16, v17
	v_cvt_pk_f16_f32 v9, v14, v15
	v_cvt_pk_f16_f32 v5, v18, v19
	s_not_b64 exec, s[72:73]
	s_cbranch_execz .Lmyf_C4_0
	v_mov_b32_e32 v114, v6
	v_mov_b32_e32 v115, v7
	v_mov_b32_e32 v116, v8
	v_mov_b32_e32 v117, v9
	v_mov_b32_e32 v70, v2
	v_mov_b32_e32 v71, v3
	v_mov_b32_e32 v72, v4
	v_mov_b32_e32 v73, v5

.Lmyf_C4_7:
	s_mov_b64 exec, -1
	s_waitcnt vmcnt(21)
	v_cvt_f16_f32_e32 v158, v147
	v_cvt_f16_f32_e32 v160, v146
	v_cvt_f16_f32_e32 v159, v148
	v_add_u32_e32 v251, 0x48000, v200
	buffer_load_dwordx4 v[146:149], v251, s[12:15], 0 offen sc1
	s_branch .LBB4_2

.LBB5_4:
	v_add_u32_e32 v182, s30, v161
	v_add_u32_e32 v181, -1, v182
	v_or_b32_e32 v2, v181, v164
	v_add_u32_e32 v180, 0x18400, v171
	v_cmp_gt_u32_e64 s[0:1], 64, v2
	s_mov_b64 s[4:5], -1
	s_and_b64 vcc, exec, s[24:25]
	s_cbranch_vccz .LBB5_42
	s_load_dwordx2 s[4:5], s[22:23], 0x20
	s_waitcnt lgkmcnt(0)
	s_load_dwordx2 s[26:27], s[4:5], 0x0
	s_load_dword s31, s[4:5], 0x8
	v_cmp_lt_u32_e64 s[64:65], 0, v182
	v_cmp_gt_u32_e64 s[66:67], 63, v182
	v_cmp_lt_u32_e64 s[68:69], 0, v162
	v_cmp_gt_u32_e64 s[70:71], 60, v162
	buffer_load_dwordx4 v[186:189], v180, s[16:19], 0 offen sc1
	s_and_b64 s[72:73], s[68:69], s[64:65]
	s_and_b64 s[74:75], s[68:69], s[66:67]
	s_and_b64 s[76:77], s[70:71], s[64:65]
	s_and_b64 s[78:79], s[70:71], s[66:67]
	v_add_u32_e32 v224, 0xfffe7c00, v180
	v_add_u32_e32 v225, 0xfffe8000, v180
	s_mov_b64 exec, s[72:73]
	buffer_load_dwordx4 v[110:113], v224, s[16:19], 0 offen
	buffer_load_dwordx4 v[70:73], v224, s[16:19], 0 offen offset:512
	s_mov_b64 exec, -1
	s_mov_b64 exec, s[68:69]
	buffer_load_dwordx4 v[126:129], v225, s[16:19], 0 offen offset:512
	buffer_load_dwordx4 v[98:101], v225, s[16:19], 0 offen offset:1024
	s_mov_b64 exec, -1
	s_mov_b64 exec, s[74:75]
	buffer_load_dwordx4 v[134:137], v225, s[16:19], 0 offen offset:2048
	buffer_load_dwordx4 v[114:117], v225, s[16:19], 0 offen offset:2560
	s_mov_b64 exec, -1
	v_add_u32_e32 v224, 0xfffffc00, v180
	s_mov_b64 exec, s[64:65]
	buffer_load_dwordx4 v[82:85], v224, s[16:19], 0 offen
	buffer_load_dwordx4 v[42:45], v224, s[16:19], 0 offen offset:512
	s_mov_b64 exec, -1
	buffer_load_dwordx4 v[106:109], v180, s[16:19], 0 offen offset:512
	buffer_load_dwordx4 v[62:65], v180, s[16:19], 0 offen offset:1024
	s_mov_b64 exec, s[66:67]
	buffer_load_dwordx4 v[122:125], v180, s[16:19], 0 offen offset:2048
	buffer_load_dwordx4 v[86:89], v180, s[16:19], 0 offen offset:2560
	s_mov_b64 exec, -1
	v_add_u32_e32 v224, 0x17c00, v180
	v_add_u32_e32 v225, 0x18000, v180
	s_mov_b64 exec, s[64:65]
	buffer_load_dwordx4 v[50:53], v224, s[16:19], 0 offen
	buffer_load_dwordx4 v[22:25], v224, s[16:19], 0 offen offset:512
	s_mov_b64 exec, -1
	buffer_load_dwordx4 v[66:69], v225, s[16:19], 0 offen offset:512
	buffer_load_dwordx4 v[30:33], v225, s[16:19], 0 offen offset:1024
	s_mov_b64 exec, s[66:67]
	buffer_load_dwordx4 v[94:97], v225, s[16:19], 0 offen offset:2048
	buffer_load_dwordx4 v[46:49], v225, s[16:19], 0 offen offset:2560
	s_mov_b64 exec, -1
	v_add_u32_e32 v224, 0x18000, v180
	buffer_load_dwordx4 v[154:157], v224, s[16:19], 0 offen sc1
	v_add_u32_e32 v225, 0x30000, v180
	buffer_load_dwordx4 v[150:153], v225, s[16:19], 0 offen sc1
	v_add_u32_e32 v224, 0x48000, v180
	buffer_load_dwordx4 v[146:149], v224, s[16:19], 0 offen sc1
	v_add_u32_e32 v224, 0x2fc00, v180
	v_add_u32_e32 v225, 0x30000, v180
	v_add_u32_e32 v226, 0x47c00, v180
	v_add_u32_e32 v227, 0x48000, v180
	v_add_u32_e32 v228, 0x5fc00, v180
	v_add_u32_e32 v229, 0x60000, v180
	s_cmp_lg_u32 s93, 0
	s_cbranch_scc1 .Lmybg_D1
	s_waitcnt vmcnt(22)
	v_cvt_pk_f16_f32 v172, v230, v231
	v_cvt_pk_f16_f32 v173, v234, v235
	v_cvt_pk_f16_f32 v174, v232, v233
	v_cvt_pk_f16_f32 v175, v236, v237
	v_cvt_pk_f16_f32 v176, v238, v239
	v_cvt_pk_f16_f32 v177, v242, v243
	v_cvt_pk_f16_f32 v178, v240, v241
	v_cvt_pk_f16_f32 v179, v244, v245
	s_mov_b32 s93, 1

.LBB5_42:
	s_and_b64 vcc, exec, s[4:5]
	s_cbranch_vccz .LBB5_3
	s_load_dwordx2 s[0:1], s[22:23], 0x18
	s_waitcnt lgkmcnt(0)
	s_load_dwordx2 s[6:7], s[0:1], 0x0
	s_load_dword s28, s[0:1], 0x8
	v_cmp_lt_u32_e64 s[64:65], 0, v182
	v_cmp_gt_u32_e64 s[66:67], 63, v182
	v_cmp_lt_u32_e64 s[68:69], 0, v162
	v_cmp_gt_u32_e64 s[70:71], 60, v162
	buffer_load_dwordx4 v[184:187], v180, s[16:19], 0 offen sc1
	s_and_b64 s[72:73], s[68:69], s[64:65]
	s_and_b64 s[74:75], s[68:69], s[66:67]
	s_and_b64 s[76:77], s[70:71], s[64:65]
	s_and_b64 s[78:79], s[70:71], s[66:67]
	v_add_u32_e32 v224, 0xfffe7c00, v180
	v_add_u32_e32 v225, 0xfffe8000, v180
	s_mov_b64 exec, s[72:73]
	buffer_load_dwordx4 v[110:113], v224, s[16:19], 0 offen
	buffer_load_dwordx4 v[78:81], v224, s[16:19], 0 offen offset:512
	s_mov_b64 exec, -1
	s_mov_b64 exec, s[68:69]
	buffer_load_dwordx4 v[126:129], v225, s[16:19], 0 offen offset:512
	buffer_load_dwordx4 v[102:105], v225, s[16:19], 0 offen offset:1024
	s_mov_b64 exec, -1
	s_mov_b64 exec, s[74:75]
	buffer_load_dwordx4 v[134:137], v225, s[16:19], 0 offen offset:2048
	buffer_load_dwordx4 v[114:117], v225, s[16:19], 0 offen offset:2560
	s_mov_b64 exec, -1
	v_add_u32_e32 v224, 0xfffffc00, v180
	s_mov_b64 exec, s[64:65]
	buffer_load_dwordx4 v[82:85], v224, s[16:19], 0 offen
	buffer_load_dwordx4 v[42:45], v224, s[16:19], 0 offen offset:512
	s_mov_b64 exec, -1
	buffer_load_dwordx4 v[106:109], v180, s[16:19], 0 offen offset:512
	buffer_load_dwordx4 v[62:65], v180, s[16:19], 0 offen offset:1024
	s_mov_b64 exec, s[66:67]
	buffer_load_dwordx4 v[122:125], v180, s[16:19], 0 offen offset:2048
	buffer_load_dwordx4 v[86:89], v180, s[16:19], 0 offen offset:2560
	s_mov_b64 exec, -1
	v_add_u32_e32 v224, 0x17c00, v180
	v_add_u32_e32 v225, 0x18000, v180
	s_mov_b64 exec, s[64:65]
	buffer_load_dwordx4 v[50:53], v224, s[16:19], 0 offen
	buffer_load_dwordx4 v[22:25], v224, s[16:19], 0 offen offset:512
	s_mov_b64 exec, -1
	buffer_load_dwordx4 v[66:69], v225, s[16:19], 0 offen offset:512
	buffer_load_dwordx4 v[34:37], v225, s[16:19], 0 offen offset:1024
	s_mov_b64 exec, s[66:67]
	buffer_load_dwordx4 v[94:97], v225, s[16:19], 0 offen offset:2048
	buffer_load_dwordx4 v[46:49], v225, s[16:19], 0 offen offset:2560
	s_mov_b64 exec, -1
	v_add_u32_e32 v224, 0x18000, v180
	buffer_load_dwordx4 v[154:157], v224, s[16:19], 0 offen sc1
	v_add_u32_e32 v225, 0x30000, v180
	buffer_load_dwordx4 v[150:153], v225, s[16:19], 0 offen sc1
	v_add_u32_e32 v224, 0x48000, v180
	buffer_load_dwordx4 v[146:149], v224, s[16:19], 0 offen sc1
	v_add_u32_e32 v224, 0x2fc00, v180
	v_add_u32_e32 v225, 0x30000, v180
	v_add_u32_e32 v226, 0x47c00, v180
	v_add_u32_e32 v227, 0x48000, v180
	v_add_u32_e32 v228, 0x5fc00, v180
	v_add_u32_e32 v229, 0x60000, v180
	s_cmp_lg_u32 s93, 0
	s_cbranch_scc1 .Lmybg_D2
	s_waitcnt vmcnt(22)
	v_cvt_pk_f16_f32 v172, v230, v231
	v_cvt_pk_f16_f32 v173, v234, v235
	v_cvt_pk_f16_f32 v174, v232, v233
	v_cvt_pk_f16_f32 v175, v236, v237
	v_cvt_pk_f16_f32 v176, v238, v239
	v_cvt_pk_f16_f32 v177, v242, v243
	v_cvt_pk_f16_f32 v178, v240, v241
	v_cvt_pk_f16_f32 v179, v244, v245
	s_mov_b32 s93, 1

_Z7k_attn2ILi2EEv8AttnArgs:
	v_readfirstlane_b32 s3, v0
	s_lshl_b32 s12, s3, 1
	v_lshlrev_b32_e32 v3, 3, v0
	s_and_b32 s12, s12, 0x80
	v_and_b32_e32 v3, 0x78, v3
	s_load_dwordx4 s[8:11], s[0:1], 0x0
	s_load_dwordx2 s[4:5], s[0:1], 0x10
	s_load_dwordx2 s[6:7], s[0:1], 0x50
	v_or_b32_e32 v180, s12, v3
	s_lshl_b32 s12, s2, 5
	v_lshrrev_b32_e32 v1, 5, v0
	v_bfe_u32 v2, v0, 4, 2
	s_and_b32 s14, s12, 0xe0
	s_lshr_b32 s12, s2, 3
	v_lshrrev_b32_e32 v0, 6, v0
	v_and_b32_e32 v1, 4, v1
	s_add_i32 s14, s14, s12
	s_and_b32 s2, s2, 56
	v_and_b32_e32 v0, 4, v0
	v_and_or_b32 v181, s14, 56, v0
	v_or3_b32 v182, v2, s2, v1
	s_and_b32 s2, s14, 0x3ffffc0
	v_or_b32_e32 v4, s2, v181
	v_lshlrev_b32_e32 v0, 1, v180
	v_mov_b32_e32 v1, 0
	s_waitcnt lgkmcnt(0)
	v_lshl_add_u64 v[2:3], s[6:7], 0, v[0:1]
	v_lshl_or_b32 v0, v4, 6, v182
	v_lshlrev_b64 v[4:5], 9, v[0:1]
	v_lshl_add_u64 v[8:9], v[2:3], 0, v[4:5]
	v_or_b32_e32 v4, 64, v0
	v_mov_b32_e32 v5, v1
	v_lshlrev_b64 v[4:5], 9, v[4:5]
	v_lshlrev_b32_e32 v20, 2, v180
	v_lshl_add_u64 v[10:11], v[2:3], 0, v[4:5]
	global_load_dwordx4 v[240:243], v20, s[10:11] offset:16
	global_load_dwordx4 v[236:239], v20, s[10:11]
	global_load_dwordx4 v[248:251], v20, s[4:5] offset:16
	global_load_dwordx4 v[244:247], v20, s[4:5]
	global_load_dwordx4 v[12:15], v[8:9], off nt
	global_load_dwordx4 v[4:7], v[10:11], off nt
	v_or_b32_e32 v8, 0x80, v0
	v_mov_b32_e32 v9, v1
	v_lshlrev_b64 v[8:9], 9, v[8:9]
	v_or_b32_e32 v0, 0xc0, v0
	v_lshl_add_u64 v[20:21], v[2:3], 0, v[8:9]
	v_lshlrev_b64 v[0:1], 9, v[0:1]
	v_lshl_add_u64 v[34:35], v[2:3], 0, v[0:1]
	global_load_dwordx4 v[8:11], v[20:21], off nt
	global_load_dwordx4 v[0:3], v[34:35], off nt
	s_bitcmp1_b32 s3, 6
	s_cselect_b64 s[4:5], -1, 0
	s_and_b32 s2, s14, 0x3ffc0
	v_or_b32_e32 v20, s2, v181
	v_lshl_or_b32 v20, v20, 6, v182
	v_add_u32_e32 v184, -1, v182
	v_add_u32_e32 v185, -1, v181
	v_mul_u32_u24_e32 v20, 0x300, v20
	v_or_b32_e32 v34, v185, v184
	v_or_b32_e32 v20, v180, v20
	s_mov_b32 s11, 0x20000
	s_mov_b32 s10, 0x1800000
	s_and_b32 s9, s9, 0xffff
	v_lshlrev_b32_e32 v183, 1, v20
	v_cmp_gt_u32_e64 s[2:3], 64, v34
	s_and_b64 vcc, exec, s[4:5]
	s_cbranch_vccz .LBB6_38
	s_load_dwordx2 s[12:13], s[0:1], 0x20
	s_waitcnt lgkmcnt(0)
	s_load_dwordx2 s[4:5], s[12:13], 0x0
	s_load_dword s12, s[12:13], 0x8
	v_cmp_lt_u32_e64 s[64:65], 0, v182
	v_cmp_gt_u32_e64 s[66:67], 63, v182
	v_cmp_lt_u32_e64 s[68:69], 0, v181
	v_cmp_gt_u32_e64 s[70:71], 60, v181
	buffer_load_dwordx4 v[190:193], v183, s[8:11], 0 offen sc1
	s_and_b64 s[72:73], s[68:69], s[64:65]
	s_and_b64 s[74:75], s[68:69], s[66:67]
	s_and_b64 s[76:77], s[70:71], s[64:65]
	s_and_b64 s[78:79], s[70:71], s[66:67]
	v_add_u32_e32 v228, 0xfffe7c00, v183
	v_add_u32_e32 v229, 0xfffe8000, v183
	s_mov_b64 exec, s[72:73]
	buffer_load_dwordx4 v[136:139], v228, s[8:11], 0 offen
	buffer_load_dwordx4 v[96:99], v228, s[8:11], 0 offen offset:512
	s_mov_b64 exec, -1
	s_mov_b64 exec, s[68:69]
	buffer_load_dwordx4 v[152:155], v229, s[8:11], 0 offen offset:512
	buffer_load_dwordx4 v[124:127], v229, s[8:11], 0 offen offset:1024
	s_mov_b64 exec, -1
	s_mov_b64 exec, s[74:75]
	buffer_load_dwordx4 v[160:163], v229, s[8:11], 0 offen offset:2048
	buffer_load_dwordx4 v[140:143], v229, s[8:11], 0 offen offset:2560
	s_mov_b64 exec, -1
	v_add_u32_e32 v228, 0xfffffc00, v183
	s_mov_b64 exec, s[64:65]
	buffer_load_dwordx4 v[112:115], v228, s[8:11], 0 offen
	buffer_load_dwordx4 v[68:71], v228, s[8:11], 0 offen offset:512
	s_mov_b64 exec, -1
	buffer_load_dwordx4 v[132:135], v183, s[8:11], 0 offen offset:512
	buffer_load_dwordx4 v[88:91], v183, s[8:11], 0 offen offset:1024
	s_mov_b64 exec, s[66:67]
	buffer_load_dwordx4 v[148:151], v183, s[8:11], 0 offen offset:2048
	buffer_load_dwordx4 v[108:111], v183, s[8:11], 0 offen offset:2560
	s_mov_b64 exec, -1
	v_add_u32_e32 v228, 0x17c00, v183
	v_add_u32_e32 v229, 0x18000, v183
	s_mov_b64 exec, s[64:65]
	buffer_load_dwordx4 v[76:79], v228, s[8:11], 0 offen
	buffer_load_dwordx4 v[48:51], v228, s[8:11], 0 offen offset:512
	s_mov_b64 exec, -1
	buffer_load_dwordx4 v[92:95], v229, s[8:11], 0 offen offset:512
	buffer_load_dwordx4 v[56:59], v229, s[8:11], 0 offen offset:1024
	s_mov_b64 exec, s[66:67]
	buffer_load_dwordx4 v[116:119], v229, s[8:11], 0 offen offset:2048
	buffer_load_dwordx4 v[72:75], v229, s[8:11], 0 offen offset:2560
	s_mov_b64 exec, -1
	v_add_u32_e32 v228, 0x18000, v183
	buffer_load_dwordx4 v[176:179], v228, s[8:11], 0 offen sc1
	v_add_u32_e32 v229, 0x30000, v183
	buffer_load_dwordx4 v[172:175], v229, s[8:11], 0 offen sc1
	v_add_u32_e32 v228, 0x48000, v183
	buffer_load_dwordx4 v[168:171], v228, s[8:11], 0 offen sc1
	v_add_u32_e32 v228, 0x2fc00, v183
	v_add_u32_e32 v229, 0x30000, v183
	v_add_u32_e32 v230, 0x47c00, v183
	v_add_u32_e32 v231, 0x48000, v183
	v_add_u32_e32 v232, 0x5fc00, v183
	v_add_u32_e32 v233, 0x60000, v183
	s_waitcnt vmcnt(26)
	v_cvt_pk_f16_f32 v22, v240, v241
	v_cvt_pk_f16_f32 v20, v236, v237
	v_cvt_pk_f16_f32 v21, v238, v239
	v_cvt_pk_f16_f32 v16, v244, v245
	v_cvt_pk_f16_f32 v17, v246, v247
	v_cvt_pk_f16_f32 v18, v248, v249
	v_cvt_pk_f16_f32 v23, v242, v243
	v_cvt_pk_f16_f32 v19, v250, v251
	s_not_b64 exec, s[72:73]
	s_cbranch_execz .Lmyf_E1_0
	v_mov_b32_e32 v136, v20
	v_mov_b32_e32 v137, v21
	v_mov_b32_e32 v138, v22
	v_mov_b32_e32 v139, v23
	v_mov_b32_e32 v96, v16
	v_mov_b32_e32 v97, v17
	v_mov_b32_e32 v98, v18
	v_mov_b32_e32 v99, v19

.LBB6_38:
	s_load_dwordx2 s[12:13], s[0:1], 0x60
	s_cbranch_execz .LBB6_76
	s_load_dwordx2 s[2:3], s[0:1], 0x18
	s_waitcnt lgkmcnt(0)
	s_load_dwordx2 s[0:1], s[2:3], 0x0
	s_load_dword s4, s[2:3], 0x8
	v_cmp_lt_u32_e64 s[64:65], 0, v182
	v_cmp_gt_u32_e64 s[66:67], 63, v182
	v_cmp_lt_u32_e64 s[68:69], 0, v181
	v_cmp_gt_u32_e64 s[70:71], 60, v181
	buffer_load_dwordx4 v[168:171], v183, s[8:11], 0 offen sc1
	s_and_b64 s[72:73], s[68:69], s[64:65]
	s_and_b64 s[74:75], s[68:69], s[66:67]
	s_and_b64 s[76:77], s[70:71], s[64:65]
	s_and_b64 s[78:79], s[70:71], s[66:67]
	v_add_u32_e32 v228, 0xfffe7c00, v183
	v_add_u32_e32 v229, 0xfffe8000, v183
	s_mov_b64 exec, s[72:73]
	buffer_load_dwordx4 v[140:143], v228, s[8:11], 0 offen
	buffer_load_dwordx4 v[120:123], v228, s[8:11], 0 offen offset:512
	s_mov_b64 exec, -1
	s_mov_b64 exec, s[68:69]
	buffer_load_dwordx4 v[152:155], v229, s[8:11], 0 offen offset:512
	buffer_load_dwordx4 v[132:135], v229, s[8:11], 0 offen offset:1024
	s_mov_b64 exec, -1
	s_mov_b64 exec, s[74:75]
	buffer_load_dwordx4 v[156:159], v229, s[8:11], 0 offen offset:2048
	buffer_load_dwordx4 v[144:147], v229, s[8:11], 0 offen offset:2560
	s_mov_b64 exec, -1
	v_add_u32_e32 v228, 0xfffffc00, v183
	s_mov_b64 exec, s[64:65]
	buffer_load_dwordx4 v[124:127], v228, s[8:11], 0 offen
	buffer_load_dwordx4 v[104:107], v228, s[8:11], 0 offen offset:512
	s_mov_b64 exec, -1
	buffer_load_dwordx4 v[136:139], v183, s[8:11], 0 offen offset:512
	buffer_load_dwordx4 v[108:111], v183, s[8:11], 0 offen offset:1024
	s_mov_b64 exec, s[66:67]
	buffer_load_dwordx4 v[148:151], v183, s[8:11], 0 offen offset:2048
	buffer_load_dwordx4 v[88:91], v183, s[8:11], 0 offen offset:2560
	s_mov_b64 exec, -1
	v_add_u32_e32 v228, 0x17c00, v183
	v_add_u32_e32 v229, 0x18000, v183
	s_mov_b64 exec, s[64:65]
	buffer_load_dwordx4 v[64:67], v228, s[8:11], 0 offen
	buffer_load_dwordx4 v[40:43], v228, s[8:11], 0 offen offset:512
	s_mov_b64 exec, -1
	buffer_load_dwordx4 v[76:79], v229, s[8:11], 0 offen offset:512
	buffer_load_dwordx4 v[48:51], v229, s[8:11], 0 offen offset:1024
	s_mov_b64 exec, s[66:67]
	buffer_load_dwordx4 v[92:95], v229, s[8:11], 0 offen offset:2048
	buffer_load_dwordx4 v[60:63], v229, s[8:11], 0 offen offset:2560
	s_mov_b64 exec, -1
	v_add_u32_e32 v228, 0x2fc00, v183
	v_add_u32_e32 v229, 0x30000, v183
	s_mov_b64 exec, s[64:65]
	buffer_load_dwordx4 v[36:39], v228, s[8:11], 0 offen
	buffer_load_dwordx4 v[24:27], v228, s[8:11], 0 offen offset:512
	s_mov_b64 exec, -1
	buffer_load_dwordx4 v[52:55], v229, s[8:11], 0 offen offset:512
	buffer_load_dwordx4 v[28:31], v229, s[8:11], 0 offen offset:1024
	s_mov_b64 exec, s[66:67]
	buffer_load_dwordx4 v[68:71], v229, s[8:11], 0 offen offset:2048
	buffer_load_dwordx4 v[32:35], v229, s[8:11], 0 offen offset:2560
	s_mov_b64 exec, -1
	v_add_u32_e32 v228, 0x18000, v183
	buffer_load_dwordx4 v[160:163], v228, s[8:11], 0 offen sc1
	v_add_u32_e32 v228, 0x47c00, v183
	v_add_u32_e32 v229, 0x48000, v183
	v_add_u32_e32 v230, 0x5fc00, v183
	v_add_u32_e32 v231, 0x60000, v183
	s_waitcnt vmcnt(30)
	v_cvt_pk_f16_f32 v22, v240, v241
	v_cvt_pk_f16_f32 v20, v236, v237
	v_cvt_pk_f16_f32 v21, v238, v239
	v_cvt_pk_f16_f32 v16, v244, v245
	v_cvt_pk_f16_f32 v17, v246, v247
	v_cvt_pk_f16_f32 v18, v248, v249
	v_cvt_pk_f16_f32 v23, v242, v243
	v_cvt_pk_f16_f32 v19, v250, v251
	s_not_b64 exec, s[72:73]
	s_cbranch_execz .Lmyf_E2_0
	v_mov_b32_e32 v140, v20
	v_mov_b32_e32 v141, v21
	v_mov_b32_e32 v142, v22
	v_mov_b32_e32 v143, v23
	v_mov_b32_e32 v120, v16
	v_mov_b32_e32 v121, v17
	v_mov_b32_e32 v122, v18
	v_mov_b32_e32 v123, v19
